# code placement: the nine GEMM K-loop heads aligned to 64 bytes, attention loop heads pinned at their previous 64-byte phase
# speedup vs baseline: 1.0014x; 1.0014x over previous
.LBB0_296:
	s_ashr_i32 s15, s14, 31
	s_lshl_b64 s[16:17], s[14:15], 19
	s_add_u32 s16, s31, s16
	s_addc_u32 s17, s35, s17
	s_and_b64 s[18:19], s[38:39], exec
	s_cselect_b32 s15, s17, s21
	s_cselect_b32 s51, s16, s20
	s_ashr_i32 s13, s12, 31
	s_lshl_b64 s[18:19], s[12:13], 19
	s_add_u32 s18, s36, s18
	s_addc_u32 s19, s37, s19
	s_and_b64 s[26:27], s[38:39], exec
	s_cselect_b32 s13, s19, s23
	s_cselect_b32 s52, s18, s22
	s_add_u32 s53, s22, 0x100
	s_addc_u32 s54, s23, 0
	s_mov_b32 s55, -2
	s_add_u32 s22, s20, 0x100
	s_addc_u32 s23, s21, 0
	s_add_i32 s56, 0, 0x10000
	s_cmp_eq_u32 s55, 12
	s_cselect_b32 s41, s15, s23
	s_cselect_b32 s40, s51, s22
	v_add_u32_e32 v2, s56, v205
	s_cselect_b32 s27, s13, s54
	s_cselect_b32 s26, s52, s53
	s_add_i32 s57, 0, 0x14000
	ds_read_b128 v[132:135], v2
	ds_read_b128 v[136:139], v2 offset:1024
	ds_read_b128 v[140:143], v2 offset:2048
	ds_read_b128 v[144:147], v2 offset:3072
	v_add_u32_e32 v2, s57, v205
	ds_read_b128 v[148:151], v2
	ds_read_b128 v[152:155], v2 offset:1024
	ds_read_b128 v[156:159], v2 offset:2048
	ds_read_b128 v[160:163], v2 offset:3072
	v_lshl_add_u64 v[214:215], s[20:21], 0, v[212:213]
	s_add_i32 m0, s44, 0xc000
	ds_read_b128 v[164:167], v207
	ds_read_b128 v[168:171], v207 offset:1024
	ds_read_b128 v[172:175], v207 offset:2048
	ds_read_b128 v[176:179], v207 offset:3072
	ds_read_b128 v[180:183], v207 offset:4096
	ds_read_b128 v[184:187], v207 offset:5120
	ds_read_b128 v[188:191], v207 offset:6144
	ds_read_b128 v[192:195], v207 offset:7168
	global_load_lds_dwordx4 v[214:215], off
	v_lshl_add_u64 v[214:215], s[20:21], 0, v[210:211]
	s_add_i32 m0, s44, 0xe000
	s_nop 0
	global_load_lds_dwordx4 v[214:215], off
	s_waitcnt vmcnt(8)
	s_waitcnt lgkmcnt(0)
	s_barrier
	s_setprio 1
	s_waitcnt lgkmcnt(0)
	v_mfma_f32_16x16x32_bf16 v[128:131], v[132:135], v[164:167], 0
	v_mfma_f32_16x16x32_bf16 v[124:127], v[140:143], v[164:167], 0
	v_mfma_f32_16x16x32_bf16 v[112:115], v[132:135], v[172:175], 0
	v_mfma_f32_16x16x32_bf16 v[108:111], v[140:143], v[172:175], 0
	v_mfma_f32_16x16x32_bf16 v[96:99], v[132:135], v[180:183], 0
	v_mfma_f32_16x16x32_bf16 v[92:95], v[140:143], v[180:183], 0
	v_mfma_f32_16x16x32_bf16 v[80:83], v[132:135], v[188:191], 0
	v_mfma_f32_16x16x32_bf16 v[76:79], v[140:143], v[188:191], 0
	v_mfma_f32_16x16x32_bf16 v[128:131], v[136:139], v[168:171], v[128:131]
	v_mfma_f32_16x16x32_bf16 v[124:127], v[144:147], v[168:171], v[124:127]
	v_mfma_f32_16x16x32_bf16 v[112:115], v[136:139], v[176:179], v[112:115]
	v_mfma_f32_16x16x32_bf16 v[108:111], v[144:147], v[176:179], v[108:111]
	v_mfma_f32_16x16x32_bf16 v[96:99], v[136:139], v[184:187], v[96:99]
	v_mfma_f32_16x16x32_bf16 v[92:95], v[144:147], v[184:187], v[92:95]
	v_mfma_f32_16x16x32_bf16 v[80:83], v[136:139], v[192:195], v[80:83]
	v_mfma_f32_16x16x32_bf16 v[76:79], v[144:147], v[192:195], v[76:79]
	s_setprio 0
	s_setprio 1
	v_mfma_f32_16x16x32_bf16 v[120:123], v[148:151], v[164:167], 0
	v_mfma_f32_16x16x32_bf16 v[116:119], v[156:159], v[164:167], 0
	v_mfma_f32_16x16x32_bf16 v[104:107], v[148:151], v[172:175], 0
	v_mfma_f32_16x16x32_bf16 v[100:103], v[156:159], v[172:175], 0
	v_mfma_f32_16x16x32_bf16 v[88:91], v[148:151], v[180:183], 0
	v_mfma_f32_16x16x32_bf16 v[84:87], v[156:159], v[180:183], 0
	v_mfma_f32_16x16x32_bf16 v[72:75], v[148:151], v[188:191], 0
	v_mfma_f32_16x16x32_bf16 v[68:71], v[156:159], v[188:191], 0
	v_mfma_f32_16x16x32_bf16 v[120:123], v[152:155], v[168:171], v[120:123]
	v_mfma_f32_16x16x32_bf16 v[116:119], v[160:163], v[168:171], v[116:119]
	v_mfma_f32_16x16x32_bf16 v[104:107], v[152:155], v[176:179], v[104:107]
	v_mfma_f32_16x16x32_bf16 v[100:103], v[160:163], v[176:179], v[100:103]
	v_mfma_f32_16x16x32_bf16 v[88:91], v[152:155], v[184:187], v[88:91]
	v_mfma_f32_16x16x32_bf16 v[84:87], v[160:163], v[184:187], v[84:87]
	v_mfma_f32_16x16x32_bf16 v[72:75], v[152:155], v[192:195], v[72:75]
	v_mfma_f32_16x16x32_bf16 v[68:71], v[160:163], v[192:195], v[68:71]
	s_setprio 0
	s_barrier
	s_add_i32 s20, s56, s42
	v_lshl_add_u64 v[214:215], s[26:27], 0, v[198:199]
	s_mov_b32 m0, s20
	ds_read_b128 v[164:167], v207 offset:16384
	ds_read_b128 v[168:171], v207 offset:17408
	ds_read_b128 v[172:175], v207 offset:18432
	ds_read_b128 v[176:179], v207 offset:19456
	ds_read_b128 v[180:183], v207 offset:20480
	ds_read_b128 v[184:187], v207 offset:21504
	ds_read_b128 v[188:191], v207 offset:22528
	ds_read_b128 v[192:195], v207 offset:23552
	global_load_lds_dwordx4 v[214:215], off
	s_add_i32 m0, s20, 0x2000
	s_add_u32 s20, s26, 0x40000
	v_lshl_add_u64 v[216:217], s[26:27], 0, v[0:1]
	s_addc_u32 s21, s27, 0
	s_add_i32 s56, s57, s42
	global_load_lds_dwordx4 v[216:217], off
	v_lshl_add_u64 v[218:219], s[20:21], 0, v[198:199]
	s_mov_b32 m0, s56
	v_lshl_add_u64 v[220:221], s[40:41], 0, v[196:197]
	global_load_lds_dwordx4 v[218:219], off
	v_lshl_add_u64 v[218:219], s[20:21], 0, v[0:1]
	s_add_i32 m0, s56, 0x2000
	s_nop 0
	global_load_lds_dwordx4 v[218:219], off
	v_lshl_add_u64 v[218:219], s[40:41], 0, v[200:201]
	s_mov_b32 m0, s44
	s_nop 0
	global_load_lds_dwordx4 v[218:219], off
	s_mov_b32 m0, s45
	s_nop 0
	global_load_lds_dwordx4 v[220:221], off
	s_waitcnt vmcnt(8)
	s_waitcnt lgkmcnt(0)
	s_barrier
	s_setprio 1
	s_waitcnt lgkmcnt(0)
	v_mfma_f32_16x16x32_bf16 v[64:67], v[132:135], v[164:167], 0
	v_mfma_f32_16x16x32_bf16 v[60:63], v[140:143], v[164:167], 0
	v_mfma_f32_16x16x32_bf16 v[48:51], v[132:135], v[172:175], 0
	v_mfma_f32_16x16x32_bf16 v[44:47], v[140:143], v[172:175], 0
	v_mfma_f32_16x16x32_bf16 v[32:35], v[132:135], v[180:183], 0
	v_mfma_f32_16x16x32_bf16 v[28:31], v[140:143], v[180:183], 0
	v_mfma_f32_16x16x32_bf16 v[16:19], v[132:135], v[188:191], 0
	v_mfma_f32_16x16x32_bf16 v[12:15], v[140:143], v[188:191], 0
	v_mfma_f32_16x16x32_bf16 v[64:67], v[136:139], v[168:171], v[64:67]
	v_mfma_f32_16x16x32_bf16 v[60:63], v[144:147], v[168:171], v[60:63]
	v_mfma_f32_16x16x32_bf16 v[48:51], v[136:139], v[176:179], v[48:51]
	v_mfma_f32_16x16x32_bf16 v[44:47], v[144:147], v[176:179], v[44:47]
	v_mfma_f32_16x16x32_bf16 v[32:35], v[136:139], v[184:187], v[32:35]
	v_mfma_f32_16x16x32_bf16 v[28:31], v[144:147], v[184:187], v[28:31]
	v_mfma_f32_16x16x32_bf16 v[16:19], v[136:139], v[192:195], v[16:19]
	v_mfma_f32_16x16x32_bf16 v[12:15], v[144:147], v[192:195], v[12:15]
	s_setprio 0
	s_setprio 1
	v_mfma_f32_16x16x32_bf16 v[56:59], v[148:151], v[164:167], 0
	v_mfma_f32_16x16x32_bf16 v[52:55], v[156:159], v[164:167], 0
	v_mfma_f32_16x16x32_bf16 v[40:43], v[148:151], v[172:175], 0
	v_mfma_f32_16x16x32_bf16 v[36:39], v[156:159], v[172:175], 0
	v_mfma_f32_16x16x32_bf16 v[24:27], v[148:151], v[180:183], 0
	v_mfma_f32_16x16x32_bf16 v[20:23], v[156:159], v[180:183], 0
	v_mfma_f32_16x16x32_bf16 v[8:11], v[148:151], v[188:191], 0
	v_mfma_f32_16x16x32_bf16 v[4:7], v[156:159], v[188:191], 0
	v_mfma_f32_16x16x32_bf16 v[56:59], v[152:155], v[168:171], v[56:59]
	v_mfma_f32_16x16x32_bf16 v[52:55], v[160:163], v[168:171], v[52:55]
	v_mfma_f32_16x16x32_bf16 v[40:43], v[152:155], v[176:179], v[40:43]
	v_mfma_f32_16x16x32_bf16 v[36:39], v[160:163], v[176:179], v[36:39]
	v_mfma_f32_16x16x32_bf16 v[24:27], v[152:155], v[184:187], v[24:27]
	v_mfma_f32_16x16x32_bf16 v[20:23], v[160:163], v[184:187], v[20:23]
	v_mfma_f32_16x16x32_bf16 v[8:11], v[152:155], v[192:195], v[8:11]
	v_mfma_f32_16x16x32_bf16 v[4:7], v[160:163], v[192:195], v[4:7]
	s_setprio 0
	s_barrier
	s_add_i32 s56, 0, 0x18000
	v_add_u32_e32 v2, s56, v205
	s_add_i32 s57, 0, 0x1c000
	ds_read_b128 v[132:135], v2
	ds_read_b128 v[136:139], v2 offset:1024
	ds_read_b128 v[140:143], v2 offset:2048
	ds_read_b128 v[144:147], v2 offset:3072
	v_add_u32_e32 v2, s57, v205
	ds_read_b128 v[148:151], v2
	ds_read_b128 v[152:155], v2 offset:1024
	ds_read_b128 v[156:159], v2 offset:2048
	ds_read_b128 v[160:163], v2 offset:3072
	s_add_u32 s20, s40, 0x40000
	s_addc_u32 s21, s41, 0
	s_mov_b32 m0, s46
	v_lshl_add_u64 v[222:223], s[20:21], 0, v[200:201]
	ds_read_b128 v[164:167], v207 offset:32768
	ds_read_b128 v[168:171], v207 offset:33792
	ds_read_b128 v[172:175], v207 offset:34816
	ds_read_b128 v[176:179], v207 offset:35840
	ds_read_b128 v[180:183], v207 offset:36864
	ds_read_b128 v[184:187], v207 offset:37888
	ds_read_b128 v[188:191], v207 offset:38912
	ds_read_b128 v[192:195], v207 offset:39936
	global_load_lds_dwordx4 v[222:223], off
	v_lshl_add_u64 v[222:223], s[20:21], 0, v[196:197]
	s_mov_b32 m0, s47
	s_nop 0
	global_load_lds_dwordx4 v[222:223], off
	s_waitcnt vmcnt(8)
	s_waitcnt lgkmcnt(0)
	s_barrier
	s_setprio 1
	s_waitcnt lgkmcnt(0)
	v_mfma_f32_16x16x32_bf16 v[128:131], v[132:135], v[164:167], v[128:131]
	v_mfma_f32_16x16x32_bf16 v[124:127], v[140:143], v[164:167], v[124:127]
	v_mfma_f32_16x16x32_bf16 v[112:115], v[132:135], v[172:175], v[112:115]
	v_mfma_f32_16x16x32_bf16 v[108:111], v[140:143], v[172:175], v[108:111]
	v_mfma_f32_16x16x32_bf16 v[96:99], v[132:135], v[180:183], v[96:99]
	v_mfma_f32_16x16x32_bf16 v[92:95], v[140:143], v[180:183], v[92:95]
	v_mfma_f32_16x16x32_bf16 v[80:83], v[132:135], v[188:191], v[80:83]
	v_mfma_f32_16x16x32_bf16 v[76:79], v[140:143], v[188:191], v[76:79]
	v_mfma_f32_16x16x32_bf16 v[128:131], v[136:139], v[168:171], v[128:131]
	v_mfma_f32_16x16x32_bf16 v[124:127], v[144:147], v[168:171], v[124:127]
	v_mfma_f32_16x16x32_bf16 v[112:115], v[136:139], v[176:179], v[112:115]
	v_mfma_f32_16x16x32_bf16 v[108:111], v[144:147], v[176:179], v[108:111]
	v_mfma_f32_16x16x32_bf16 v[96:99], v[136:139], v[184:187], v[96:99]
	v_mfma_f32_16x16x32_bf16 v[92:95], v[144:147], v[184:187], v[92:95]
	v_mfma_f32_16x16x32_bf16 v[80:83], v[136:139], v[192:195], v[80:83]
	v_mfma_f32_16x16x32_bf16 v[76:79], v[144:147], v[192:195], v[76:79]
	s_setprio 0
	s_setprio 1
	v_mfma_f32_16x16x32_bf16 v[120:123], v[148:151], v[164:167], v[120:123]
	v_mfma_f32_16x16x32_bf16 v[116:119], v[156:159], v[164:167], v[116:119]
	v_mfma_f32_16x16x32_bf16 v[104:107], v[148:151], v[172:175], v[104:107]
	v_mfma_f32_16x16x32_bf16 v[100:103], v[156:159], v[172:175], v[100:103]
	v_mfma_f32_16x16x32_bf16 v[88:91], v[148:151], v[180:183], v[88:91]
	v_mfma_f32_16x16x32_bf16 v[84:87], v[156:159], v[180:183], v[84:87]
	v_mfma_f32_16x16x32_bf16 v[72:75], v[148:151], v[188:191], v[72:75]
	v_mfma_f32_16x16x32_bf16 v[68:71], v[156:159], v[188:191], v[68:71]
	v_mfma_f32_16x16x32_bf16 v[120:123], v[152:155], v[168:171], v[120:123]
	v_mfma_f32_16x16x32_bf16 v[116:119], v[160:163], v[168:171], v[116:119]
	v_mfma_f32_16x16x32_bf16 v[104:107], v[152:155], v[176:179], v[104:107]
	v_mfma_f32_16x16x32_bf16 v[100:103], v[160:163], v[176:179], v[100:103]
	v_mfma_f32_16x16x32_bf16 v[88:91], v[152:155], v[184:187], v[88:91]
	v_mfma_f32_16x16x32_bf16 v[84:87], v[160:163], v[184:187], v[84:87]
	v_mfma_f32_16x16x32_bf16 v[72:75], v[152:155], v[192:195], v[72:75]
	v_mfma_f32_16x16x32_bf16 v[68:71], v[160:163], v[192:195], v[68:71]
	s_setprio 0
	s_barrier
	s_add_i32 s20, s56, s42
	v_lshl_add_u64 v[214:215], v[214:215], 0, s[28:29]
	s_mov_b32 m0, s20
	ds_read_b128 v[164:167], v207 offset:49152
	ds_read_b128 v[168:171], v207 offset:50176
	ds_read_b128 v[172:175], v207 offset:51200
	ds_read_b128 v[176:179], v207 offset:52224
	ds_read_b128 v[180:183], v207 offset:53248
	ds_read_b128 v[184:187], v207 offset:54272
	ds_read_b128 v[188:191], v207 offset:55296
	ds_read_b128 v[192:195], v207 offset:56320
	global_load_lds_dwordx4 v[214:215], off
	s_add_i32 m0, s20, 0x2000
	s_add_u32 s20, s26, 0x40080
	v_lshl_add_u64 v[214:215], v[216:217], 0, s[28:29]
	s_addc_u32 s21, s27, 0
	s_add_i32 s26, s57, s42
	global_load_lds_dwordx4 v[214:215], off
	v_lshl_add_u64 v[214:215], s[20:21], 0, v[198:199]
	s_mov_b32 m0, s26
	s_nop 0
	global_load_lds_dwordx4 v[214:215], off
	v_lshl_add_u64 v[214:215], s[20:21], 0, v[0:1]
	s_add_i32 m0, s26, 0x2000
	s_nop 0
	global_load_lds_dwordx4 v[214:215], off
	v_lshl_add_u64 v[214:215], v[218:219], 0, s[28:29]
	s_mov_b32 m0, s48
	s_nop 0
	global_load_lds_dwordx4 v[214:215], off
	v_lshl_add_u64 v[214:215], v[220:221], 0, s[28:29]
	s_mov_b32 m0, s49
	s_nop 0
	global_load_lds_dwordx4 v[214:215], off
	s_waitcnt vmcnt(8)
	s_waitcnt lgkmcnt(0)
	s_barrier
	s_setprio 1
	s_waitcnt lgkmcnt(0)
	v_mfma_f32_16x16x32_bf16 v[64:67], v[132:135], v[164:167], v[64:67]
	v_mfma_f32_16x16x32_bf16 v[60:63], v[140:143], v[164:167], v[60:63]
	v_mfma_f32_16x16x32_bf16 v[48:51], v[132:135], v[172:175], v[48:51]
	v_mfma_f32_16x16x32_bf16 v[44:47], v[140:143], v[172:175], v[44:47]
	v_mfma_f32_16x16x32_bf16 v[32:35], v[132:135], v[180:183], v[32:35]
	v_mfma_f32_16x16x32_bf16 v[28:31], v[140:143], v[180:183], v[28:31]
	v_mfma_f32_16x16x32_bf16 v[16:19], v[132:135], v[188:191], v[16:19]
	v_mfma_f32_16x16x32_bf16 v[12:15], v[140:143], v[188:191], v[12:15]
	v_mfma_f32_16x16x32_bf16 v[64:67], v[136:139], v[168:171], v[64:67]
	v_mfma_f32_16x16x32_bf16 v[60:63], v[144:147], v[168:171], v[60:63]
	v_mfma_f32_16x16x32_bf16 v[48:51], v[136:139], v[176:179], v[48:51]
	v_mfma_f32_16x16x32_bf16 v[44:47], v[144:147], v[176:179], v[44:47]
	v_mfma_f32_16x16x32_bf16 v[32:35], v[136:139], v[184:187], v[32:35]
	v_mfma_f32_16x16x32_bf16 v[28:31], v[144:147], v[184:187], v[28:31]
	v_mfma_f32_16x16x32_bf16 v[16:19], v[136:139], v[192:195], v[16:19]
	v_mfma_f32_16x16x32_bf16 v[12:15], v[144:147], v[192:195], v[12:15]
	s_setprio 0
	s_setprio 1
	v_mfma_f32_16x16x32_bf16 v[56:59], v[148:151], v[164:167], v[56:59]
	v_mfma_f32_16x16x32_bf16 v[52:55], v[156:159], v[164:167], v[52:55]
	v_mfma_f32_16x16x32_bf16 v[40:43], v[148:151], v[172:175], v[40:43]
	v_mfma_f32_16x16x32_bf16 v[36:39], v[156:159], v[172:175], v[36:39]
	v_mfma_f32_16x16x32_bf16 v[24:27], v[148:151], v[180:183], v[24:27]
	v_mfma_f32_16x16x32_bf16 v[20:23], v[156:159], v[180:183], v[20:23]
	v_mfma_f32_16x16x32_bf16 v[8:11], v[148:151], v[188:191], v[8:11]
	v_mfma_f32_16x16x32_bf16 v[4:7], v[156:159], v[188:191], v[4:7]
	v_mfma_f32_16x16x32_bf16 v[56:59], v[152:155], v[168:171], v[56:59]
	v_mfma_f32_16x16x32_bf16 v[52:55], v[160:163], v[168:171], v[52:55]
	v_mfma_f32_16x16x32_bf16 v[40:43], v[152:155], v[176:179], v[40:43]
	v_mfma_f32_16x16x32_bf16 v[36:39], v[160:163], v[176:179], v[36:39]
	v_mfma_f32_16x16x32_bf16 v[24:27], v[152:155], v[184:187], v[24:27]
	v_mfma_f32_16x16x32_bf16 v[20:23], v[160:163], v[184:187], v[20:23]
	v_mfma_f32_16x16x32_bf16 v[8:11], v[152:155], v[192:195], v[8:11]
	v_mfma_f32_16x16x32_bf16 v[4:7], v[160:163], v[192:195], v[4:7]
	s_setprio 0
	s_barrier
	s_add_i32 s55, s55, 2
	s_add_u32 s53, s53, 0x100
	s_addc_u32 s54, s54, 0
	s_cmp_gt_u32 s55, 13
	s_mov_b64 s[20:21], s[22:23]
	s_cbranch_scc1 .Lmy_gx0
	.p2alignl 6, 3212836864

.LBB0_438:
	s_lshl_b32 s2, s12, 1
	s_and_b32 s2, s2, 14
	s_ashr_i32 s3, s12, 7
	s_add_i32 s2, s2, s3
	s_ashr_i32 s3, s2, 2
	s_lshl_b32 s22, s3, 8
	s_lshl_b32 s21, s3, 12
	s_lshl_b32 s3, s12, 5
	s_lshl_b32 s2, s2, 7
	v_mov_b32_e32 v205, v3
	v_readlane_b32 s8, v254, 27
	s_and_b32 s3, s3, 0xf00
	s_and_b32 s10, s2, 0x180
	v_mbcnt_lo_u32_b32 v0, -1, 0
	v_mbcnt_hi_u32_b32 v0, -1, v0
	s_add_i32 s13, s22, 0x4000
	v_add_u32_e32 v204, s8, v0
	s_or_b32 s11, s21, s3
	s_lshl_b32 s80, s10, 1
	s_add_u32 s2, s52, s80
	v_lshlrev_b32_e32 v0, 4, v204
	v_add_u32_e32 v6, 0x200, v204
	v_add_u32_e32 v12, 0x400, v204
	v_add_u32_e32 v14, 0x600, v204
	s_addc_u32 s3, s53, 0
	v_and_b32_e32 v2, 0xf0, v0
	v_ashrrev_i32_e32 v36, 4, v204
	v_ashrrev_i32_e32 v38, 4, v6
	v_ashrrev_i32_e32 v40, 4, v12
	v_ashrrev_i32_e32 v42, 4, v14
	v_add_u32_e32 v20, 0x800, v204
	v_add_u32_e32 v22, 0xa00, v204
	v_lshl_add_u64 v[0:1], s[2:3], 0, v[2:3]
	v_add_u32_e32 v4, s11, v36
	s_movk_i32 s18, 0x1400
	v_add_u32_e32 v6, s11, v38
	v_add_u32_e32 v12, s11, v40
	v_add_u32_e32 v14, s11, v42
	v_ashrrev_i32_e32 v44, 4, v20
	v_ashrrev_i32_e32 v46, 4, v22
	v_add_u32_e32 v28, 0xc00, v204
	v_add_u32_e32 v32, 0xe00, v204
	v_mad_i64_i32 v[4:5], s[8:9], v4, s18, v[0:1]
	v_mad_i64_i32 v[8:9], s[8:9], v6, s18, v[0:1]
	v_mad_i64_i32 v[12:13], s[8:9], v12, s18, v[0:1]
	v_mad_i64_i32 v[16:17], s[8:9], v14, s18, v[0:1]
	v_add_u32_e32 v20, s11, v44
	v_add_u32_e32 v22, s11, v46
	v_ashrrev_i32_e32 v47, 4, v28
	v_ashrrev_i32_e32 v48, 4, v32
	global_load_dwordx4 v[4:7], v[4:5], off
	s_nop 0
	global_load_dwordx4 v[8:11], v[8:9], off
	s_nop 0
	global_load_dwordx4 v[12:15], v[12:13], off
	s_nop 0
	global_load_dwordx4 v[16:19], v[16:17], off
	v_mad_i64_i32 v[20:21], s[8:9], v20, s18, v[0:1]
	v_mad_i64_i32 v[24:25], s[8:9], v22, s18, v[0:1]
	v_add_u32_e32 v28, s11, v47
	v_add_u32_e32 v32, s11, v48
	global_load_dwordx4 v[20:23], v[20:21], off
	s_nop 0
	global_load_dwordx4 v[24:27], v[24:25], off
	v_mad_i64_i32 v[28:29], s[8:9], v28, s18, v[0:1]
	v_mad_i64_i32 v[0:1], s[8:9], v32, s18, v[0:1]
	global_load_dwordx4 v[28:31], v[28:29], off
	v_add_u32_e32 v206, 0x11800, v205
	global_load_dwordx4 v[32:35], v[0:1], off
	v_add_u32_e32 v0, v206, v2
	v_mad_u64_u32 v[36:37], s[14:15], v36, s30, v[0:1]
	v_mad_u64_u32 v[38:39], s[14:15], v38, s30, v[0:1]
	v_mad_u64_u32 v[40:41], s[14:15], v40, s30, v[0:1]
	v_mad_u64_u32 v[42:43], s[14:15], v42, s30, v[0:1]
	v_mad_u64_u32 v[44:45], s[14:15], v44, s30, v[0:1]
	v_and_b32_e32 v2, 63, v204
	v_ashrrev_i32_e32 v49, 6, v204
	s_mov_b64 s[24:25], 0x400
	v_readfirstlane_b32 s8, v49
	s_mov_b32 s23, 0
	v_mov_b32_e32 v210, 0
	v_mov_b32_e32 v208, 0xf149f2ca
	v_mov_b32_e32 v209, 0xf149f2ca
	v_mov_b32_e32 v207, 0
	s_waitcnt vmcnt(7)
	ds_write_b128 v36, v[4:7]
	s_waitcnt vmcnt(6)
	ds_write_b128 v38, v[8:11]
	s_waitcnt vmcnt(5)
	ds_write_b128 v40, v[12:15]
	s_waitcnt vmcnt(4)
	ds_write_b128 v42, v[16:19]
	s_waitcnt vmcnt(3)
	ds_write_b128 v44, v[20:23]
	v_mad_u64_u32 v[4:5], s[14:15], v46, s30, v[0:1]
	s_waitcnt vmcnt(2)
	ds_write_b128 v4, v[24:27]
	v_mad_u64_u32 v[4:5], s[14:15], v47, s30, v[0:1]
	v_mad_u64_u32 v[0:1], s[14:15], v48, s30, v[0:1]
	s_waitcnt vmcnt(1)
	ds_write_b128 v4, v[28:31]
	s_waitcnt vmcnt(0)
	ds_write_b128 v0, v[32:35]
	v_or_b32_e32 v4, s13, v2
	v_mov_b64_e32 v[0:1], s[52:53]
	v_mad_i64_i32 v[0:1], s[14:15], v4, s18, v[0:1]
	s_lshl_b32 s14, s8, 3
	s_add_i32 s15, s21, 0xffffff00
	s_cmp_lt_i32 s8, 32
	s_cselect_b32 s9, s13, s15
	s_add_i32 s9, s9, s14
	s_mul_hi_i32 s18, s9, 0x1400
	s_mulk_i32 s9, 0x1400
	s_add_u32 s9, s52, s9
	v_lshlrev_b32_e32 v4, 3, v49
	s_addc_u32 s19, s53, s18
	v_lshl_add_u64 v[0:1], v[0:1], 0, s[80:81]
	v_ashrrev_i32_e32 v5, 31, v4
	s_add_u32 s18, s9, s80
	v_lshl_add_u64 v[0:1], v[4:5], 1, v[0:1]
	s_addc_u32 s19, s19, 0
	v_lshlrev_b32_e32 v2, 2, v2
	global_load_dwordx4 v[176:179], v[0:1], off offset:2048
	global_load_dwordx4 v[180:183], v[0:1], off offset:2176
	v_lshl_add_u64 v[0:1], s[18:19], 0, v[2:3]
	s_mul_i32 s19, s8, 0x880
	v_add_u32_e32 v4, s19, v205
	s_or_b32 s20, s14, 1
	v_readfirstlane_b32 s9, v4
	s_cmpk_lt_i32 s20, 0x100
	s_mov_b32 m0, s9
	s_cselect_b32 s9, s13, s15
	s_add_i32 s9, s9, s20
	s_mul_hi_i32 s18, s9, 0x1400
	s_mulk_i32 s9, 0x1400
	s_add_u32 s9, s52, s9
	s_mulk_i32 s20, 0x110
	s_addc_u32 s18, s53, s18
	v_add_u32_e32 v4, s20, v205
	v_lshl_add_u64 v[0:1], v[0:1], 0, s[24:25]
	s_add_u32 s26, s9, s80
	v_readfirstlane_b32 s9, v4
	global_load_lds_dword v[0:1], off
	s_addc_u32 s27, s18, 0
	s_mov_b32 m0, s9
	s_or_b32 s9, s14, 2
	s_cmpk_lt_i32 s9, 0x100
	s_cselect_b32 s18, s13, s15
	s_add_i32 s9, s18, s9
	s_mul_hi_i32 s18, s9, 0x1400
	s_mulk_i32 s9, 0x1400
	s_add_u32 s9, s52, s9
	s_addc_u32 s18, s53, s18
	v_lshl_add_u64 v[0:1], s[26:27], 0, v[2:3]
	s_add_u32 s26, s9, s80
	s_addc_u32 s27, s18, 0
	s_add_i32 s9, s20, 0x110
	v_add_u32_e32 v4, s9, v205
	v_lshl_add_u64 v[0:1], v[0:1], 0, s[24:25]
	v_readfirstlane_b32 s9, v4
	global_load_lds_dword v[0:1], off
	s_mov_b32 m0, s9
	s_or_b32 s9, s14, 3
	s_cmpk_lt_i32 s9, 0x100
	s_cselect_b32 s18, s13, s15
	s_add_i32 s9, s18, s9
	s_mul_hi_i32 s18, s9, 0x1400
	s_mulk_i32 s9, 0x1400
	s_add_u32 s9, s52, s9
	s_addc_u32 s18, s53, s18
	v_lshl_add_u64 v[0:1], s[26:27], 0, v[2:3]
	s_add_u32 s26, s9, s80
	s_addc_u32 s27, s18, 0
	s_add_i32 s9, s20, 0x220
	v_add_u32_e32 v4, s9, v205
	v_lshl_add_u64 v[0:1], v[0:1], 0, s[24:25]
	v_readfirstlane_b32 s9, v4
	global_load_lds_dword v[0:1], off
	s_mov_b32 m0, s9
	s_or_b32 s9, s14, 4
	s_cmpk_lt_i32 s9, 0x100
	s_cselect_b32 s18, s13, s15
	s_add_i32 s9, s18, s9
	s_mul_hi_i32 s18, s9, 0x1400
	s_mulk_i32 s9, 0x1400
	s_add_u32 s9, s52, s9
	s_addc_u32 s18, s53, s18
	v_lshl_add_u64 v[0:1], s[26:27], 0, v[2:3]
	s_add_u32 s26, s9, s80
	s_addc_u32 s27, s18, 0
	s_add_i32 s9, s20, 0x330
	v_add_u32_e32 v4, s9, v205
	v_lshl_add_u64 v[0:1], v[0:1], 0, s[24:25]
	v_readfirstlane_b32 s9, v4
	global_load_lds_dword v[0:1], off
	s_mov_b32 m0, s9
	s_or_b32 s9, s14, 5
	s_cmpk_lt_i32 s9, 0x100
	s_cselect_b32 s18, s13, s15
	s_add_i32 s9, s18, s9
	s_mul_hi_i32 s18, s9, 0x1400
	s_mulk_i32 s9, 0x1400
	s_add_u32 s9, s52, s9
	s_addc_u32 s18, s53, s18
	v_lshl_add_u64 v[0:1], s[26:27], 0, v[2:3]
	s_add_u32 s26, s9, s80
	s_addc_u32 s27, s18, 0
	s_add_i32 s9, s20, 0x440
	v_add_u32_e32 v4, s9, v205
	v_lshl_add_u64 v[0:1], v[0:1], 0, s[24:25]
	v_readfirstlane_b32 s9, v4
	global_load_lds_dword v[0:1], off
	s_mov_b32 m0, s9
	s_or_b32 s9, s14, 6
	s_cmpk_lt_i32 s9, 0x100
	s_cselect_b32 s18, s13, s15
	s_add_i32 s9, s18, s9
	s_mul_hi_i32 s18, s9, 0x1400
	s_mulk_i32 s9, 0x1400
	s_add_u32 s9, s52, s9
	s_addc_u32 s18, s53, s18
	v_lshl_add_u64 v[0:1], s[26:27], 0, v[2:3]
	s_add_u32 s26, s9, s80
	s_addc_u32 s27, s18, 0
	s_add_i32 s9, s20, 0x550
	v_add_u32_e32 v4, s9, v205
	v_lshl_add_u64 v[0:1], v[0:1], 0, s[24:25]
	v_readfirstlane_b32 s9, v4
	global_load_lds_dword v[0:1], off
	s_mov_b32 m0, s9
	s_or_b32 s9, s14, 7
	s_cmpk_lt_i32 s9, 0x100
	s_cselect_b32 s18, s13, s15
	s_add_i32 s9, s18, s9
	s_mul_hi_i32 s18, s9, 0x1400
	s_mulk_i32 s9, 0x1400
	s_add_u32 s9, s52, s9
	s_addc_u32 s18, s53, s18
	v_lshl_add_u64 v[0:1], s[26:27], 0, v[2:3]
	s_add_u32 s26, s9, s80
	v_lshl_add_u64 v[0:1], v[0:1], 0, s[24:25]
	s_addc_u32 s27, s18, 0
	s_add_i32 s9, s20, 0x660
	global_load_lds_dword v[0:1], off
	v_lshl_add_u64 v[0:1], s[26:27], 0, v[2:3]
	v_add_u32_e32 v2, s9, v205
	v_lshl_add_u64 v[0:1], v[0:1], 0, s[24:25]
	v_readfirstlane_b32 s9, v2
	s_mov_b32 m0, s9
	s_movk_i32 s9, 0x480
	global_load_lds_dword v[0:1], off
	v_bfe_u32 v0, v204, 2, 2
	v_and_b32_e32 v1, 12, v204
	v_cmp_ne_u32_e32 vcc, 2, v0
	v_mov_b32_e32 v14, v3
	v_mov_b32_e32 v15, v3
	v_cndmask_b32_e32 v1, 4, v1, vcc
	v_cmp_ne_u32_e32 vcc, 1, v0
	v_mov_b32_e32 v2, v3
	v_mov_b32_e32 v4, v3
	v_cndmask_b32_e32 v0, 8, v1, vcc
	v_and_or_b32 v0, v204, 51, v0
	v_mul_lo_u32 v1, v49, s9
	v_lshlrev_b32_e32 v0, 1, v0
	v_add3_u32 v0, v205, v1, v0
	s_waitcnt vmcnt(0)
	ds_write_b16 v0, v176 offset:34816
	ds_write_b16_d16_hi v0, v176 offset:34960
	ds_write_b16 v0, v177 offset:35104
	ds_write_b16_d16_hi v0, v177 offset:35248
	ds_write_b16 v0, v178 offset:35392
	ds_write_b16_d16_hi v0, v178 offset:35536
	ds_write_b16 v0, v179 offset:35680
	ds_write_b16_d16_hi v0, v179 offset:35824
	ds_write_b16 v0, v180 offset:44032
	ds_write_b16_d16_hi v0, v180 offset:44176
	ds_write_b16 v0, v181 offset:44320
	ds_write_b16_d16_hi v0, v181 offset:44464
	ds_write_b16 v0, v182 offset:44608
	ds_write_b16_d16_hi v0, v182 offset:44752
	ds_write_b16 v0, v183 offset:44896
	ds_write_b16_d16_hi v0, v183 offset:45040
	v_mov_b32_e32 v0, v3
	v_mov_b32_e32 v1, v3
	v_mov_b32_e32 v5, v3
	v_mov_b32_e32 v6, v3
	v_mov_b32_e32 v7, v3
	v_mov_b32_e32 v8, v3
	v_mov_b32_e32 v9, v3
	v_mov_b32_e32 v10, v3
	v_mov_b32_e32 v11, v3
	v_mov_b32_e32 v12, v3
	v_mov_b32_e32 v13, v3
	v_mov_b64_e32 v[30:31], v[14:15]
	v_mov_b64_e32 v[62:63], v[14:15]
	v_mov_b64_e32 v[94:95], v[14:15]
	v_mov_b64_e32 v[126:127], v[14:15]
	v_mov_b64_e32 v[46:47], v[14:15]
	v_mov_b64_e32 v[78:79], v[14:15]
	v_mov_b64_e32 v[110:111], v[14:15]
	v_mov_b64_e32 v[142:143], v[14:15]
	s_lshl_b32 s18, s8, 5
	s_addk_i32 s21, 0xff40
	s_addk_i32 s22, 0x4040
	v_mov_b64_e32 v[28:29], v[12:13]
	v_mov_b64_e32 v[26:27], v[10:11]
	v_mov_b64_e32 v[24:25], v[8:9]
	v_mov_b64_e32 v[22:23], v[6:7]
	v_mov_b64_e32 v[20:21], v[4:5]
	v_mov_b64_e32 v[18:19], v[2:3]
	v_mov_b64_e32 v[16:17], v[0:1]
	v_mov_b64_e32 v[60:61], v[12:13]
	v_mov_b64_e32 v[58:59], v[10:11]
	v_mov_b64_e32 v[56:57], v[8:9]
	v_mov_b64_e32 v[54:55], v[6:7]
	v_mov_b64_e32 v[52:53], v[4:5]
	v_mov_b64_e32 v[50:51], v[2:3]
	v_mov_b64_e32 v[48:49], v[0:1]
	v_mov_b64_e32 v[92:93], v[12:13]
	v_mov_b64_e32 v[90:91], v[10:11]
	v_mov_b64_e32 v[88:89], v[8:9]
	v_mov_b64_e32 v[86:87], v[6:7]
	v_mov_b64_e32 v[84:85], v[4:5]
	v_mov_b64_e32 v[82:83], v[2:3]
	v_mov_b64_e32 v[80:81], v[0:1]
	v_mov_b64_e32 v[124:125], v[12:13]
	v_mov_b64_e32 v[122:123], v[10:11]
	v_mov_b64_e32 v[120:121], v[8:9]
	v_mov_b64_e32 v[118:119], v[6:7]
	v_mov_b64_e32 v[116:117], v[4:5]
	v_mov_b64_e32 v[114:115], v[2:3]
	v_mov_b64_e32 v[112:113], v[0:1]
	v_mov_b64_e32 v[44:45], v[12:13]
	v_mov_b64_e32 v[42:43], v[10:11]
	v_mov_b64_e32 v[40:41], v[8:9]
	v_mov_b64_e32 v[38:39], v[6:7]
	v_mov_b64_e32 v[36:37], v[4:5]
	v_mov_b64_e32 v[34:35], v[2:3]
	v_mov_b64_e32 v[32:33], v[0:1]
	v_mov_b64_e32 v[76:77], v[12:13]
	v_mov_b64_e32 v[74:75], v[10:11]
	v_mov_b64_e32 v[72:73], v[8:9]
	v_mov_b64_e32 v[70:71], v[6:7]
	v_mov_b64_e32 v[68:69], v[4:5]
	v_mov_b64_e32 v[66:67], v[2:3]
	v_mov_b64_e32 v[64:65], v[0:1]
	v_mov_b64_e32 v[108:109], v[12:13]
	v_mov_b64_e32 v[106:107], v[10:11]
	v_mov_b64_e32 v[104:105], v[8:9]
	v_mov_b64_e32 v[102:103], v[6:7]
	v_mov_b64_e32 v[100:101], v[4:5]
	v_mov_b64_e32 v[98:99], v[2:3]
	v_mov_b64_e32 v[96:97], v[0:1]
	v_mov_b64_e32 v[140:141], v[12:13]
	v_mov_b64_e32 v[138:139], v[10:11]
	v_mov_b64_e32 v[136:137], v[8:9]
	v_mov_b64_e32 v[134:135], v[6:7]
	v_mov_b64_e32 v[132:133], v[4:5]
	v_mov_b64_e32 v[130:131], v[2:3]
	v_mov_b64_e32 v[128:129], v[0:1]
	s_mov_b32 s26, 0
	s_waitcnt lgkmcnt(0)
	s_barrier
	v_and_b32_e32 v2, 31, v204
	v_bfe_u32 v15, v204, 5, 1
	v_lshlrev_b32_e32 v15, 4, v15
	v_or_b32_e32 v13, s18, v2
	v_mul_u32_u24_e32 v1, 0x90, v2
	v_mad_u32_u24 v0, v2, s30, v15
	v_mul_lo_u32 v13, v13, s30
	v_add_u32_e32 v0, v0, v205
	v_add3_u32 v1, v1, v15, v205
	v_add3_u32 v13, v206, v13, v15
	v_bfe_u32 v15, v204, 2, 2
	v_and_b32_e32 v2, 12, v204
	v_cmp_ne_u32_e32 vcc, 2, v15
	s_movk_i32 s8, 0x480
	v_ashrrev_i32_e32 v211, 6, v204
	v_cndmask_b32_e32 v2, 4, v2, vcc
	v_cmp_ne_u32_e32 vcc, 1, v15
	v_mul_lo_u32 v211, v211, s8
	s_nop 0
	v_cndmask_b32_e32 v15, 8, v2, vcc
	v_and_or_b32 v2, v204, 51, v15
	v_lshlrev_b32_e32 v2, 1, v2
	v_add3_u32 v2, v205, v211, v2
	.p2alignl 6, 3212836864
	s_nop 0
	s_nop 0
	s_nop 0
	s_nop 0
	s_nop 0
	s_nop 0
	s_nop 0
	s_nop 0
	s_nop 0
	s_nop 0
	s_nop 0
	s_nop 0

.LBB0_745:
	s_and_b64 vcc, exec, s[0:1]
	s_cbranch_vccz .LBB0_454
	s_ashr_i32 s0, s22, 2
	s_lshl_b32 s15, s0, 8
	s_lshl_b32 s12, s0, 12
	s_lshl_b32 s0, s22, 7
	v_mov_b32_e32 v205, v3
	v_readlane_b32 s1, v254, 27
	s_and_b32 s8, s0, 0x180
	v_mbcnt_lo_u32_b32 v0, -1, 0
	v_mbcnt_hi_u32_b32 v0, -1, v0
	s_add_i32 s9, s15, 0x4000
	v_add_u32_e32 v204, s1, v0
	s_lshl_b32 s80, s8, 1
	s_add_u32 s0, s52, s80
	v_lshlrev_b32_e32 v0, 4, v204
	v_add_u32_e32 v6, 0x200, v204
	v_add_u32_e32 v12, 0x400, v204
	v_add_u32_e32 v14, 0x600, v204
	v_add_u32_e32 v20, 0x800, v204
	v_add_u32_e32 v22, 0xa00, v204
	v_add_u32_e32 v28, 0xc00, v204
	v_add_u32_e32 v32, 0xe00, v204
	s_addc_u32 s1, s53, 0
	v_and_b32_e32 v2, 0xf0, v0
	v_ashrrev_i32_e32 v36, 4, v204
	v_ashrrev_i32_e32 v38, 4, v6
	v_ashrrev_i32_e32 v40, 4, v12
	v_ashrrev_i32_e32 v42, 4, v14
	v_ashrrev_i32_e32 v44, 4, v20
	v_ashrrev_i32_e32 v46, 4, v22
	v_ashrrev_i32_e32 v48, 4, v28
	v_ashrrev_i32_e32 v50, 4, v32
	v_lshl_add_u64 v[0:1], s[0:1], 0, v[2:3]
	v_add_u32_e32 v4, s9, v36
	s_movk_i32 s13, 0x1400
	v_add_u32_e32 v6, s9, v38
	v_add_u32_e32 v12, s9, v40
	v_add_u32_e32 v14, s9, v42
	v_add_u32_e32 v20, s9, v44
	v_add_u32_e32 v22, s9, v46
	v_add_u32_e32 v28, s9, v48
	v_add_u32_e32 v32, s9, v50
	v_mad_i64_i32 v[4:5], s[2:3], v4, s13, v[0:1]
	v_mad_i64_i32 v[8:9], s[2:3], v6, s13, v[0:1]
	v_mad_i64_i32 v[12:13], s[2:3], v12, s13, v[0:1]
	v_mad_i64_i32 v[16:17], s[2:3], v14, s13, v[0:1]
	v_mad_i64_i32 v[20:21], s[2:3], v20, s13, v[0:1]
	v_mad_i64_i32 v[24:25], s[2:3], v22, s13, v[0:1]
	v_mad_i64_i32 v[28:29], s[2:3], v28, s13, v[0:1]
	v_mad_i64_i32 v[0:1], s[2:3], v32, s13, v[0:1]
	global_load_dwordx4 v[4:7], v[4:5], off
	s_nop 0
	global_load_dwordx4 v[8:11], v[8:9], off
	s_nop 0
	global_load_dwordx4 v[12:15], v[12:13], off
	s_nop 0
	global_load_dwordx4 v[16:19], v[16:17], off
	s_nop 0
	global_load_dwordx4 v[20:23], v[20:21], off
	s_nop 0
	global_load_dwordx4 v[24:27], v[24:25], off
	v_add_u32_e32 v206, 0x11800, v205
	global_load_dwordx4 v[28:31], v[28:29], off
	v_ashrrev_i32_e32 v51, 6, v204
	global_load_dwordx4 v[32:35], v[0:1], off
	v_add_u32_e32 v0, v206, v2
	v_mad_u64_u32 v[36:37], s[10:11], v36, s30, v[0:1]
	v_mad_u64_u32 v[38:39], s[10:11], v38, s30, v[0:1]
	v_mad_u64_u32 v[40:41], s[10:11], v40, s30, v[0:1]
	v_mad_u64_u32 v[42:43], s[10:11], v42, s30, v[0:1]
	v_mad_u64_u32 v[44:45], s[10:11], v44, s30, v[0:1]
	v_mad_u64_u32 v[46:47], s[10:11], v46, s30, v[0:1]
	v_mad_u64_u32 v[48:49], s[10:11], v48, s30, v[0:1]
	v_mad_u64_u32 v[0:1], s[10:11], v50, s30, v[0:1]
	v_and_b32_e32 v2, 63, v204
	v_readfirstlane_b32 s2, v51
	s_mov_b64 s[24:25], 0x400
	v_mov_b32_e32 v226, 0x3ecc95a3
	v_mov_b32_e32 v210, 0
	v_mov_b32_e32 v208, 0xf149f2ca
	s_waitcnt vmcnt(7)
	ds_write_b128 v36, v[4:7]
	s_waitcnt vmcnt(6)
	ds_write_b128 v38, v[8:11]
	s_waitcnt vmcnt(5)
	ds_write_b128 v40, v[12:15]
	s_waitcnt vmcnt(4)
	ds_write_b128 v42, v[16:19]
	s_waitcnt vmcnt(3)
	ds_write_b128 v44, v[20:23]
	s_waitcnt vmcnt(2)
	ds_write_b128 v46, v[24:27]
	s_waitcnt vmcnt(1)
	ds_write_b128 v48, v[28:31]
	v_or_b32_e32 v4, s9, v2
	v_lshlrev_b32_e32 v2, 2, v2
	v_mov_b32_e32 v14, v3
	s_waitcnt vmcnt(0)
	ds_write_b128 v0, v[32:35]
	v_mov_b64_e32 v[0:1], s[52:53]
	v_mad_i64_i32 v[0:1], s[10:11], v4, s13, v[0:1]
	s_lshl_b32 s10, s2, 3
	s_add_i32 s11, s12, 0xffffff00
	s_cmp_lt_i32 s2, 32
	s_cselect_b32 s3, s9, s11
	s_add_i32 s3, s3, s10
	s_mul_hi_i32 s12, s3, 0x1400
	s_mulk_i32 s3, 0x1400
	s_add_u32 s3, s52, s3
	v_lshlrev_b32_e32 v4, 3, v51
	s_addc_u32 s13, s53, s12
	v_lshl_add_u64 v[0:1], v[0:1], 0, s[80:81]
	v_ashrrev_i32_e32 v5, 31, v4
	s_add_u32 s12, s3, s80
	v_lshl_add_u64 v[0:1], v[4:5], 1, v[0:1]
	s_addc_u32 s13, s13, 0
	global_load_dwordx4 v[176:179], v[0:1], off offset:2048
	global_load_dwordx4 v[180:183], v[0:1], off offset:2176
	v_lshl_add_u64 v[0:1], s[12:13], 0, v[2:3]
	s_mul_i32 s13, s2, 0x880
	v_add_u32_e32 v4, s13, v205
	s_or_b32 s14, s10, 1
	v_readfirstlane_b32 s3, v4
	s_cmpk_lt_i32 s14, 0x100
	s_mov_b32 m0, s3
	s_cselect_b32 s3, s9, s11
	s_add_i32 s3, s3, s14
	s_mul_hi_i32 s12, s3, 0x1400
	s_mulk_i32 s3, 0x1400
	s_add_u32 s3, s52, s3
	s_mulk_i32 s14, 0x110
	s_addc_u32 s12, s53, s12
	v_add_u32_e32 v4, s14, v205
	v_lshl_add_u64 v[0:1], v[0:1], 0, s[24:25]
	s_add_u32 s22, s3, s80
	v_readfirstlane_b32 s3, v4
	global_load_lds_dword v[0:1], off
	s_addc_u32 s23, s12, 0
	s_mov_b32 m0, s3
	s_or_b32 s3, s10, 2
	s_cmpk_lt_i32 s3, 0x100
	s_cselect_b32 s12, s9, s11
	s_add_i32 s3, s12, s3
	s_mul_hi_i32 s12, s3, 0x1400
	s_mulk_i32 s3, 0x1400
	s_add_u32 s3, s52, s3
	s_addc_u32 s12, s53, s12
	v_lshl_add_u64 v[0:1], s[22:23], 0, v[2:3]
	s_add_u32 s22, s3, s80
	s_addc_u32 s23, s12, 0
	s_add_i32 s3, s14, 0x110
	v_add_u32_e32 v4, s3, v205
	v_lshl_add_u64 v[0:1], v[0:1], 0, s[24:25]
	v_readfirstlane_b32 s3, v4
	global_load_lds_dword v[0:1], off
	s_mov_b32 m0, s3
	s_or_b32 s3, s10, 3
	s_cmpk_lt_i32 s3, 0x100
	s_cselect_b32 s12, s9, s11
	s_add_i32 s3, s12, s3
	s_mul_hi_i32 s12, s3, 0x1400
	s_mulk_i32 s3, 0x1400
	s_add_u32 s3, s52, s3
	s_addc_u32 s12, s53, s12
	v_lshl_add_u64 v[0:1], s[22:23], 0, v[2:3]
	s_add_u32 s22, s3, s80
	s_addc_u32 s23, s12, 0
	s_add_i32 s3, s14, 0x220
	v_add_u32_e32 v4, s3, v205
	v_lshl_add_u64 v[0:1], v[0:1], 0, s[24:25]
	v_readfirstlane_b32 s3, v4
	global_load_lds_dword v[0:1], off
	s_mov_b32 m0, s3
	s_or_b32 s3, s10, 4
	s_cmpk_lt_i32 s3, 0x100
	s_cselect_b32 s12, s9, s11
	s_add_i32 s3, s12, s3
	s_mul_hi_i32 s12, s3, 0x1400
	s_mulk_i32 s3, 0x1400
	s_add_u32 s3, s52, s3
	s_addc_u32 s12, s53, s12
	v_lshl_add_u64 v[0:1], s[22:23], 0, v[2:3]
	s_add_u32 s22, s3, s80
	s_addc_u32 s23, s12, 0
	s_add_i32 s3, s14, 0x330
	v_add_u32_e32 v4, s3, v205
	v_lshl_add_u64 v[0:1], v[0:1], 0, s[24:25]
	v_readfirstlane_b32 s3, v4
	global_load_lds_dword v[0:1], off
	s_mov_b32 m0, s3
	s_or_b32 s3, s10, 5
	s_cmpk_lt_i32 s3, 0x100
	s_cselect_b32 s12, s9, s11
	s_add_i32 s3, s12, s3
	s_mul_hi_i32 s12, s3, 0x1400
	s_mulk_i32 s3, 0x1400
	s_add_u32 s3, s52, s3
	s_addc_u32 s12, s53, s12
	v_lshl_add_u64 v[0:1], s[22:23], 0, v[2:3]
	s_add_u32 s22, s3, s80
	s_addc_u32 s23, s12, 0
	s_add_i32 s3, s14, 0x440
	v_add_u32_e32 v4, s3, v205
	v_lshl_add_u64 v[0:1], v[0:1], 0, s[24:25]
	v_readfirstlane_b32 s3, v4
	global_load_lds_dword v[0:1], off
	s_mov_b32 m0, s3
	s_or_b32 s3, s10, 6
	s_cmpk_lt_i32 s3, 0x100
	s_cselect_b32 s12, s9, s11
	s_add_i32 s3, s12, s3
	s_mul_hi_i32 s12, s3, 0x1400
	s_mulk_i32 s3, 0x1400
	s_add_u32 s3, s52, s3
	s_addc_u32 s12, s53, s12
	v_lshl_add_u64 v[0:1], s[22:23], 0, v[2:3]
	s_add_u32 s22, s3, s80
	s_addc_u32 s23, s12, 0
	s_add_i32 s3, s14, 0x550
	v_add_u32_e32 v4, s3, v205
	v_lshl_add_u64 v[0:1], v[0:1], 0, s[24:25]
	v_readfirstlane_b32 s3, v4
	global_load_lds_dword v[0:1], off
	s_mov_b32 m0, s3
	s_or_b32 s3, s10, 7
	s_cmpk_lt_i32 s3, 0x100
	s_cselect_b32 s12, s9, s11
	s_add_i32 s3, s12, s3
	s_mul_hi_i32 s12, s3, 0x1400
	s_mulk_i32 s3, 0x1400
	s_add_u32 s3, s52, s3
	s_addc_u32 s12, s53, s12
	v_lshl_add_u64 v[0:1], s[22:23], 0, v[2:3]
	s_add_u32 s22, s3, s80
	v_lshl_add_u64 v[0:1], v[0:1], 0, s[24:25]
	s_addc_u32 s23, s12, 0
	s_add_i32 s3, s14, 0x660
	global_load_lds_dword v[0:1], off
	v_lshl_add_u64 v[0:1], s[22:23], 0, v[2:3]
	v_add_u32_e32 v2, s3, v205
	v_lshl_add_u64 v[0:1], v[0:1], 0, s[24:25]
	v_readfirstlane_b32 s3, v2
	s_mov_b32 m0, s3
	s_movk_i32 s3, 0x480
	global_load_lds_dword v[0:1], off
	v_bfe_u32 v0, v204, 2, 2
	v_and_b32_e32 v1, 12, v204
	v_cmp_ne_u32_e32 vcc, 2, v0
	v_mov_b32_e32 v15, v3
	v_mov_b32_e32 v2, v3
	v_cndmask_b32_e32 v1, 4, v1, vcc
	v_cmp_ne_u32_e32 vcc, 1, v0
	v_mov_b32_e32 v4, v3
	v_mov_b32_e32 v5, v3
	v_cndmask_b32_e32 v0, 8, v1, vcc
	v_and_or_b32 v0, v204, 51, v0
	v_mul_lo_u32 v1, v51, s3
	v_lshlrev_b32_e32 v0, 1, v0
	v_add3_u32 v0, v205, v1, v0
	s_waitcnt vmcnt(0)
	ds_write_b16 v0, v176 offset:34816
	ds_write_b16_d16_hi v0, v176 offset:34960
	ds_write_b16 v0, v177 offset:35104
	ds_write_b16_d16_hi v0, v177 offset:35248
	ds_write_b16 v0, v178 offset:35392
	ds_write_b16_d16_hi v0, v178 offset:35536
	ds_write_b16 v0, v179 offset:35680
	ds_write_b16_d16_hi v0, v179 offset:35824
	ds_write_b16 v0, v180 offset:44032
	ds_write_b16_d16_hi v0, v180 offset:44176
	ds_write_b16 v0, v181 offset:44320
	ds_write_b16_d16_hi v0, v181 offset:44464
	ds_write_b16 v0, v182 offset:44608
	ds_write_b16_d16_hi v0, v182 offset:44752
	ds_write_b16 v0, v183 offset:44896
	ds_write_b16_d16_hi v0, v183 offset:45040
	v_mov_b32_e32 v0, v3
	v_mov_b32_e32 v1, v3
	v_mov_b32_e32 v6, v3
	v_mov_b32_e32 v7, v3
	v_mov_b32_e32 v8, v3
	v_mov_b32_e32 v9, v3
	v_mov_b32_e32 v10, v3
	v_mov_b32_e32 v11, v3
	v_mov_b32_e32 v12, v3
	v_mov_b32_e32 v13, v3
	v_mov_b64_e32 v[30:31], v[14:15]
	v_mov_b64_e32 v[62:63], v[14:15]
	v_mov_b64_e32 v[94:95], v[14:15]
	v_mov_b64_e32 v[126:127], v[14:15]
	v_mov_b64_e32 v[46:47], v[14:15]
	v_mov_b64_e32 v[78:79], v[14:15]
	v_mov_b64_e32 v[110:111], v[14:15]
	v_mov_b64_e32 v[142:143], v[14:15]
	s_lshl_b32 s12, s2, 5
	s_addk_i32 s15, 0x4040
	s_mov_b32 s22, 0
	v_mov_b64_e32 v[28:29], v[12:13]
	v_mov_b64_e32 v[26:27], v[10:11]
	v_mov_b64_e32 v[24:25], v[8:9]
	v_mov_b64_e32 v[22:23], v[6:7]
	v_mov_b64_e32 v[20:21], v[4:5]
	v_mov_b64_e32 v[18:19], v[2:3]
	v_mov_b64_e32 v[16:17], v[0:1]
	v_mov_b64_e32 v[60:61], v[12:13]
	v_mov_b64_e32 v[58:59], v[10:11]
	v_mov_b64_e32 v[56:57], v[8:9]
	v_mov_b64_e32 v[54:55], v[6:7]
	v_mov_b64_e32 v[52:53], v[4:5]
	v_mov_b64_e32 v[50:51], v[2:3]
	v_mov_b64_e32 v[48:49], v[0:1]
	v_mov_b64_e32 v[92:93], v[12:13]
	v_mov_b64_e32 v[90:91], v[10:11]
	v_mov_b64_e32 v[88:89], v[8:9]
	v_mov_b64_e32 v[86:87], v[6:7]
	v_mov_b64_e32 v[84:85], v[4:5]
	v_mov_b64_e32 v[82:83], v[2:3]
	v_mov_b64_e32 v[80:81], v[0:1]
	v_mov_b64_e32 v[124:125], v[12:13]
	v_mov_b64_e32 v[122:123], v[10:11]
	v_mov_b64_e32 v[120:121], v[8:9]
	v_mov_b64_e32 v[118:119], v[6:7]
	v_mov_b64_e32 v[116:117], v[4:5]
	v_mov_b64_e32 v[114:115], v[2:3]
	v_mov_b64_e32 v[112:113], v[0:1]
	v_mov_b64_e32 v[44:45], v[12:13]
	v_mov_b64_e32 v[42:43], v[10:11]
	v_mov_b64_e32 v[40:41], v[8:9]
	v_mov_b64_e32 v[38:39], v[6:7]
	v_mov_b64_e32 v[36:37], v[4:5]
	v_mov_b64_e32 v[34:35], v[2:3]
	v_mov_b64_e32 v[32:33], v[0:1]
	v_mov_b64_e32 v[76:77], v[12:13]
	v_mov_b64_e32 v[74:75], v[10:11]
	v_mov_b64_e32 v[72:73], v[8:9]
	v_mov_b64_e32 v[70:71], v[6:7]
	v_mov_b64_e32 v[68:69], v[4:5]
	v_mov_b64_e32 v[66:67], v[2:3]
	v_mov_b64_e32 v[64:65], v[0:1]
	v_mov_b64_e32 v[108:109], v[12:13]
	v_mov_b64_e32 v[106:107], v[10:11]
	v_mov_b64_e32 v[104:105], v[8:9]
	v_mov_b64_e32 v[102:103], v[6:7]
	v_mov_b64_e32 v[100:101], v[4:5]
	v_mov_b64_e32 v[98:99], v[2:3]
	v_mov_b64_e32 v[96:97], v[0:1]
	v_mov_b64_e32 v[140:141], v[12:13]
	v_mov_b64_e32 v[138:139], v[10:11]
	v_mov_b64_e32 v[136:137], v[8:9]
	v_mov_b64_e32 v[134:135], v[6:7]
	v_mov_b64_e32 v[132:133], v[4:5]
	v_mov_b64_e32 v[130:131], v[2:3]
	v_mov_b64_e32 v[128:129], v[0:1]
	v_mov_b32_e32 v209, 0xf149f2ca
	v_mov_b32_e32 v207, 0
	s_mov_b32 s25, 0
	s_waitcnt lgkmcnt(0)
	s_barrier
	v_and_b32_e32 v2, 31, v204
	v_bfe_u32 v15, v204, 5, 1
	v_lshlrev_b32_e32 v15, 4, v15
	v_or_b32_e32 v13, s12, v2
	v_mul_u32_u24_e32 v1, 0x90, v2
	v_mad_u32_u24 v0, v2, s30, v15
	v_mul_lo_u32 v13, v13, s30
	v_add_u32_e32 v0, v0, v205
	v_add3_u32 v1, v1, v15, v205
	v_add3_u32 v13, v206, v13, v15
	v_bfe_u32 v15, v204, 2, 2
	v_and_b32_e32 v2, 12, v204
	v_cmp_ne_u32_e32 vcc, 2, v15
	s_movk_i32 s24, 0x480
	v_ashrrev_i32_e32 v211, 6, v204
	v_cndmask_b32_e32 v2, 4, v2, vcc
	v_cmp_ne_u32_e32 vcc, 1, v15
	v_mul_lo_u32 v211, v211, s24
	s_nop 0
	v_cndmask_b32_e32 v15, 8, v2, vcc
	v_and_or_b32 v2, v204, 51, v15
	v_lshlrev_b32_e32 v2, 1, v2
	v_add3_u32 v2, v205, v211, v2
	.p2alignl 6, 3212836864
	s_nop 0
	s_nop 0
	s_nop 0
	s_nop 0
	s_nop 0
	s_nop 0
	s_nop 0
	s_nop 0
	s_nop 0
	s_nop 0

.LBB0_825:
	s_ashr_i32 s15, s14, 31
	s_lshl_b64 s[18:19], s[14:15], 19
	s_add_u32 s13, s35, s18
	s_addc_u32 s15, s36, s19
	s_and_b64 s[18:19], s[38:39], exec
	s_cselect_b32 s19, s15, s23
	s_cselect_b32 s18, s13, s22
	s_ashr_i32 s13, s12, 31
	s_lshl_b64 s[20:21], s[12:13], 19
	s_add_u32 s13, s37, s20
	s_addc_u32 s15, s44, s21
	s_and_b64 s[20:21], s[38:39], exec
	s_cselect_b32 s21, s15, s27
	s_cselect_b32 s20, s13, s26
	s_add_u32 s13, s26, 0x100
	v_mov_b32_e32 v218, 0x3ecc95a3
	s_addc_u32 s15, s27, 0
	s_mov_b32 s58, -2
	s_add_u32 s26, s22, 0x100
	s_addc_u32 s27, s23, 0
	s_add_i32 s59, 0, 0x10000
	s_cmp_eq_u32 s58, 12
	s_cselect_b32 s43, s19, s27
	s_cselect_b32 s42, s18, s26
	s_cselect_b32 s41, s21, s15
	s_cselect_b32 s40, s20, s13
	s_add_i32 s60, 0, 0x14000
	v_add_u32_e32 v128, s59, v179
	v_add_u32_e32 v160, s60, v179
	ds_read_b128 v[116:119], v128
	ds_read_b128 v[120:123], v128 offset:1024
	ds_read_b128 v[124:127], v128 offset:2048
	ds_read_b128 v[128:131], v128 offset:3072
	ds_read_b128 v[148:151], v160
	ds_read_b128 v[152:155], v160 offset:1024
	ds_read_b128 v[156:159], v160 offset:2048
	ds_read_b128 v[160:163], v160 offset:3072
	v_lshl_add_u64 v[176:177], s[22:23], 0, v[170:171]
	s_add_i32 m0, s46, 0xc000
	ds_read_b128 v[172:175], v181
	ds_read_b128 v[182:185], v181 offset:1024
	ds_read_b128 v[186:189], v181 offset:2048
	ds_read_b128 v[190:193], v181 offset:3072
	ds_read_b128 v[194:197], v181 offset:4096
	ds_read_b128 v[198:201], v181 offset:5120
	ds_read_b128 v[202:205], v181 offset:6144
	ds_read_b128 v[206:209], v181 offset:7168
	global_load_lds_dwordx4 v[176:177], off
	v_lshl_add_u64 v[176:177], s[22:23], 0, v[168:169]
	s_add_i32 m0, s46, 0xe000
	s_nop 0
	global_load_lds_dwordx4 v[176:177], off
	s_waitcnt vmcnt(8)
	s_waitcnt lgkmcnt(0)
	s_barrier
	s_setprio 1
	s_waitcnt lgkmcnt(0)
	v_mfma_f32_16x16x32_bf16 v[144:147], v[116:119], v[172:175], 0
	v_mfma_f32_16x16x32_bf16 v[140:143], v[124:127], v[172:175], 0
	v_mfma_f32_16x16x32_bf16 v[112:115], v[116:119], v[186:189], 0
	v_mfma_f32_16x16x32_bf16 v[108:111], v[124:127], v[186:189], 0
	v_mfma_f32_16x16x32_bf16 v[100:103], v[116:119], v[194:197], 0
	v_mfma_f32_16x16x32_bf16 v[92:95], v[124:127], v[194:197], 0
	v_mfma_f32_16x16x32_bf16 v[84:87], v[116:119], v[202:205], 0
	v_mfma_f32_16x16x32_bf16 v[76:79], v[124:127], v[202:205], 0
	v_mfma_f32_16x16x32_bf16 v[144:147], v[120:123], v[182:185], v[144:147]
	v_mfma_f32_16x16x32_bf16 v[140:143], v[128:131], v[182:185], v[140:143]
	v_mfma_f32_16x16x32_bf16 v[112:115], v[120:123], v[190:193], v[112:115]
	v_mfma_f32_16x16x32_bf16 v[108:111], v[128:131], v[190:193], v[108:111]
	v_mfma_f32_16x16x32_bf16 v[100:103], v[120:123], v[198:201], v[100:103]
	v_mfma_f32_16x16x32_bf16 v[92:95], v[128:131], v[198:201], v[92:95]
	v_mfma_f32_16x16x32_bf16 v[84:87], v[120:123], v[206:209], v[84:87]
	v_mfma_f32_16x16x32_bf16 v[76:79], v[128:131], v[206:209], v[76:79]
	s_setprio 0
	s_setprio 1
	v_mfma_f32_16x16x32_bf16 v[136:139], v[148:151], v[172:175], 0
	v_mfma_f32_16x16x32_bf16 v[132:135], v[156:159], v[172:175], 0
	v_mfma_f32_16x16x32_bf16 v[104:107], v[148:151], v[186:189], 0
	v_mfma_f32_16x16x32_bf16 v[96:99], v[156:159], v[186:189], 0
	v_mfma_f32_16x16x32_bf16 v[88:91], v[148:151], v[194:197], 0
	v_mfma_f32_16x16x32_bf16 v[80:83], v[156:159], v[194:197], 0
	v_mfma_f32_16x16x32_bf16 v[72:75], v[148:151], v[202:205], 0
	v_mfma_f32_16x16x32_bf16 v[68:71], v[156:159], v[202:205], 0
	v_mfma_f32_16x16x32_bf16 v[136:139], v[152:155], v[182:185], v[136:139]
	v_mfma_f32_16x16x32_bf16 v[132:135], v[160:163], v[182:185], v[132:135]
	v_mfma_f32_16x16x32_bf16 v[104:107], v[152:155], v[190:193], v[104:107]
	v_mfma_f32_16x16x32_bf16 v[96:99], v[160:163], v[190:193], v[96:99]
	v_mfma_f32_16x16x32_bf16 v[88:91], v[152:155], v[198:201], v[88:91]
	v_mfma_f32_16x16x32_bf16 v[80:83], v[160:163], v[198:201], v[80:83]
	v_mfma_f32_16x16x32_bf16 v[72:75], v[152:155], v[206:209], v[72:75]
	v_mfma_f32_16x16x32_bf16 v[68:71], v[160:163], v[206:209], v[68:71]
	s_setprio 0
	s_barrier
	s_add_i32 s22, s59, s45
	v_lshl_add_u64 v[176:177], s[40:41], 0, v[2:3]
	s_mov_b32 m0, s22
	ds_read_b128 v[172:175], v181 offset:16384
	ds_read_b128 v[182:185], v181 offset:17408
	ds_read_b128 v[186:189], v181 offset:18432
	ds_read_b128 v[190:193], v181 offset:19456
	ds_read_b128 v[194:197], v181 offset:20480
	ds_read_b128 v[198:201], v181 offset:21504
	ds_read_b128 v[202:205], v181 offset:22528
	ds_read_b128 v[206:209], v181 offset:23552
	global_load_lds_dwordx4 v[176:177], off
	s_add_i32 m0, s22, 0x2000
	s_add_u32 s22, s40, 0x40000
	v_lshl_add_u64 v[210:211], s[40:41], 0, v[166:167]
	s_addc_u32 s23, s41, 0
	s_add_i32 s59, s60, s45
	global_load_lds_dwordx4 v[210:211], off
	v_lshl_add_u64 v[212:213], s[22:23], 0, v[2:3]
	s_mov_b32 m0, s59
	v_lshl_add_u64 v[214:215], s[42:43], 0, v[164:165]
	global_load_lds_dwordx4 v[212:213], off
	v_lshl_add_u64 v[212:213], s[22:23], 0, v[166:167]
	s_add_i32 m0, s59, 0x2000
	s_nop 0
	global_load_lds_dwordx4 v[212:213], off
	v_lshl_add_u64 v[212:213], s[42:43], 0, v[0:1]
	s_mov_b32 m0, s46
	s_nop 0
	global_load_lds_dwordx4 v[212:213], off
	s_mov_b32 m0, s47
	s_nop 0
	global_load_lds_dwordx4 v[214:215], off
	s_waitcnt vmcnt(8)
	s_waitcnt lgkmcnt(0)
	s_barrier
	s_setprio 1
	s_waitcnt lgkmcnt(0)
	v_mfma_f32_16x16x32_bf16 v[64:67], v[116:119], v[172:175], 0
	v_mfma_f32_16x16x32_bf16 v[60:63], v[124:127], v[172:175], 0
	v_mfma_f32_16x16x32_bf16 v[48:51], v[116:119], v[186:189], 0
	v_mfma_f32_16x16x32_bf16 v[44:47], v[124:127], v[186:189], 0
	v_mfma_f32_16x16x32_bf16 v[36:39], v[116:119], v[194:197], 0
	v_mfma_f32_16x16x32_bf16 v[28:31], v[124:127], v[194:197], 0
	v_mfma_f32_16x16x32_bf16 v[20:23], v[116:119], v[202:205], 0
	v_mfma_f32_16x16x32_bf16 v[12:15], v[124:127], v[202:205], 0
	v_mfma_f32_16x16x32_bf16 v[64:67], v[120:123], v[182:185], v[64:67]
	v_mfma_f32_16x16x32_bf16 v[60:63], v[128:131], v[182:185], v[60:63]
	v_mfma_f32_16x16x32_bf16 v[48:51], v[120:123], v[190:193], v[48:51]
	v_mfma_f32_16x16x32_bf16 v[44:47], v[128:131], v[190:193], v[44:47]
	v_mfma_f32_16x16x32_bf16 v[36:39], v[120:123], v[198:201], v[36:39]
	v_mfma_f32_16x16x32_bf16 v[28:31], v[128:131], v[198:201], v[28:31]
	v_mfma_f32_16x16x32_bf16 v[20:23], v[120:123], v[206:209], v[20:23]
	v_mfma_f32_16x16x32_bf16 v[12:15], v[128:131], v[206:209], v[12:15]
	s_setprio 0
	s_setprio 1
	v_mfma_f32_16x16x32_bf16 v[56:59], v[148:151], v[172:175], 0
	v_mfma_f32_16x16x32_bf16 v[52:55], v[156:159], v[172:175], 0
	v_mfma_f32_16x16x32_bf16 v[40:43], v[148:151], v[186:189], 0
	v_mfma_f32_16x16x32_bf16 v[32:35], v[156:159], v[186:189], 0
	v_mfma_f32_16x16x32_bf16 v[24:27], v[148:151], v[194:197], 0
	v_mfma_f32_16x16x32_bf16 v[16:19], v[156:159], v[194:197], 0
	v_mfma_f32_16x16x32_bf16 v[8:11], v[148:151], v[202:205], 0
	v_mfma_f32_16x16x32_bf16 v[4:7], v[156:159], v[202:205], 0
	v_mfma_f32_16x16x32_bf16 v[56:59], v[152:155], v[182:185], v[56:59]
	v_mfma_f32_16x16x32_bf16 v[52:55], v[160:163], v[182:185], v[52:55]
	v_mfma_f32_16x16x32_bf16 v[40:43], v[152:155], v[190:193], v[40:43]
	v_mfma_f32_16x16x32_bf16 v[32:35], v[160:163], v[190:193], v[32:35]
	v_mfma_f32_16x16x32_bf16 v[24:27], v[152:155], v[198:201], v[24:27]
	v_mfma_f32_16x16x32_bf16 v[16:19], v[160:163], v[198:201], v[16:19]
	v_mfma_f32_16x16x32_bf16 v[8:11], v[152:155], v[206:209], v[8:11]
	v_mfma_f32_16x16x32_bf16 v[4:7], v[160:163], v[206:209], v[4:7]
	s_setprio 0
	s_barrier
	s_add_i32 s59, 0, 0x18000
	s_add_i32 s60, 0, 0x1c000
	v_add_u32_e32 v128, s59, v179
	v_add_u32_e32 v160, s60, v179
	ds_read_b128 v[116:119], v128
	ds_read_b128 v[120:123], v128 offset:1024
	ds_read_b128 v[124:127], v128 offset:2048
	ds_read_b128 v[128:131], v128 offset:3072
	ds_read_b128 v[148:151], v160
	ds_read_b128 v[152:155], v160 offset:1024
	ds_read_b128 v[156:159], v160 offset:2048
	ds_read_b128 v[160:163], v160 offset:3072
	s_add_u32 s22, s42, 0x40000
	s_addc_u32 s23, s43, 0
	s_mov_b32 m0, s52
	v_lshl_add_u64 v[216:217], s[22:23], 0, v[0:1]
	ds_read_b128 v[172:175], v181 offset:32768
	ds_read_b128 v[182:185], v181 offset:33792
	ds_read_b128 v[186:189], v181 offset:34816
	ds_read_b128 v[190:193], v181 offset:35840
	ds_read_b128 v[194:197], v181 offset:36864
	ds_read_b128 v[198:201], v181 offset:37888
	ds_read_b128 v[202:205], v181 offset:38912
	ds_read_b128 v[206:209], v181 offset:39936
	global_load_lds_dwordx4 v[216:217], off
	v_lshl_add_u64 v[216:217], s[22:23], 0, v[164:165]
	s_mov_b32 m0, s53
	s_nop 0
	global_load_lds_dwordx4 v[216:217], off
	s_waitcnt vmcnt(8)
	s_waitcnt lgkmcnt(0)
	s_barrier
	s_setprio 1
	s_waitcnt lgkmcnt(0)
	v_mfma_f32_16x16x32_bf16 v[144:147], v[116:119], v[172:175], v[144:147]
	v_mfma_f32_16x16x32_bf16 v[140:143], v[124:127], v[172:175], v[140:143]
	v_mfma_f32_16x16x32_bf16 v[112:115], v[116:119], v[186:189], v[112:115]
	v_mfma_f32_16x16x32_bf16 v[108:111], v[124:127], v[186:189], v[108:111]
	v_mfma_f32_16x16x32_bf16 v[100:103], v[116:119], v[194:197], v[100:103]
	v_mfma_f32_16x16x32_bf16 v[92:95], v[124:127], v[194:197], v[92:95]
	v_mfma_f32_16x16x32_bf16 v[84:87], v[116:119], v[202:205], v[84:87]
	v_mfma_f32_16x16x32_bf16 v[76:79], v[124:127], v[202:205], v[76:79]
	v_mfma_f32_16x16x32_bf16 v[144:147], v[120:123], v[182:185], v[144:147]
	v_mfma_f32_16x16x32_bf16 v[140:143], v[128:131], v[182:185], v[140:143]
	v_mfma_f32_16x16x32_bf16 v[112:115], v[120:123], v[190:193], v[112:115]
	v_mfma_f32_16x16x32_bf16 v[108:111], v[128:131], v[190:193], v[108:111]
	v_mfma_f32_16x16x32_bf16 v[100:103], v[120:123], v[198:201], v[100:103]
	v_mfma_f32_16x16x32_bf16 v[92:95], v[128:131], v[198:201], v[92:95]
	v_mfma_f32_16x16x32_bf16 v[84:87], v[120:123], v[206:209], v[84:87]
	v_mfma_f32_16x16x32_bf16 v[76:79], v[128:131], v[206:209], v[76:79]
	s_setprio 0
	s_setprio 1
	v_mfma_f32_16x16x32_bf16 v[136:139], v[148:151], v[172:175], v[136:139]
	v_mfma_f32_16x16x32_bf16 v[132:135], v[156:159], v[172:175], v[132:135]
	v_mfma_f32_16x16x32_bf16 v[104:107], v[148:151], v[186:189], v[104:107]
	v_mfma_f32_16x16x32_bf16 v[96:99], v[156:159], v[186:189], v[96:99]
	v_mfma_f32_16x16x32_bf16 v[88:91], v[148:151], v[194:197], v[88:91]
	v_mfma_f32_16x16x32_bf16 v[80:83], v[156:159], v[194:197], v[80:83]
	v_mfma_f32_16x16x32_bf16 v[72:75], v[148:151], v[202:205], v[72:75]
	v_mfma_f32_16x16x32_bf16 v[68:71], v[156:159], v[202:205], v[68:71]
	v_mfma_f32_16x16x32_bf16 v[136:139], v[152:155], v[182:185], v[136:139]
	v_mfma_f32_16x16x32_bf16 v[132:135], v[160:163], v[182:185], v[132:135]
	v_mfma_f32_16x16x32_bf16 v[104:107], v[152:155], v[190:193], v[104:107]
	v_mfma_f32_16x16x32_bf16 v[96:99], v[160:163], v[190:193], v[96:99]
	v_mfma_f32_16x16x32_bf16 v[88:91], v[152:155], v[198:201], v[88:91]
	v_mfma_f32_16x16x32_bf16 v[80:83], v[160:163], v[198:201], v[80:83]
	v_mfma_f32_16x16x32_bf16 v[72:75], v[152:155], v[206:209], v[72:75]
	v_mfma_f32_16x16x32_bf16 v[68:71], v[160:163], v[206:209], v[68:71]
	s_setprio 0
	s_barrier
	s_add_i32 s22, s59, s45
	v_lshl_add_u64 v[176:177], v[176:177], 0, s[28:29]
	s_mov_b32 m0, s22
	ds_read_b128 v[172:175], v181 offset:49152
	ds_read_b128 v[182:185], v181 offset:50176
	ds_read_b128 v[186:189], v181 offset:51200
	ds_read_b128 v[190:193], v181 offset:52224
	ds_read_b128 v[194:197], v181 offset:53248
	ds_read_b128 v[198:201], v181 offset:54272
	ds_read_b128 v[202:205], v181 offset:55296
	ds_read_b128 v[206:209], v181 offset:56320
	global_load_lds_dwordx4 v[176:177], off
	s_add_i32 m0, s22, 0x2000
	s_add_u32 s22, s40, 0x40080
	v_lshl_add_u64 v[176:177], v[210:211], 0, s[28:29]
	s_addc_u32 s23, s41, 0
	s_add_i32 s40, s60, s45
	global_load_lds_dwordx4 v[176:177], off
	v_lshl_add_u64 v[176:177], s[22:23], 0, v[2:3]
	s_mov_b32 m0, s40
	s_nop 0
	global_load_lds_dwordx4 v[176:177], off
	v_lshl_add_u64 v[176:177], s[22:23], 0, v[166:167]
	s_add_i32 m0, s40, 0x2000
	s_nop 0
	global_load_lds_dwordx4 v[176:177], off
	v_lshl_add_u64 v[176:177], v[212:213], 0, s[28:29]
	s_mov_b32 m0, s55
	s_nop 0
	global_load_lds_dwordx4 v[176:177], off
	v_lshl_add_u64 v[176:177], v[214:215], 0, s[28:29]
	s_mov_b32 m0, s56
	s_nop 0
	global_load_lds_dwordx4 v[176:177], off
	s_waitcnt vmcnt(8)
	s_waitcnt lgkmcnt(0)
	s_barrier
	s_setprio 1
	s_waitcnt lgkmcnt(0)
	v_mfma_f32_16x16x32_bf16 v[64:67], v[116:119], v[172:175], v[64:67]
	v_mfma_f32_16x16x32_bf16 v[60:63], v[124:127], v[172:175], v[60:63]
	v_mfma_f32_16x16x32_bf16 v[48:51], v[116:119], v[186:189], v[48:51]
	v_mfma_f32_16x16x32_bf16 v[44:47], v[124:127], v[186:189], v[44:47]
	v_mfma_f32_16x16x32_bf16 v[36:39], v[116:119], v[194:197], v[36:39]
	v_mfma_f32_16x16x32_bf16 v[28:31], v[124:127], v[194:197], v[28:31]
	v_mfma_f32_16x16x32_bf16 v[20:23], v[116:119], v[202:205], v[20:23]
	v_mfma_f32_16x16x32_bf16 v[12:15], v[124:127], v[202:205], v[12:15]
	v_mfma_f32_16x16x32_bf16 v[64:67], v[120:123], v[182:185], v[64:67]
	v_mfma_f32_16x16x32_bf16 v[60:63], v[128:131], v[182:185], v[60:63]
	v_mfma_f32_16x16x32_bf16 v[48:51], v[120:123], v[190:193], v[48:51]
	v_mfma_f32_16x16x32_bf16 v[44:47], v[128:131], v[190:193], v[44:47]
	v_mfma_f32_16x16x32_bf16 v[36:39], v[120:123], v[198:201], v[36:39]
	v_mfma_f32_16x16x32_bf16 v[28:31], v[128:131], v[198:201], v[28:31]
	v_mfma_f32_16x16x32_bf16 v[20:23], v[120:123], v[206:209], v[20:23]
	v_mfma_f32_16x16x32_bf16 v[12:15], v[128:131], v[206:209], v[12:15]
	s_setprio 0
	s_setprio 1
	v_mfma_f32_16x16x32_bf16 v[56:59], v[148:151], v[172:175], v[56:59]
	v_mfma_f32_16x16x32_bf16 v[52:55], v[156:159], v[172:175], v[52:55]
	v_mfma_f32_16x16x32_bf16 v[40:43], v[148:151], v[186:189], v[40:43]
	v_mfma_f32_16x16x32_bf16 v[32:35], v[156:159], v[186:189], v[32:35]
	v_mfma_f32_16x16x32_bf16 v[24:27], v[148:151], v[194:197], v[24:27]
	v_mfma_f32_16x16x32_bf16 v[16:19], v[156:159], v[194:197], v[16:19]
	v_mfma_f32_16x16x32_bf16 v[8:11], v[148:151], v[202:205], v[8:11]
	v_mfma_f32_16x16x32_bf16 v[4:7], v[156:159], v[202:205], v[4:7]
	v_mfma_f32_16x16x32_bf16 v[56:59], v[152:155], v[182:185], v[56:59]
	v_mfma_f32_16x16x32_bf16 v[52:55], v[160:163], v[182:185], v[52:55]
	v_mfma_f32_16x16x32_bf16 v[40:43], v[152:155], v[190:193], v[40:43]
	v_mfma_f32_16x16x32_bf16 v[32:35], v[160:163], v[190:193], v[32:35]
	v_mfma_f32_16x16x32_bf16 v[24:27], v[152:155], v[198:201], v[24:27]
	v_mfma_f32_16x16x32_bf16 v[16:19], v[160:163], v[198:201], v[16:19]
	v_mfma_f32_16x16x32_bf16 v[8:11], v[152:155], v[206:209], v[8:11]
	v_mfma_f32_16x16x32_bf16 v[4:7], v[160:163], v[206:209], v[4:7]
	s_setprio 0
	s_barrier
	s_add_i32 s58, s58, 2
	s_add_u32 s13, s13, 0x100
	s_addc_u32 s15, s15, 0
	s_cmp_gt_u32 s58, 13
	s_mov_b64 s[22:23], s[26:27]
	s_cbranch_scc1 .Lmy_gx1
	.p2alignl 6, 3212836864

.LBB0_1035:
	s_ashr_i32 s15, s14, 31
	s_lshl_b64 s[18:19], s[14:15], 19
	s_add_u32 s18, s25, s18
	s_addc_u32 s19, s31, s19
	s_and_b64 s[20:21], s[38:39], exec
	s_cselect_b32 s15, s19, s23
	s_cselect_b32 s54, s18, s22
	s_ashr_i32 s13, s12, 31
	s_lshl_b64 s[20:21], s[12:13], 19
	s_add_u32 s20, s35, s20
	s_addc_u32 s21, s36, s21
	s_and_b64 s[40:41], s[38:39], exec
	s_cselect_b32 s13, s21, s27
	s_cselect_b32 s55, s20, s26
	s_add_u32 s56, s26, 0x100
	s_addc_u32 s57, s27, 0
	s_mov_b32 s58, -2
	s_add_u32 s26, s22, 0x100
	s_addc_u32 s27, s23, 0
	s_add_i32 s59, 0, 0x10000
	s_cmp_eq_u32 s58, 12
	s_cselect_b32 s43, s15, s27
	s_cselect_b32 s42, s54, s26
	s_cselect_b32 s41, s13, s57
	s_cselect_b32 s40, s55, s56
	s_add_i32 s60, 0, 0x14000
	v_add_u32_e32 v156, s59, v141
	v_add_u32_e32 v172, s60, v141
	ds_read_b128 v[144:147], v156
	ds_read_b128 v[148:151], v156 offset:1024
	ds_read_b128 v[152:155], v156 offset:2048
	ds_read_b128 v[156:159], v156 offset:3072
	ds_read_b128 v[160:163], v172
	ds_read_b128 v[164:167], v172 offset:1024
	ds_read_b128 v[168:171], v172 offset:2048
	ds_read_b128 v[172:175], v172 offset:3072
	v_lshl_add_u64 v[208:209], s[22:23], 0, v[138:139]
	s_add_i32 m0, s45, 0xc000
	ds_read_b128 v[176:179], v143
	ds_read_b128 v[180:183], v143 offset:1024
	ds_read_b128 v[184:187], v143 offset:2048
	ds_read_b128 v[188:191], v143 offset:3072
	ds_read_b128 v[192:195], v143 offset:4096
	ds_read_b128 v[196:199], v143 offset:5120
	ds_read_b128 v[200:203], v143 offset:6144
	ds_read_b128 v[204:207], v143 offset:7168
	global_load_lds_dwordx4 v[208:209], off
	v_lshl_add_u64 v[208:209], s[22:23], 0, v[136:137]
	s_add_i32 m0, s45, 0xe000
	s_nop 0
	global_load_lds_dwordx4 v[208:209], off
	s_waitcnt vmcnt(8)
	s_waitcnt lgkmcnt(0)
	s_barrier
	s_setprio 1
	s_waitcnt lgkmcnt(0)
	v_mfma_f32_16x16x32_bf16 v[128:131], v[144:147], v[176:179], 0
	v_mfma_f32_16x16x32_bf16 v[120:123], v[152:155], v[176:179], 0
	v_mfma_f32_16x16x32_bf16 v[112:115], v[144:147], v[184:187], 0
	v_mfma_f32_16x16x32_bf16 v[104:107], v[152:155], v[184:187], 0
	v_mfma_f32_16x16x32_bf16 v[96:99], v[144:147], v[192:195], 0
	v_mfma_f32_16x16x32_bf16 v[88:91], v[152:155], v[192:195], 0
	v_mfma_f32_16x16x32_bf16 v[80:83], v[144:147], v[200:203], 0
	v_mfma_f32_16x16x32_bf16 v[72:75], v[152:155], v[200:203], 0
	v_mfma_f32_16x16x32_bf16 v[128:131], v[148:151], v[180:183], v[128:131]
	v_mfma_f32_16x16x32_bf16 v[120:123], v[156:159], v[180:183], v[120:123]
	v_mfma_f32_16x16x32_bf16 v[112:115], v[148:151], v[188:191], v[112:115]
	v_mfma_f32_16x16x32_bf16 v[104:107], v[156:159], v[188:191], v[104:107]
	v_mfma_f32_16x16x32_bf16 v[96:99], v[148:151], v[196:199], v[96:99]
	v_mfma_f32_16x16x32_bf16 v[88:91], v[156:159], v[196:199], v[88:91]
	v_mfma_f32_16x16x32_bf16 v[80:83], v[148:151], v[204:207], v[80:83]
	v_mfma_f32_16x16x32_bf16 v[72:75], v[156:159], v[204:207], v[72:75]
	s_setprio 0
	s_setprio 1
	v_mfma_f32_16x16x32_bf16 v[124:127], v[160:163], v[176:179], 0
	v_mfma_f32_16x16x32_bf16 v[116:119], v[168:171], v[176:179], 0
	v_mfma_f32_16x16x32_bf16 v[108:111], v[160:163], v[184:187], 0
	v_mfma_f32_16x16x32_bf16 v[100:103], v[168:171], v[184:187], 0
	v_mfma_f32_16x16x32_bf16 v[92:95], v[160:163], v[192:195], 0
	v_mfma_f32_16x16x32_bf16 v[84:87], v[168:171], v[192:195], 0
	v_mfma_f32_16x16x32_bf16 v[76:79], v[160:163], v[200:203], 0
	v_mfma_f32_16x16x32_bf16 v[68:71], v[168:171], v[200:203], 0
	v_mfma_f32_16x16x32_bf16 v[124:127], v[164:167], v[180:183], v[124:127]
	v_mfma_f32_16x16x32_bf16 v[116:119], v[172:175], v[180:183], v[116:119]
	v_mfma_f32_16x16x32_bf16 v[108:111], v[164:167], v[188:191], v[108:111]
	v_mfma_f32_16x16x32_bf16 v[100:103], v[172:175], v[188:191], v[100:103]
	v_mfma_f32_16x16x32_bf16 v[92:95], v[164:167], v[196:199], v[92:95]
	v_mfma_f32_16x16x32_bf16 v[84:87], v[172:175], v[196:199], v[84:87]
	v_mfma_f32_16x16x32_bf16 v[76:79], v[164:167], v[204:207], v[76:79]
	v_mfma_f32_16x16x32_bf16 v[68:71], v[172:175], v[204:207], v[68:71]
	s_setprio 0
	s_barrier
	s_add_i32 s22, s59, s37
	v_lshl_add_u64 v[208:209], s[40:41], 0, v[2:3]
	s_mov_b32 m0, s22
	ds_read_b128 v[176:179], v143 offset:16384
	ds_read_b128 v[180:183], v143 offset:17408
	ds_read_b128 v[184:187], v143 offset:18432
	ds_read_b128 v[188:191], v143 offset:19456
	ds_read_b128 v[192:195], v143 offset:20480
	ds_read_b128 v[196:199], v143 offset:21504
	ds_read_b128 v[200:203], v143 offset:22528
	ds_read_b128 v[204:207], v143 offset:23552
	global_load_lds_dwordx4 v[208:209], off
	s_add_i32 m0, s22, 0x2000
	s_add_u32 s22, s40, 0x40000
	v_lshl_add_u64 v[210:211], s[40:41], 0, v[0:1]
	s_addc_u32 s23, s41, 0
	s_add_i32 s59, s60, s37
	global_load_lds_dwordx4 v[210:211], off
	v_lshl_add_u64 v[212:213], s[22:23], 0, v[2:3]
	s_mov_b32 m0, s59
	v_lshl_add_u64 v[214:215], s[42:43], 0, v[132:133]
	global_load_lds_dwordx4 v[212:213], off
	v_lshl_add_u64 v[212:213], s[22:23], 0, v[0:1]
	s_add_i32 m0, s59, 0x2000
	s_nop 0
	global_load_lds_dwordx4 v[212:213], off
	v_lshl_add_u64 v[212:213], s[42:43], 0, v[134:135]
	s_mov_b32 m0, s45
	s_nop 0
	global_load_lds_dwordx4 v[212:213], off
	s_mov_b32 m0, s46
	s_nop 0
	global_load_lds_dwordx4 v[214:215], off
	s_waitcnt vmcnt(8)
	s_waitcnt lgkmcnt(0)
	s_barrier
	s_setprio 1
	s_waitcnt lgkmcnt(0)
	v_mfma_f32_16x16x32_bf16 v[64:67], v[144:147], v[176:179], 0
	v_mfma_f32_16x16x32_bf16 v[56:59], v[152:155], v[176:179], 0
	v_mfma_f32_16x16x32_bf16 v[48:51], v[144:147], v[184:187], 0
	v_mfma_f32_16x16x32_bf16 v[40:43], v[152:155], v[184:187], 0
	v_mfma_f32_16x16x32_bf16 v[32:35], v[144:147], v[192:195], 0
	v_mfma_f32_16x16x32_bf16 v[24:27], v[152:155], v[192:195], 0
	v_mfma_f32_16x16x32_bf16 v[16:19], v[144:147], v[200:203], 0
	v_mfma_f32_16x16x32_bf16 v[8:11], v[152:155], v[200:203], 0
	v_mfma_f32_16x16x32_bf16 v[64:67], v[148:151], v[180:183], v[64:67]
	v_mfma_f32_16x16x32_bf16 v[56:59], v[156:159], v[180:183], v[56:59]
	v_mfma_f32_16x16x32_bf16 v[48:51], v[148:151], v[188:191], v[48:51]
	v_mfma_f32_16x16x32_bf16 v[40:43], v[156:159], v[188:191], v[40:43]
	v_mfma_f32_16x16x32_bf16 v[32:35], v[148:151], v[196:199], v[32:35]
	v_mfma_f32_16x16x32_bf16 v[24:27], v[156:159], v[196:199], v[24:27]
	v_mfma_f32_16x16x32_bf16 v[16:19], v[148:151], v[204:207], v[16:19]
	v_mfma_f32_16x16x32_bf16 v[8:11], v[156:159], v[204:207], v[8:11]
	s_setprio 0
	s_setprio 1
	v_mfma_f32_16x16x32_bf16 v[60:63], v[160:163], v[176:179], 0
	v_mfma_f32_16x16x32_bf16 v[52:55], v[168:171], v[176:179], 0
	v_mfma_f32_16x16x32_bf16 v[44:47], v[160:163], v[184:187], 0
	v_mfma_f32_16x16x32_bf16 v[36:39], v[168:171], v[184:187], 0
	v_mfma_f32_16x16x32_bf16 v[28:31], v[160:163], v[192:195], 0
	v_mfma_f32_16x16x32_bf16 v[20:23], v[168:171], v[192:195], 0
	v_mfma_f32_16x16x32_bf16 v[12:15], v[160:163], v[200:203], 0
	v_mfma_f32_16x16x32_bf16 v[4:7], v[168:171], v[200:203], 0
	v_mfma_f32_16x16x32_bf16 v[60:63], v[164:167], v[180:183], v[60:63]
	v_mfma_f32_16x16x32_bf16 v[52:55], v[172:175], v[180:183], v[52:55]
	v_mfma_f32_16x16x32_bf16 v[44:47], v[164:167], v[188:191], v[44:47]
	v_mfma_f32_16x16x32_bf16 v[36:39], v[172:175], v[188:191], v[36:39]
	v_mfma_f32_16x16x32_bf16 v[28:31], v[164:167], v[196:199], v[28:31]
	v_mfma_f32_16x16x32_bf16 v[20:23], v[172:175], v[196:199], v[20:23]
	v_mfma_f32_16x16x32_bf16 v[12:15], v[164:167], v[204:207], v[12:15]
	v_mfma_f32_16x16x32_bf16 v[4:7], v[172:175], v[204:207], v[4:7]
	s_setprio 0
	s_barrier
	s_add_i32 s59, 0, 0x18000
	s_add_i32 s60, 0, 0x1c000
	v_add_u32_e32 v156, s59, v141
	v_add_u32_e32 v172, s60, v141
	ds_read_b128 v[144:147], v156
	ds_read_b128 v[148:151], v156 offset:1024
	ds_read_b128 v[152:155], v156 offset:2048
	ds_read_b128 v[156:159], v156 offset:3072
	ds_read_b128 v[160:163], v172
	ds_read_b128 v[164:167], v172 offset:1024
	ds_read_b128 v[168:171], v172 offset:2048
	ds_read_b128 v[172:175], v172 offset:3072
	s_add_u32 s22, s42, 0x40000
	s_addc_u32 s23, s43, 0
	s_mov_b32 m0, s47
	v_lshl_add_u64 v[216:217], s[22:23], 0, v[134:135]
	ds_read_b128 v[176:179], v143 offset:32768
	ds_read_b128 v[180:183], v143 offset:33792
	ds_read_b128 v[184:187], v143 offset:34816
	ds_read_b128 v[188:191], v143 offset:35840
	ds_read_b128 v[192:195], v143 offset:36864
	ds_read_b128 v[196:199], v143 offset:37888
	ds_read_b128 v[200:203], v143 offset:38912
	ds_read_b128 v[204:207], v143 offset:39936
	global_load_lds_dwordx4 v[216:217], off
	v_lshl_add_u64 v[216:217], s[22:23], 0, v[132:133]
	s_mov_b32 m0, s50
	s_nop 0
	global_load_lds_dwordx4 v[216:217], off
	s_waitcnt vmcnt(8)
	s_waitcnt lgkmcnt(0)
	s_barrier
	s_setprio 1
	s_waitcnt lgkmcnt(0)
	v_mfma_f32_16x16x32_bf16 v[128:131], v[144:147], v[176:179], v[128:131]
	v_mfma_f32_16x16x32_bf16 v[120:123], v[152:155], v[176:179], v[120:123]
	v_mfma_f32_16x16x32_bf16 v[112:115], v[144:147], v[184:187], v[112:115]
	v_mfma_f32_16x16x32_bf16 v[104:107], v[152:155], v[184:187], v[104:107]
	v_mfma_f32_16x16x32_bf16 v[96:99], v[144:147], v[192:195], v[96:99]
	v_mfma_f32_16x16x32_bf16 v[88:91], v[152:155], v[192:195], v[88:91]
	v_mfma_f32_16x16x32_bf16 v[80:83], v[144:147], v[200:203], v[80:83]
	v_mfma_f32_16x16x32_bf16 v[72:75], v[152:155], v[200:203], v[72:75]
	v_mfma_f32_16x16x32_bf16 v[128:131], v[148:151], v[180:183], v[128:131]
	v_mfma_f32_16x16x32_bf16 v[120:123], v[156:159], v[180:183], v[120:123]
	v_mfma_f32_16x16x32_bf16 v[112:115], v[148:151], v[188:191], v[112:115]
	v_mfma_f32_16x16x32_bf16 v[104:107], v[156:159], v[188:191], v[104:107]
	v_mfma_f32_16x16x32_bf16 v[96:99], v[148:151], v[196:199], v[96:99]
	v_mfma_f32_16x16x32_bf16 v[88:91], v[156:159], v[196:199], v[88:91]
	v_mfma_f32_16x16x32_bf16 v[80:83], v[148:151], v[204:207], v[80:83]
	v_mfma_f32_16x16x32_bf16 v[72:75], v[156:159], v[204:207], v[72:75]
	s_setprio 0
	s_setprio 1
	v_mfma_f32_16x16x32_bf16 v[124:127], v[160:163], v[176:179], v[124:127]
	v_mfma_f32_16x16x32_bf16 v[116:119], v[168:171], v[176:179], v[116:119]
	v_mfma_f32_16x16x32_bf16 v[108:111], v[160:163], v[184:187], v[108:111]
	v_mfma_f32_16x16x32_bf16 v[100:103], v[168:171], v[184:187], v[100:103]
	v_mfma_f32_16x16x32_bf16 v[92:95], v[160:163], v[192:195], v[92:95]
	v_mfma_f32_16x16x32_bf16 v[84:87], v[168:171], v[192:195], v[84:87]
	v_mfma_f32_16x16x32_bf16 v[76:79], v[160:163], v[200:203], v[76:79]
	v_mfma_f32_16x16x32_bf16 v[68:71], v[168:171], v[200:203], v[68:71]
	v_mfma_f32_16x16x32_bf16 v[124:127], v[164:167], v[180:183], v[124:127]
	v_mfma_f32_16x16x32_bf16 v[116:119], v[172:175], v[180:183], v[116:119]
	v_mfma_f32_16x16x32_bf16 v[108:111], v[164:167], v[188:191], v[108:111]
	v_mfma_f32_16x16x32_bf16 v[100:103], v[172:175], v[188:191], v[100:103]
	v_mfma_f32_16x16x32_bf16 v[92:95], v[164:167], v[196:199], v[92:95]
	v_mfma_f32_16x16x32_bf16 v[84:87], v[172:175], v[196:199], v[84:87]
	v_mfma_f32_16x16x32_bf16 v[76:79], v[164:167], v[204:207], v[76:79]
	v_mfma_f32_16x16x32_bf16 v[68:71], v[172:175], v[204:207], v[68:71]
	s_setprio 0
	s_barrier
	s_add_i32 s22, s59, s37
	v_lshl_add_u64 v[208:209], v[208:209], 0, s[28:29]
	s_mov_b32 m0, s22
	ds_read_b128 v[176:179], v143 offset:49152
	ds_read_b128 v[180:183], v143 offset:50176
	ds_read_b128 v[184:187], v143 offset:51200
	ds_read_b128 v[188:191], v143 offset:52224
	ds_read_b128 v[192:195], v143 offset:53248
	ds_read_b128 v[196:199], v143 offset:54272
	ds_read_b128 v[200:203], v143 offset:55296
	ds_read_b128 v[204:207], v143 offset:56320
	global_load_lds_dwordx4 v[208:209], off
	s_add_i32 m0, s22, 0x2000
	s_add_u32 s22, s40, 0x40080
	v_lshl_add_u64 v[208:209], v[210:211], 0, s[28:29]
	s_addc_u32 s23, s41, 0
	s_add_i32 s40, s60, s37
	global_load_lds_dwordx4 v[208:209], off
	v_lshl_add_u64 v[208:209], s[22:23], 0, v[2:3]
	s_mov_b32 m0, s40
	s_nop 0
	global_load_lds_dwordx4 v[208:209], off
	v_lshl_add_u64 v[208:209], s[22:23], 0, v[0:1]
	s_add_i32 m0, s40, 0x2000
	s_nop 0
	global_load_lds_dwordx4 v[208:209], off
	v_lshl_add_u64 v[208:209], v[212:213], 0, s[28:29]
	s_mov_b32 m0, s51
	s_nop 0
	global_load_lds_dwordx4 v[208:209], off
	v_lshl_add_u64 v[208:209], v[214:215], 0, s[28:29]
	s_mov_b32 m0, s52
	s_nop 0
	global_load_lds_dwordx4 v[208:209], off
	s_waitcnt vmcnt(8)
	s_waitcnt lgkmcnt(0)
	s_barrier
	s_setprio 1
	s_waitcnt lgkmcnt(0)
	v_mfma_f32_16x16x32_bf16 v[64:67], v[144:147], v[176:179], v[64:67]
	v_mfma_f32_16x16x32_bf16 v[56:59], v[152:155], v[176:179], v[56:59]
	v_mfma_f32_16x16x32_bf16 v[48:51], v[144:147], v[184:187], v[48:51]
	v_mfma_f32_16x16x32_bf16 v[40:43], v[152:155], v[184:187], v[40:43]
	v_mfma_f32_16x16x32_bf16 v[32:35], v[144:147], v[192:195], v[32:35]
	v_mfma_f32_16x16x32_bf16 v[24:27], v[152:155], v[192:195], v[24:27]
	v_mfma_f32_16x16x32_bf16 v[16:19], v[144:147], v[200:203], v[16:19]
	v_mfma_f32_16x16x32_bf16 v[8:11], v[152:155], v[200:203], v[8:11]
	v_mfma_f32_16x16x32_bf16 v[64:67], v[148:151], v[180:183], v[64:67]
	v_mfma_f32_16x16x32_bf16 v[56:59], v[156:159], v[180:183], v[56:59]
	v_mfma_f32_16x16x32_bf16 v[48:51], v[148:151], v[188:191], v[48:51]
	v_mfma_f32_16x16x32_bf16 v[40:43], v[156:159], v[188:191], v[40:43]
	v_mfma_f32_16x16x32_bf16 v[32:35], v[148:151], v[196:199], v[32:35]
	v_mfma_f32_16x16x32_bf16 v[24:27], v[156:159], v[196:199], v[24:27]
	v_mfma_f32_16x16x32_bf16 v[16:19], v[148:151], v[204:207], v[16:19]
	v_mfma_f32_16x16x32_bf16 v[8:11], v[156:159], v[204:207], v[8:11]
	s_setprio 0
	s_setprio 1
	v_mfma_f32_16x16x32_bf16 v[60:63], v[160:163], v[176:179], v[60:63]
	v_mfma_f32_16x16x32_bf16 v[52:55], v[168:171], v[176:179], v[52:55]
	v_mfma_f32_16x16x32_bf16 v[44:47], v[160:163], v[184:187], v[44:47]
	v_mfma_f32_16x16x32_bf16 v[36:39], v[168:171], v[184:187], v[36:39]
	v_mfma_f32_16x16x32_bf16 v[28:31], v[160:163], v[192:195], v[28:31]
	v_mfma_f32_16x16x32_bf16 v[20:23], v[168:171], v[192:195], v[20:23]
	v_mfma_f32_16x16x32_bf16 v[12:15], v[160:163], v[200:203], v[12:15]
	v_mfma_f32_16x16x32_bf16 v[4:7], v[168:171], v[200:203], v[4:7]
	v_mfma_f32_16x16x32_bf16 v[60:63], v[164:167], v[180:183], v[60:63]
	v_mfma_f32_16x16x32_bf16 v[52:55], v[172:175], v[180:183], v[52:55]
	v_mfma_f32_16x16x32_bf16 v[44:47], v[164:167], v[188:191], v[44:47]
	v_mfma_f32_16x16x32_bf16 v[36:39], v[172:175], v[188:191], v[36:39]
	v_mfma_f32_16x16x32_bf16 v[28:31], v[164:167], v[196:199], v[28:31]
	v_mfma_f32_16x16x32_bf16 v[20:23], v[172:175], v[196:199], v[20:23]
	v_mfma_f32_16x16x32_bf16 v[12:15], v[164:167], v[204:207], v[12:15]
	v_mfma_f32_16x16x32_bf16 v[4:7], v[172:175], v[204:207], v[4:7]
	s_setprio 0
	s_barrier
	s_add_i32 s58, s58, 2
	s_add_u32 s56, s56, 0x100
	s_addc_u32 s57, s57, 0
	s_cmp_gt_u32 s58, 13
	s_mov_b64 s[22:23], s[26:27]
	s_cbranch_scc1 .Lmy_gx2
	.p2alignl 6, 3212836864

.LBB0_1111:
	s_add_u32 s54, s18, 0x100
	s_addc_u32 s55, s19, 0
	s_mov_b32 s56, -2
	s_waitcnt vmcnt(0)
	s_add_u32 s18, s10, 0x100
	s_addc_u32 s19, s11, 0
	s_add_i32 s57, 0, 0x10000
	s_cmp_eq_u32 s56, 40
	s_cselect_b32 s23, s1, s19
	s_cselect_b32 s22, s0, s18
	s_cselect_b32 s21, s15, s55
	s_cselect_b32 s20, s14, s54
	s_add_i32 s58, 0, 0x14000
	v_add_u32_e32 v128, s57, v179
	v_add_u32_e32 v160, s58, v179
	ds_read_b128 v[116:119], v128
	ds_read_b128 v[120:123], v128 offset:1024
	ds_read_b128 v[124:127], v128 offset:2048
	ds_read_b128 v[128:131], v128 offset:3072
	ds_read_b128 v[148:151], v160
	ds_read_b128 v[152:155], v160 offset:1024
	ds_read_b128 v[156:159], v160 offset:2048
	ds_read_b128 v[160:163], v160 offset:3072
	v_lshl_add_u64 v[176:177], s[10:11], 0, v[170:171]
	s_add_i32 m0, s40, 0xc000
	ds_read_b128 v[172:175], v181
	ds_read_b128 v[182:185], v181 offset:1024
	ds_read_b128 v[186:189], v181 offset:2048
	ds_read_b128 v[190:193], v181 offset:3072
	ds_read_b128 v[194:197], v181 offset:4096
	ds_read_b128 v[198:201], v181 offset:5120
	ds_read_b128 v[202:205], v181 offset:6144
	ds_read_b128 v[206:209], v181 offset:7168
	global_load_lds_dwordx4 v[176:177], off
	v_lshl_add_u64 v[176:177], s[10:11], 0, v[168:169]
	s_add_i32 m0, s40, 0xe000
	s_nop 0
	global_load_lds_dwordx4 v[176:177], off
	s_waitcnt vmcnt(8)
	s_waitcnt lgkmcnt(0)
	s_barrier
	s_setprio 1
	s_waitcnt lgkmcnt(0)
	v_mfma_f32_16x16x32_bf16 v[144:147], v[116:119], v[172:175], 0
	v_mfma_f32_16x16x32_bf16 v[140:143], v[124:127], v[172:175], 0
	v_mfma_f32_16x16x32_bf16 v[112:115], v[116:119], v[186:189], 0
	v_mfma_f32_16x16x32_bf16 v[108:111], v[124:127], v[186:189], 0
	v_mfma_f32_16x16x32_bf16 v[100:103], v[116:119], v[194:197], 0
	v_mfma_f32_16x16x32_bf16 v[92:95], v[124:127], v[194:197], 0
	v_mfma_f32_16x16x32_bf16 v[84:87], v[116:119], v[202:205], 0
	v_mfma_f32_16x16x32_bf16 v[76:79], v[124:127], v[202:205], 0
	v_mfma_f32_16x16x32_bf16 v[144:147], v[120:123], v[182:185], v[144:147]
	v_mfma_f32_16x16x32_bf16 v[140:143], v[128:131], v[182:185], v[140:143]
	v_mfma_f32_16x16x32_bf16 v[112:115], v[120:123], v[190:193], v[112:115]
	v_mfma_f32_16x16x32_bf16 v[108:111], v[128:131], v[190:193], v[108:111]
	v_mfma_f32_16x16x32_bf16 v[100:103], v[120:123], v[198:201], v[100:103]
	v_mfma_f32_16x16x32_bf16 v[92:95], v[128:131], v[198:201], v[92:95]
	v_mfma_f32_16x16x32_bf16 v[84:87], v[120:123], v[206:209], v[84:87]
	v_mfma_f32_16x16x32_bf16 v[76:79], v[128:131], v[206:209], v[76:79]
	s_setprio 0
	s_setprio 1
	v_mfma_f32_16x16x32_bf16 v[136:139], v[148:151], v[172:175], 0
	v_mfma_f32_16x16x32_bf16 v[132:135], v[156:159], v[172:175], 0
	v_mfma_f32_16x16x32_bf16 v[104:107], v[148:151], v[186:189], 0
	v_mfma_f32_16x16x32_bf16 v[96:99], v[156:159], v[186:189], 0
	v_mfma_f32_16x16x32_bf16 v[88:91], v[148:151], v[194:197], 0
	v_mfma_f32_16x16x32_bf16 v[80:83], v[156:159], v[194:197], 0
	v_mfma_f32_16x16x32_bf16 v[72:75], v[148:151], v[202:205], 0
	v_mfma_f32_16x16x32_bf16 v[68:71], v[156:159], v[202:205], 0
	v_mfma_f32_16x16x32_bf16 v[136:139], v[152:155], v[182:185], v[136:139]
	v_mfma_f32_16x16x32_bf16 v[132:135], v[160:163], v[182:185], v[132:135]
	v_mfma_f32_16x16x32_bf16 v[104:107], v[152:155], v[190:193], v[104:107]
	v_mfma_f32_16x16x32_bf16 v[96:99], v[160:163], v[190:193], v[96:99]
	v_mfma_f32_16x16x32_bf16 v[88:91], v[152:155], v[198:201], v[88:91]
	v_mfma_f32_16x16x32_bf16 v[80:83], v[160:163], v[198:201], v[80:83]
	v_mfma_f32_16x16x32_bf16 v[72:75], v[152:155], v[206:209], v[72:75]
	v_mfma_f32_16x16x32_bf16 v[68:71], v[160:163], v[206:209], v[68:71]
	s_setprio 0
	s_barrier
	s_add_i32 s10, s57, s37
	v_lshl_add_u64 v[176:177], s[20:21], 0, v[2:3]
	s_mov_b32 m0, s10
	ds_read_b128 v[172:175], v181 offset:16384
	ds_read_b128 v[182:185], v181 offset:17408
	ds_read_b128 v[186:189], v181 offset:18432
	ds_read_b128 v[190:193], v181 offset:19456
	ds_read_b128 v[194:197], v181 offset:20480
	ds_read_b128 v[198:201], v181 offset:21504
	ds_read_b128 v[202:205], v181 offset:22528
	ds_read_b128 v[206:209], v181 offset:23552
	global_load_lds_dwordx4 v[176:177], off
	s_add_i32 m0, s10, 0x2000
	s_add_u32 s10, s20, 0xb0000
	v_lshl_add_u64 v[210:211], s[20:21], 0, v[166:167]
	s_addc_u32 s11, s21, 0
	s_add_i32 s57, s58, s37
	global_load_lds_dwordx4 v[210:211], off
	v_lshl_add_u64 v[212:213], s[10:11], 0, v[2:3]
	s_mov_b32 m0, s57
	v_lshl_add_u64 v[214:215], s[22:23], 0, v[164:165]
	global_load_lds_dwordx4 v[212:213], off
	v_lshl_add_u64 v[212:213], s[10:11], 0, v[166:167]
	s_add_i32 m0, s57, 0x2000
	s_nop 0
	global_load_lds_dwordx4 v[212:213], off
	v_lshl_add_u64 v[212:213], s[22:23], 0, v[0:1]
	s_mov_b32 m0, s40
	s_nop 0
	global_load_lds_dwordx4 v[212:213], off
	s_mov_b32 m0, s41
	s_nop 0
	global_load_lds_dwordx4 v[214:215], off
	s_waitcnt vmcnt(8)
	s_waitcnt lgkmcnt(0)
	s_barrier
	s_setprio 1
	s_waitcnt lgkmcnt(0)
	v_mfma_f32_16x16x32_bf16 v[64:67], v[116:119], v[172:175], 0
	v_mfma_f32_16x16x32_bf16 v[60:63], v[124:127], v[172:175], 0
	v_mfma_f32_16x16x32_bf16 v[48:51], v[116:119], v[186:189], 0
	v_mfma_f32_16x16x32_bf16 v[44:47], v[124:127], v[186:189], 0
	v_mfma_f32_16x16x32_bf16 v[36:39], v[116:119], v[194:197], 0
	v_mfma_f32_16x16x32_bf16 v[28:31], v[124:127], v[194:197], 0
	v_mfma_f32_16x16x32_bf16 v[20:23], v[116:119], v[202:205], 0
	v_mfma_f32_16x16x32_bf16 v[12:15], v[124:127], v[202:205], 0
	v_mfma_f32_16x16x32_bf16 v[64:67], v[120:123], v[182:185], v[64:67]
	v_mfma_f32_16x16x32_bf16 v[60:63], v[128:131], v[182:185], v[60:63]
	v_mfma_f32_16x16x32_bf16 v[48:51], v[120:123], v[190:193], v[48:51]
	v_mfma_f32_16x16x32_bf16 v[44:47], v[128:131], v[190:193], v[44:47]
	v_mfma_f32_16x16x32_bf16 v[36:39], v[120:123], v[198:201], v[36:39]
	v_mfma_f32_16x16x32_bf16 v[28:31], v[128:131], v[198:201], v[28:31]
	v_mfma_f32_16x16x32_bf16 v[20:23], v[120:123], v[206:209], v[20:23]
	v_mfma_f32_16x16x32_bf16 v[12:15], v[128:131], v[206:209], v[12:15]
	s_setprio 0
	s_setprio 1
	v_mfma_f32_16x16x32_bf16 v[56:59], v[148:151], v[172:175], 0
	v_mfma_f32_16x16x32_bf16 v[52:55], v[156:159], v[172:175], 0
	v_mfma_f32_16x16x32_bf16 v[40:43], v[148:151], v[186:189], 0
	v_mfma_f32_16x16x32_bf16 v[32:35], v[156:159], v[186:189], 0
	v_mfma_f32_16x16x32_bf16 v[24:27], v[148:151], v[194:197], 0
	v_mfma_f32_16x16x32_bf16 v[16:19], v[156:159], v[194:197], 0
	v_mfma_f32_16x16x32_bf16 v[8:11], v[148:151], v[202:205], 0
	v_mfma_f32_16x16x32_bf16 v[4:7], v[156:159], v[202:205], 0
	v_mfma_f32_16x16x32_bf16 v[56:59], v[152:155], v[182:185], v[56:59]
	v_mfma_f32_16x16x32_bf16 v[52:55], v[160:163], v[182:185], v[52:55]
	v_mfma_f32_16x16x32_bf16 v[40:43], v[152:155], v[190:193], v[40:43]
	v_mfma_f32_16x16x32_bf16 v[32:35], v[160:163], v[190:193], v[32:35]
	v_mfma_f32_16x16x32_bf16 v[24:27], v[152:155], v[198:201], v[24:27]
	v_mfma_f32_16x16x32_bf16 v[16:19], v[160:163], v[198:201], v[16:19]
	v_mfma_f32_16x16x32_bf16 v[8:11], v[152:155], v[206:209], v[8:11]
	v_mfma_f32_16x16x32_bf16 v[4:7], v[160:163], v[206:209], v[4:7]
	s_setprio 0
	s_barrier
	s_add_i32 s57, 0, 0x18000
	s_add_i32 s58, 0, 0x1c000
	v_add_u32_e32 v128, s57, v179
	v_add_u32_e32 v160, s58, v179
	ds_read_b128 v[116:119], v128
	ds_read_b128 v[120:123], v128 offset:1024
	ds_read_b128 v[124:127], v128 offset:2048
	ds_read_b128 v[128:131], v128 offset:3072
	ds_read_b128 v[148:151], v160
	ds_read_b128 v[152:155], v160 offset:1024
	ds_read_b128 v[156:159], v160 offset:2048
	ds_read_b128 v[160:163], v160 offset:3072
	s_add_u32 s10, s22, 0xb0000
	s_addc_u32 s11, s23, 0
	s_mov_b32 m0, s42
	v_lshl_add_u64 v[216:217], s[10:11], 0, v[0:1]
	ds_read_b128 v[172:175], v181 offset:32768
	ds_read_b128 v[182:185], v181 offset:33792
	ds_read_b128 v[186:189], v181 offset:34816
	ds_read_b128 v[190:193], v181 offset:35840
	ds_read_b128 v[194:197], v181 offset:36864
	ds_read_b128 v[198:201], v181 offset:37888
	ds_read_b128 v[202:205], v181 offset:38912
	ds_read_b128 v[206:209], v181 offset:39936
	global_load_lds_dwordx4 v[216:217], off
	v_lshl_add_u64 v[216:217], s[10:11], 0, v[164:165]
	s_mov_b32 m0, s43
	s_nop 0
	global_load_lds_dwordx4 v[216:217], off
	s_waitcnt vmcnt(8)
	s_waitcnt lgkmcnt(0)
	s_barrier
	s_setprio 1
	s_waitcnt lgkmcnt(0)
	v_mfma_f32_16x16x32_bf16 v[144:147], v[116:119], v[172:175], v[144:147]
	v_mfma_f32_16x16x32_bf16 v[140:143], v[124:127], v[172:175], v[140:143]
	v_mfma_f32_16x16x32_bf16 v[112:115], v[116:119], v[186:189], v[112:115]
	v_mfma_f32_16x16x32_bf16 v[108:111], v[124:127], v[186:189], v[108:111]
	v_mfma_f32_16x16x32_bf16 v[100:103], v[116:119], v[194:197], v[100:103]
	v_mfma_f32_16x16x32_bf16 v[92:95], v[124:127], v[194:197], v[92:95]
	v_mfma_f32_16x16x32_bf16 v[84:87], v[116:119], v[202:205], v[84:87]
	v_mfma_f32_16x16x32_bf16 v[76:79], v[124:127], v[202:205], v[76:79]
	v_mfma_f32_16x16x32_bf16 v[144:147], v[120:123], v[182:185], v[144:147]
	v_mfma_f32_16x16x32_bf16 v[140:143], v[128:131], v[182:185], v[140:143]
	v_mfma_f32_16x16x32_bf16 v[112:115], v[120:123], v[190:193], v[112:115]
	v_mfma_f32_16x16x32_bf16 v[108:111], v[128:131], v[190:193], v[108:111]
	v_mfma_f32_16x16x32_bf16 v[100:103], v[120:123], v[198:201], v[100:103]
	v_mfma_f32_16x16x32_bf16 v[92:95], v[128:131], v[198:201], v[92:95]
	v_mfma_f32_16x16x32_bf16 v[84:87], v[120:123], v[206:209], v[84:87]
	v_mfma_f32_16x16x32_bf16 v[76:79], v[128:131], v[206:209], v[76:79]
	s_setprio 0
	s_setprio 1
	v_mfma_f32_16x16x32_bf16 v[136:139], v[148:151], v[172:175], v[136:139]
	v_mfma_f32_16x16x32_bf16 v[132:135], v[156:159], v[172:175], v[132:135]
	v_mfma_f32_16x16x32_bf16 v[104:107], v[148:151], v[186:189], v[104:107]
	v_mfma_f32_16x16x32_bf16 v[96:99], v[156:159], v[186:189], v[96:99]
	v_mfma_f32_16x16x32_bf16 v[88:91], v[148:151], v[194:197], v[88:91]
	v_mfma_f32_16x16x32_bf16 v[80:83], v[156:159], v[194:197], v[80:83]
	v_mfma_f32_16x16x32_bf16 v[72:75], v[148:151], v[202:205], v[72:75]
	v_mfma_f32_16x16x32_bf16 v[68:71], v[156:159], v[202:205], v[68:71]
	v_mfma_f32_16x16x32_bf16 v[136:139], v[152:155], v[182:185], v[136:139]
	v_mfma_f32_16x16x32_bf16 v[132:135], v[160:163], v[182:185], v[132:135]
	v_mfma_f32_16x16x32_bf16 v[104:107], v[152:155], v[190:193], v[104:107]
	v_mfma_f32_16x16x32_bf16 v[96:99], v[160:163], v[190:193], v[96:99]
	v_mfma_f32_16x16x32_bf16 v[88:91], v[152:155], v[198:201], v[88:91]
	v_mfma_f32_16x16x32_bf16 v[80:83], v[160:163], v[198:201], v[80:83]
	v_mfma_f32_16x16x32_bf16 v[72:75], v[152:155], v[206:209], v[72:75]
	v_mfma_f32_16x16x32_bf16 v[68:71], v[160:163], v[206:209], v[68:71]
	s_setprio 0
	s_barrier
	s_add_i32 s10, s57, s37
	v_lshl_add_u64 v[176:177], v[176:177], 0, s[28:29]
	s_mov_b32 m0, s10
	ds_read_b128 v[172:175], v181 offset:49152
	ds_read_b128 v[182:185], v181 offset:50176
	ds_read_b128 v[186:189], v181 offset:51200
	ds_read_b128 v[190:193], v181 offset:52224
	ds_read_b128 v[194:197], v181 offset:53248
	ds_read_b128 v[198:201], v181 offset:54272
	ds_read_b128 v[202:205], v181 offset:55296
	ds_read_b128 v[206:209], v181 offset:56320
	global_load_lds_dwordx4 v[176:177], off
	s_add_i32 m0, s10, 0x2000
	s_add_u32 s10, s20, 0xb0080
	v_lshl_add_u64 v[176:177], v[210:211], 0, s[28:29]
	s_addc_u32 s11, s21, 0
	s_add_i32 s20, s58, s37
	global_load_lds_dwordx4 v[176:177], off
	v_lshl_add_u64 v[176:177], s[10:11], 0, v[2:3]
	s_mov_b32 m0, s20
	s_nop 0
	global_load_lds_dwordx4 v[176:177], off
	v_lshl_add_u64 v[176:177], s[10:11], 0, v[166:167]
	s_add_i32 m0, s20, 0x2000
	s_nop 0
	global_load_lds_dwordx4 v[176:177], off
	v_lshl_add_u64 v[176:177], v[212:213], 0, s[28:29]
	s_mov_b32 m0, s45
	s_nop 0
	global_load_lds_dwordx4 v[176:177], off
	v_lshl_add_u64 v[176:177], v[214:215], 0, s[28:29]
	s_mov_b32 m0, s46
	s_nop 0
	global_load_lds_dwordx4 v[176:177], off
	s_waitcnt vmcnt(8)
	s_waitcnt lgkmcnt(0)
	s_barrier
	s_setprio 1
	s_waitcnt lgkmcnt(0)
	v_mfma_f32_16x16x32_bf16 v[64:67], v[116:119], v[172:175], v[64:67]
	v_mfma_f32_16x16x32_bf16 v[60:63], v[124:127], v[172:175], v[60:63]
	v_mfma_f32_16x16x32_bf16 v[48:51], v[116:119], v[186:189], v[48:51]
	v_mfma_f32_16x16x32_bf16 v[44:47], v[124:127], v[186:189], v[44:47]
	v_mfma_f32_16x16x32_bf16 v[36:39], v[116:119], v[194:197], v[36:39]
	v_mfma_f32_16x16x32_bf16 v[28:31], v[124:127], v[194:197], v[28:31]
	v_mfma_f32_16x16x32_bf16 v[20:23], v[116:119], v[202:205], v[20:23]
	v_mfma_f32_16x16x32_bf16 v[12:15], v[124:127], v[202:205], v[12:15]
	v_mfma_f32_16x16x32_bf16 v[64:67], v[120:123], v[182:185], v[64:67]
	v_mfma_f32_16x16x32_bf16 v[60:63], v[128:131], v[182:185], v[60:63]
	v_mfma_f32_16x16x32_bf16 v[48:51], v[120:123], v[190:193], v[48:51]
	v_mfma_f32_16x16x32_bf16 v[44:47], v[128:131], v[190:193], v[44:47]
	v_mfma_f32_16x16x32_bf16 v[36:39], v[120:123], v[198:201], v[36:39]
	v_mfma_f32_16x16x32_bf16 v[28:31], v[128:131], v[198:201], v[28:31]
	v_mfma_f32_16x16x32_bf16 v[20:23], v[120:123], v[206:209], v[20:23]
	v_mfma_f32_16x16x32_bf16 v[12:15], v[128:131], v[206:209], v[12:15]
	s_setprio 0
	s_setprio 1
	v_mfma_f32_16x16x32_bf16 v[56:59], v[148:151], v[172:175], v[56:59]
	v_mfma_f32_16x16x32_bf16 v[52:55], v[156:159], v[172:175], v[52:55]
	v_mfma_f32_16x16x32_bf16 v[40:43], v[148:151], v[186:189], v[40:43]
	v_mfma_f32_16x16x32_bf16 v[32:35], v[156:159], v[186:189], v[32:35]
	v_mfma_f32_16x16x32_bf16 v[24:27], v[148:151], v[194:197], v[24:27]
	v_mfma_f32_16x16x32_bf16 v[16:19], v[156:159], v[194:197], v[16:19]
	v_mfma_f32_16x16x32_bf16 v[8:11], v[148:151], v[202:205], v[8:11]
	v_mfma_f32_16x16x32_bf16 v[4:7], v[156:159], v[202:205], v[4:7]
	v_mfma_f32_16x16x32_bf16 v[56:59], v[152:155], v[182:185], v[56:59]
	v_mfma_f32_16x16x32_bf16 v[52:55], v[160:163], v[182:185], v[52:55]
	v_mfma_f32_16x16x32_bf16 v[40:43], v[152:155], v[190:193], v[40:43]
	v_mfma_f32_16x16x32_bf16 v[32:35], v[160:163], v[190:193], v[32:35]
	v_mfma_f32_16x16x32_bf16 v[24:27], v[152:155], v[198:201], v[24:27]
	v_mfma_f32_16x16x32_bf16 v[16:19], v[160:163], v[198:201], v[16:19]
	v_mfma_f32_16x16x32_bf16 v[8:11], v[152:155], v[206:209], v[8:11]
	v_mfma_f32_16x16x32_bf16 v[4:7], v[160:163], v[206:209], v[4:7]
	s_setprio 0
	s_barrier
	s_add_i32 s56, s56, 2
	s_add_u32 s54, s54, 0x100
	s_addc_u32 s55, s55, 0
	s_cmp_gt_u32 s56, 41
	s_mov_b64 s[10:11], s[18:19]
	s_cbranch_scc1 .Lmy_gx3
	.p2alignl 6, 3212836864

.LBB0_1329:
	s_ashr_i32 s17, s16, 31
	s_lshl_b64 s[18:19], s[16:17], 19
	s_add_u32 s18, s35, s18
	s_addc_u32 s19, s36, s19
	s_and_b64 s[20:21], s[38:39], exec
	s_cselect_b32 s13, s19, s23
	s_cselect_b32 s17, s18, s22
	s_ashr_i32 s15, s14, 31
	s_lshl_b64 s[20:21], s[14:15], 19
	s_add_u32 s20, s37, s20
	s_addc_u32 s21, s46, s21
	s_and_b64 s[40:41], s[38:39], exec
	s_cselect_b32 s15, s21, s27
	s_cselect_b32 s58, s20, s26
	s_add_u32 s59, s26, 0x100
	s_addc_u32 s60, s27, 0
	s_mov_b32 s61, -2
	s_add_u32 s26, s22, 0x100
	s_addc_u32 s27, s23, 0
	s_add_i32 s62, 0, 0x10000
	s_cmp_eq_u32 s61, 12
	s_cselect_b32 s43, s13, s27
	s_cselect_b32 s42, s17, s26
	v_add_u32_e32 v142, s62, v145
	s_cselect_b32 s41, s15, s60
	s_cselect_b32 s40, s58, s59
	s_add_i32 s63, 0, 0x14000
	ds_read_b128 v[148:151], v142
	ds_read_b128 v[152:155], v142 offset:1024
	ds_read_b128 v[156:159], v142 offset:2048
	ds_read_b128 v[160:163], v142 offset:3072
	v_add_u32_e32 v142, s63, v145
	ds_read_b128 v[164:167], v142
	ds_read_b128 v[168:171], v142 offset:1024
	ds_read_b128 v[172:175], v142 offset:2048
	ds_read_b128 v[176:179], v142 offset:3072
	v_lshl_add_u64 v[142:143], s[22:23], 0, v[140:141]
	s_add_i32 m0, s50, 0xc000
	ds_read_b128 v[180:183], v147
	ds_read_b128 v[184:187], v147 offset:1024
	ds_read_b128 v[188:191], v147 offset:2048
	ds_read_b128 v[192:195], v147 offset:3072
	ds_read_b128 v[196:199], v147 offset:4096
	ds_read_b128 v[200:203], v147 offset:5120
	ds_read_b128 v[204:207], v147 offset:6144
	ds_read_b128 v[208:211], v147 offset:7168
	global_load_lds_dwordx4 v[142:143], off
	v_lshl_add_u64 v[142:143], s[22:23], 0, v[138:139]
	s_add_i32 m0, s50, 0xe000
	s_nop 0
	global_load_lds_dwordx4 v[142:143], off
	s_waitcnt vmcnt(8)
	s_waitcnt lgkmcnt(0)
	s_barrier
	s_setprio 1
	s_waitcnt lgkmcnt(0)
	v_mfma_f32_16x16x32_bf16 v[96:99], v[148:151], v[180:183], 0
	v_mfma_f32_16x16x32_bf16 v[88:91], v[156:159], v[180:183], 0
	v_mfma_f32_16x16x32_bf16 v[80:83], v[148:151], v[188:191], 0
	v_mfma_f32_16x16x32_bf16 v[76:79], v[156:159], v[188:191], 0
	v_mfma_f32_16x16x32_bf16 v[72:75], v[148:151], v[196:199], 0
	v_mfma_f32_16x16x32_bf16 v[64:67], v[156:159], v[196:199], 0
	v_mfma_f32_16x16x32_bf16 v[56:59], v[148:151], v[204:207], 0
	v_mfma_f32_16x16x32_bf16 v[52:55], v[156:159], v[204:207], 0
	v_mfma_f32_16x16x32_bf16 v[96:99], v[152:155], v[184:187], v[96:99]
	v_mfma_f32_16x16x32_bf16 v[88:91], v[160:163], v[184:187], v[88:91]
	v_mfma_f32_16x16x32_bf16 v[80:83], v[152:155], v[192:195], v[80:83]
	v_mfma_f32_16x16x32_bf16 v[76:79], v[160:163], v[192:195], v[76:79]
	v_mfma_f32_16x16x32_bf16 v[72:75], v[152:155], v[200:203], v[72:75]
	v_mfma_f32_16x16x32_bf16 v[64:67], v[160:163], v[200:203], v[64:67]
	v_mfma_f32_16x16x32_bf16 v[56:59], v[152:155], v[208:211], v[56:59]
	v_mfma_f32_16x16x32_bf16 v[52:55], v[160:163], v[208:211], v[52:55]
	s_setprio 0
	s_setprio 1
	v_mfma_f32_16x16x32_bf16 v[128:131], v[164:167], v[180:183], 0
	v_mfma_f32_16x16x32_bf16 v[124:127], v[172:175], v[180:183], 0
	v_mfma_f32_16x16x32_bf16 v[120:123], v[164:167], v[188:191], 0
	v_mfma_f32_16x16x32_bf16 v[116:119], v[172:175], v[188:191], 0
	v_mfma_f32_16x16x32_bf16 v[112:115], v[164:167], v[196:199], 0
	v_mfma_f32_16x16x32_bf16 v[108:111], v[172:175], v[196:199], 0
	v_mfma_f32_16x16x32_bf16 v[104:107], v[164:167], v[204:207], 0
	v_mfma_f32_16x16x32_bf16 v[100:103], v[172:175], v[204:207], 0
	v_mfma_f32_16x16x32_bf16 v[128:131], v[168:171], v[184:187], v[128:131]
	v_mfma_f32_16x16x32_bf16 v[124:127], v[176:179], v[184:187], v[124:127]
	v_mfma_f32_16x16x32_bf16 v[120:123], v[168:171], v[192:195], v[120:123]
	v_mfma_f32_16x16x32_bf16 v[116:119], v[176:179], v[192:195], v[116:119]
	v_mfma_f32_16x16x32_bf16 v[112:115], v[168:171], v[200:203], v[112:115]
	v_mfma_f32_16x16x32_bf16 v[108:111], v[176:179], v[200:203], v[108:111]
	v_mfma_f32_16x16x32_bf16 v[104:107], v[168:171], v[208:211], v[104:107]
	v_mfma_f32_16x16x32_bf16 v[100:103], v[176:179], v[208:211], v[100:103]
	s_setprio 0
	s_barrier
	s_add_i32 s22, s62, s47
	v_lshl_add_u64 v[142:143], s[40:41], 0, v[2:3]
	s_mov_b32 m0, s22
	ds_read_b128 v[180:183], v147 offset:16384
	ds_read_b128 v[184:187], v147 offset:17408
	ds_read_b128 v[188:191], v147 offset:18432
	ds_read_b128 v[192:195], v147 offset:19456
	ds_read_b128 v[196:199], v147 offset:20480
	ds_read_b128 v[200:203], v147 offset:21504
	ds_read_b128 v[204:207], v147 offset:22528
	ds_read_b128 v[208:211], v147 offset:23552
	global_load_lds_dwordx4 v[142:143], off
	s_add_i32 m0, s22, 0x2000
	s_add_u32 s22, s40, 0x40000
	v_lshl_add_u64 v[212:213], s[40:41], 0, v[134:135]
	s_addc_u32 s23, s41, 0
	s_add_i32 s62, s63, s47
	global_load_lds_dwordx4 v[212:213], off
	v_lshl_add_u64 v[214:215], s[22:23], 0, v[2:3]
	s_mov_b32 m0, s62
	v_lshl_add_u64 v[216:217], s[42:43], 0, v[132:133]
	global_load_lds_dwordx4 v[214:215], off
	v_lshl_add_u64 v[214:215], s[22:23], 0, v[134:135]
	s_add_i32 m0, s62, 0x2000
	s_nop 0
	global_load_lds_dwordx4 v[214:215], off
	v_lshl_add_u64 v[214:215], s[42:43], 0, v[0:1]
	s_mov_b32 m0, s50
	s_nop 0
	global_load_lds_dwordx4 v[214:215], off
	s_mov_b32 m0, s51
	s_nop 0
	global_load_lds_dwordx4 v[216:217], off
	s_waitcnt vmcnt(8)
	s_waitcnt lgkmcnt(0)
	s_barrier
	s_setprio 1
	s_waitcnt lgkmcnt(0)
	v_mfma_f32_16x16x32_bf16 v[36:39], v[148:151], v[180:183], 0
	v_mfma_f32_16x16x32_bf16 v[28:31], v[156:159], v[180:183], 0
	v_mfma_f32_16x16x32_bf16 v[24:27], v[148:151], v[188:191], 0
	v_mfma_f32_16x16x32_bf16 v[20:23], v[156:159], v[188:191], 0
	v_mfma_f32_16x16x32_bf16 v[16:19], v[148:151], v[196:199], 0
	v_mfma_f32_16x16x32_bf16 v[12:15], v[156:159], v[196:199], 0
	v_mfma_f32_16x16x32_bf16 v[8:11], v[148:151], v[204:207], 0
	v_mfma_f32_16x16x32_bf16 v[4:7], v[156:159], v[204:207], 0
	v_mfma_f32_16x16x32_bf16 v[36:39], v[152:155], v[184:187], v[36:39]
	v_mfma_f32_16x16x32_bf16 v[28:31], v[160:163], v[184:187], v[28:31]
	v_mfma_f32_16x16x32_bf16 v[24:27], v[152:155], v[192:195], v[24:27]
	v_mfma_f32_16x16x32_bf16 v[20:23], v[160:163], v[192:195], v[20:23]
	v_mfma_f32_16x16x32_bf16 v[16:19], v[152:155], v[200:203], v[16:19]
	v_mfma_f32_16x16x32_bf16 v[12:15], v[160:163], v[200:203], v[12:15]
	v_mfma_f32_16x16x32_bf16 v[8:11], v[152:155], v[208:211], v[8:11]
	v_mfma_f32_16x16x32_bf16 v[4:7], v[160:163], v[208:211], v[4:7]
	s_setprio 0
	s_setprio 1
	v_mfma_f32_16x16x32_bf16 v[92:95], v[164:167], v[180:183], 0
	v_mfma_f32_16x16x32_bf16 v[84:87], v[172:175], v[180:183], 0
	v_mfma_f32_16x16x32_bf16 v[68:71], v[164:167], v[188:191], 0
	v_mfma_f32_16x16x32_bf16 v[60:63], v[172:175], v[188:191], 0
	v_mfma_f32_16x16x32_bf16 v[48:51], v[164:167], v[196:199], 0
	v_mfma_f32_16x16x32_bf16 v[44:47], v[172:175], v[196:199], 0
	v_mfma_f32_16x16x32_bf16 v[40:43], v[164:167], v[204:207], 0
	v_mfma_f32_16x16x32_bf16 v[32:35], v[172:175], v[204:207], 0
	v_mfma_f32_16x16x32_bf16 v[92:95], v[168:171], v[184:187], v[92:95]
	v_mfma_f32_16x16x32_bf16 v[84:87], v[176:179], v[184:187], v[84:87]
	v_mfma_f32_16x16x32_bf16 v[68:71], v[168:171], v[192:195], v[68:71]
	v_mfma_f32_16x16x32_bf16 v[60:63], v[176:179], v[192:195], v[60:63]
	v_mfma_f32_16x16x32_bf16 v[48:51], v[168:171], v[200:203], v[48:51]
	v_mfma_f32_16x16x32_bf16 v[44:47], v[176:179], v[200:203], v[44:47]
	v_mfma_f32_16x16x32_bf16 v[40:43], v[168:171], v[208:211], v[40:43]
	v_mfma_f32_16x16x32_bf16 v[32:35], v[176:179], v[208:211], v[32:35]
	s_setprio 0
	s_barrier
	s_add_i32 s62, 0, 0x18000
	s_add_i32 s63, 0, 0x1c000
	v_add_u32_e32 v160, s62, v145
	v_add_u32_e32 v176, s63, v145
	ds_read_b128 v[148:151], v160
	ds_read_b128 v[152:155], v160 offset:1024
	ds_read_b128 v[156:159], v160 offset:2048
	ds_read_b128 v[160:163], v160 offset:3072
	ds_read_b128 v[164:167], v176
	ds_read_b128 v[168:171], v176 offset:1024
	ds_read_b128 v[172:175], v176 offset:2048
	ds_read_b128 v[176:179], v176 offset:3072
	s_add_u32 s22, s42, 0x40000
	s_addc_u32 s23, s43, 0
	s_mov_b32 m0, s52
	v_lshl_add_u64 v[218:219], s[22:23], 0, v[0:1]
	ds_read_b128 v[180:183], v147 offset:32768
	ds_read_b128 v[184:187], v147 offset:33792
	ds_read_b128 v[188:191], v147 offset:34816
	ds_read_b128 v[192:195], v147 offset:35840
	ds_read_b128 v[196:199], v147 offset:36864
	ds_read_b128 v[200:203], v147 offset:37888
	ds_read_b128 v[204:207], v147 offset:38912
	ds_read_b128 v[208:211], v147 offset:39936
	global_load_lds_dwordx4 v[218:219], off
	v_lshl_add_u64 v[218:219], s[22:23], 0, v[132:133]
	s_mov_b32 m0, s53
	s_nop 0
	global_load_lds_dwordx4 v[218:219], off
	s_waitcnt vmcnt(8)
	s_waitcnt lgkmcnt(0)
	s_barrier
	s_setprio 1
	s_waitcnt lgkmcnt(0)
	v_mfma_f32_16x16x32_bf16 v[96:99], v[148:151], v[180:183], v[96:99]
	v_mfma_f32_16x16x32_bf16 v[88:91], v[156:159], v[180:183], v[88:91]
	v_mfma_f32_16x16x32_bf16 v[80:83], v[148:151], v[188:191], v[80:83]
	v_mfma_f32_16x16x32_bf16 v[76:79], v[156:159], v[188:191], v[76:79]
	v_mfma_f32_16x16x32_bf16 v[72:75], v[148:151], v[196:199], v[72:75]
	v_mfma_f32_16x16x32_bf16 v[64:67], v[156:159], v[196:199], v[64:67]
	v_mfma_f32_16x16x32_bf16 v[56:59], v[148:151], v[204:207], v[56:59]
	v_mfma_f32_16x16x32_bf16 v[52:55], v[156:159], v[204:207], v[52:55]
	v_mfma_f32_16x16x32_bf16 v[96:99], v[152:155], v[184:187], v[96:99]
	v_mfma_f32_16x16x32_bf16 v[88:91], v[160:163], v[184:187], v[88:91]
	v_mfma_f32_16x16x32_bf16 v[80:83], v[152:155], v[192:195], v[80:83]
	v_mfma_f32_16x16x32_bf16 v[76:79], v[160:163], v[192:195], v[76:79]
	v_mfma_f32_16x16x32_bf16 v[72:75], v[152:155], v[200:203], v[72:75]
	v_mfma_f32_16x16x32_bf16 v[64:67], v[160:163], v[200:203], v[64:67]
	v_mfma_f32_16x16x32_bf16 v[56:59], v[152:155], v[208:211], v[56:59]
	v_mfma_f32_16x16x32_bf16 v[52:55], v[160:163], v[208:211], v[52:55]
	s_setprio 0
	s_setprio 1
	v_mfma_f32_16x16x32_bf16 v[128:131], v[164:167], v[180:183], v[128:131]
	v_mfma_f32_16x16x32_bf16 v[124:127], v[172:175], v[180:183], v[124:127]
	v_mfma_f32_16x16x32_bf16 v[120:123], v[164:167], v[188:191], v[120:123]
	v_mfma_f32_16x16x32_bf16 v[116:119], v[172:175], v[188:191], v[116:119]
	v_mfma_f32_16x16x32_bf16 v[112:115], v[164:167], v[196:199], v[112:115]
	v_mfma_f32_16x16x32_bf16 v[108:111], v[172:175], v[196:199], v[108:111]
	v_mfma_f32_16x16x32_bf16 v[104:107], v[164:167], v[204:207], v[104:107]
	v_mfma_f32_16x16x32_bf16 v[100:103], v[172:175], v[204:207], v[100:103]
	v_mfma_f32_16x16x32_bf16 v[128:131], v[168:171], v[184:187], v[128:131]
	v_mfma_f32_16x16x32_bf16 v[124:127], v[176:179], v[184:187], v[124:127]
	v_mfma_f32_16x16x32_bf16 v[120:123], v[168:171], v[192:195], v[120:123]
	v_mfma_f32_16x16x32_bf16 v[116:119], v[176:179], v[192:195], v[116:119]
	v_mfma_f32_16x16x32_bf16 v[112:115], v[168:171], v[200:203], v[112:115]
	v_mfma_f32_16x16x32_bf16 v[108:111], v[176:179], v[200:203], v[108:111]
	v_mfma_f32_16x16x32_bf16 v[104:107], v[168:171], v[208:211], v[104:107]
	v_mfma_f32_16x16x32_bf16 v[100:103], v[176:179], v[208:211], v[100:103]
	s_setprio 0
	s_barrier
	s_add_i32 s22, s62, s47
	v_lshl_add_u64 v[142:143], v[142:143], 0, s[28:29]
	s_mov_b32 m0, s22
	ds_read_b128 v[180:183], v147 offset:49152
	ds_read_b128 v[184:187], v147 offset:50176
	ds_read_b128 v[188:191], v147 offset:51200
	ds_read_b128 v[192:195], v147 offset:52224
	ds_read_b128 v[196:199], v147 offset:53248
	ds_read_b128 v[200:203], v147 offset:54272
	ds_read_b128 v[204:207], v147 offset:55296
	ds_read_b128 v[208:211], v147 offset:56320
	global_load_lds_dwordx4 v[142:143], off
	s_add_i32 m0, s22, 0x2000
	s_add_u32 s22, s40, 0x40080
	v_lshl_add_u64 v[142:143], v[212:213], 0, s[28:29]
	s_addc_u32 s23, s41, 0
	s_add_i32 s40, s63, s47
	global_load_lds_dwordx4 v[142:143], off
	v_lshl_add_u64 v[142:143], s[22:23], 0, v[2:3]
	s_mov_b32 m0, s40
	s_nop 0
	global_load_lds_dwordx4 v[142:143], off
	v_lshl_add_u64 v[142:143], s[22:23], 0, v[134:135]
	s_add_i32 m0, s40, 0x2000
	s_nop 0
	global_load_lds_dwordx4 v[142:143], off
	v_lshl_add_u64 v[142:143], v[214:215], 0, s[28:29]
	s_mov_b32 m0, s54
	s_nop 0
	global_load_lds_dwordx4 v[142:143], off
	v_lshl_add_u64 v[142:143], v[216:217], 0, s[28:29]
	s_mov_b32 m0, s55
	s_nop 0
	global_load_lds_dwordx4 v[142:143], off
	s_waitcnt vmcnt(8)
	s_waitcnt lgkmcnt(0)
	s_barrier
	s_setprio 1
	s_waitcnt lgkmcnt(0)
	v_mfma_f32_16x16x32_bf16 v[36:39], v[148:151], v[180:183], v[36:39]
	v_mfma_f32_16x16x32_bf16 v[28:31], v[156:159], v[180:183], v[28:31]
	v_mfma_f32_16x16x32_bf16 v[24:27], v[148:151], v[188:191], v[24:27]
	v_mfma_f32_16x16x32_bf16 v[20:23], v[156:159], v[188:191], v[20:23]
	v_mfma_f32_16x16x32_bf16 v[16:19], v[148:151], v[196:199], v[16:19]
	v_mfma_f32_16x16x32_bf16 v[12:15], v[156:159], v[196:199], v[12:15]
	v_mfma_f32_16x16x32_bf16 v[8:11], v[148:151], v[204:207], v[8:11]
	v_mfma_f32_16x16x32_bf16 v[4:7], v[156:159], v[204:207], v[4:7]
	v_mfma_f32_16x16x32_bf16 v[36:39], v[152:155], v[184:187], v[36:39]
	v_mfma_f32_16x16x32_bf16 v[28:31], v[160:163], v[184:187], v[28:31]
	v_mfma_f32_16x16x32_bf16 v[24:27], v[152:155], v[192:195], v[24:27]
	v_mfma_f32_16x16x32_bf16 v[20:23], v[160:163], v[192:195], v[20:23]
	v_mfma_f32_16x16x32_bf16 v[16:19], v[152:155], v[200:203], v[16:19]
	v_mfma_f32_16x16x32_bf16 v[12:15], v[160:163], v[200:203], v[12:15]
	v_mfma_f32_16x16x32_bf16 v[8:11], v[152:155], v[208:211], v[8:11]
	v_mfma_f32_16x16x32_bf16 v[4:7], v[160:163], v[208:211], v[4:7]
	s_setprio 0
	s_setprio 1
	v_mfma_f32_16x16x32_bf16 v[92:95], v[164:167], v[180:183], v[92:95]
	v_mfma_f32_16x16x32_bf16 v[84:87], v[172:175], v[180:183], v[84:87]
	v_mfma_f32_16x16x32_bf16 v[68:71], v[164:167], v[188:191], v[68:71]
	v_mfma_f32_16x16x32_bf16 v[60:63], v[172:175], v[188:191], v[60:63]
	v_mfma_f32_16x16x32_bf16 v[48:51], v[164:167], v[196:199], v[48:51]
	v_mfma_f32_16x16x32_bf16 v[44:47], v[172:175], v[196:199], v[44:47]
	v_mfma_f32_16x16x32_bf16 v[40:43], v[164:167], v[204:207], v[40:43]
	v_mfma_f32_16x16x32_bf16 v[32:35], v[172:175], v[204:207], v[32:35]
	v_mfma_f32_16x16x32_bf16 v[92:95], v[168:171], v[184:187], v[92:95]
	v_mfma_f32_16x16x32_bf16 v[84:87], v[176:179], v[184:187], v[84:87]
	v_mfma_f32_16x16x32_bf16 v[68:71], v[168:171], v[192:195], v[68:71]
	v_mfma_f32_16x16x32_bf16 v[60:63], v[176:179], v[192:195], v[60:63]
	v_mfma_f32_16x16x32_bf16 v[48:51], v[168:171], v[200:203], v[48:51]
	v_mfma_f32_16x16x32_bf16 v[44:47], v[176:179], v[200:203], v[44:47]
	v_mfma_f32_16x16x32_bf16 v[40:43], v[168:171], v[208:211], v[40:43]
	v_mfma_f32_16x16x32_bf16 v[32:35], v[176:179], v[208:211], v[32:35]
	s_setprio 0
	s_barrier
	s_add_i32 s61, s61, 2
	s_add_u32 s59, s59, 0x100
	s_addc_u32 s60, s60, 0
	s_cmp_gt_u32 s61, 13
	s_mov_b64 s[22:23], s[26:27]
	s_cbranch_scc1 .Lmy_gx4
	.p2alignl 6, 3212836864

.LBB0_1890:
	s_ashr_i32 s15, s14, 31
	s_lshl_b64 s[16:17], s[14:15], 19
	s_add_u32 s13, s36, s16
	s_addc_u32 s15, s37, s17
	s_and_b64 s[16:17], s[38:39], exec
	s_cselect_b32 s17, s15, s21
	s_cselect_b32 s16, s13, s20
	s_ashr_i32 s13, s12, 31
	s_lshl_b64 s[18:19], s[12:13], 19
	s_add_u32 s13, s42, s18
	s_addc_u32 s15, s43, s19
	s_and_b64 s[18:19], s[38:39], exec
	s_cselect_b32 s19, s15, s23
	s_cselect_b32 s18, s13, s22
	s_add_u32 s13, s22, 0x100
	v_mov_b32_e32 v218, 0x3ecc95a3
	s_addc_u32 s15, s23, 0
	s_mov_b32 s56, -2
	s_add_u32 s22, s20, 0x100
	s_addc_u32 s23, s21, 0
	s_add_i32 s57, 0, 0x10000
	s_cmp_eq_u32 s56, 12
	s_cselect_b32 s41, s17, s23
	s_cselect_b32 s40, s16, s22
	s_cselect_b32 s27, s19, s15
	s_cselect_b32 s26, s18, s13
	s_add_i32 s58, 0, 0x14000
	v_add_u32_e32 v128, s57, v179
	v_add_u32_e32 v160, s58, v179
	ds_read_b128 v[116:119], v128
	ds_read_b128 v[120:123], v128 offset:1024
	ds_read_b128 v[124:127], v128 offset:2048
	ds_read_b128 v[128:131], v128 offset:3072
	ds_read_b128 v[148:151], v160
	ds_read_b128 v[152:155], v160 offset:1024
	ds_read_b128 v[156:159], v160 offset:2048
	ds_read_b128 v[160:163], v160 offset:3072
	v_lshl_add_u64 v[176:177], s[20:21], 0, v[170:171]
	s_add_i32 m0, s47, 0xc000
	ds_read_b128 v[172:175], v181
	ds_read_b128 v[182:185], v181 offset:1024
	ds_read_b128 v[186:189], v181 offset:2048
	ds_read_b128 v[190:193], v181 offset:3072
	ds_read_b128 v[194:197], v181 offset:4096
	ds_read_b128 v[198:201], v181 offset:5120
	ds_read_b128 v[202:205], v181 offset:6144
	ds_read_b128 v[206:209], v181 offset:7168
	global_load_lds_dwordx4 v[176:177], off
	v_lshl_add_u64 v[176:177], s[20:21], 0, v[168:169]
	s_add_i32 m0, s47, 0xe000
	s_nop 0
	global_load_lds_dwordx4 v[176:177], off
	s_waitcnt vmcnt(8)
	s_waitcnt lgkmcnt(0)
	s_barrier
	s_setprio 1
	s_waitcnt lgkmcnt(0)
	v_mfma_f32_16x16x32_bf16 v[144:147], v[116:119], v[172:175], 0
	v_mfma_f32_16x16x32_bf16 v[140:143], v[124:127], v[172:175], 0
	v_mfma_f32_16x16x32_bf16 v[112:115], v[116:119], v[186:189], 0
	v_mfma_f32_16x16x32_bf16 v[108:111], v[124:127], v[186:189], 0
	v_mfma_f32_16x16x32_bf16 v[100:103], v[116:119], v[194:197], 0
	v_mfma_f32_16x16x32_bf16 v[92:95], v[124:127], v[194:197], 0
	v_mfma_f32_16x16x32_bf16 v[84:87], v[116:119], v[202:205], 0
	v_mfma_f32_16x16x32_bf16 v[76:79], v[124:127], v[202:205], 0
	v_mfma_f32_16x16x32_bf16 v[144:147], v[120:123], v[182:185], v[144:147]
	v_mfma_f32_16x16x32_bf16 v[140:143], v[128:131], v[182:185], v[140:143]
	v_mfma_f32_16x16x32_bf16 v[112:115], v[120:123], v[190:193], v[112:115]
	v_mfma_f32_16x16x32_bf16 v[108:111], v[128:131], v[190:193], v[108:111]
	v_mfma_f32_16x16x32_bf16 v[100:103], v[120:123], v[198:201], v[100:103]
	v_mfma_f32_16x16x32_bf16 v[92:95], v[128:131], v[198:201], v[92:95]
	v_mfma_f32_16x16x32_bf16 v[84:87], v[120:123], v[206:209], v[84:87]
	v_mfma_f32_16x16x32_bf16 v[76:79], v[128:131], v[206:209], v[76:79]
	s_setprio 0
	s_setprio 1
	v_mfma_f32_16x16x32_bf16 v[136:139], v[148:151], v[172:175], 0
	v_mfma_f32_16x16x32_bf16 v[132:135], v[156:159], v[172:175], 0
	v_mfma_f32_16x16x32_bf16 v[104:107], v[148:151], v[186:189], 0
	v_mfma_f32_16x16x32_bf16 v[96:99], v[156:159], v[186:189], 0
	v_mfma_f32_16x16x32_bf16 v[88:91], v[148:151], v[194:197], 0
	v_mfma_f32_16x16x32_bf16 v[80:83], v[156:159], v[194:197], 0
	v_mfma_f32_16x16x32_bf16 v[72:75], v[148:151], v[202:205], 0
	v_mfma_f32_16x16x32_bf16 v[68:71], v[156:159], v[202:205], 0
	v_mfma_f32_16x16x32_bf16 v[136:139], v[152:155], v[182:185], v[136:139]
	v_mfma_f32_16x16x32_bf16 v[132:135], v[160:163], v[182:185], v[132:135]
	v_mfma_f32_16x16x32_bf16 v[104:107], v[152:155], v[190:193], v[104:107]
	v_mfma_f32_16x16x32_bf16 v[96:99], v[160:163], v[190:193], v[96:99]
	v_mfma_f32_16x16x32_bf16 v[88:91], v[152:155], v[198:201], v[88:91]
	v_mfma_f32_16x16x32_bf16 v[80:83], v[160:163], v[198:201], v[80:83]
	v_mfma_f32_16x16x32_bf16 v[72:75], v[152:155], v[206:209], v[72:75]
	v_mfma_f32_16x16x32_bf16 v[68:71], v[160:163], v[206:209], v[68:71]
	s_setprio 0
	s_barrier
	s_add_i32 s20, s57, s46
	v_lshl_add_u64 v[176:177], s[26:27], 0, v[2:3]
	s_mov_b32 m0, s20
	ds_read_b128 v[172:175], v181 offset:16384
	ds_read_b128 v[182:185], v181 offset:17408
	ds_read_b128 v[186:189], v181 offset:18432
	ds_read_b128 v[190:193], v181 offset:19456
	ds_read_b128 v[194:197], v181 offset:20480
	ds_read_b128 v[198:201], v181 offset:21504
	ds_read_b128 v[202:205], v181 offset:22528
	ds_read_b128 v[206:209], v181 offset:23552
	global_load_lds_dwordx4 v[176:177], off
	s_add_i32 m0, s20, 0x2000
	s_add_u32 s20, s26, 0x40000
	v_lshl_add_u64 v[210:211], s[26:27], 0, v[166:167]
	s_addc_u32 s21, s27, 0
	s_add_i32 s57, s58, s46
	global_load_lds_dwordx4 v[210:211], off
	v_lshl_add_u64 v[212:213], s[20:21], 0, v[2:3]
	s_mov_b32 m0, s57
	v_lshl_add_u64 v[214:215], s[40:41], 0, v[164:165]
	global_load_lds_dwordx4 v[212:213], off
	v_lshl_add_u64 v[212:213], s[20:21], 0, v[166:167]
	s_add_i32 m0, s57, 0x2000
	s_nop 0
	global_load_lds_dwordx4 v[212:213], off
	v_lshl_add_u64 v[212:213], s[40:41], 0, v[0:1]
	s_mov_b32 m0, s47
	s_nop 0
	global_load_lds_dwordx4 v[212:213], off
	s_mov_b32 m0, s48
	s_nop 0
	global_load_lds_dwordx4 v[214:215], off
	s_waitcnt vmcnt(8)
	s_waitcnt lgkmcnt(0)
	s_barrier
	s_setprio 1
	s_waitcnt lgkmcnt(0)
	v_mfma_f32_16x16x32_bf16 v[64:67], v[116:119], v[172:175], 0
	v_mfma_f32_16x16x32_bf16 v[60:63], v[124:127], v[172:175], 0
	v_mfma_f32_16x16x32_bf16 v[48:51], v[116:119], v[186:189], 0
	v_mfma_f32_16x16x32_bf16 v[44:47], v[124:127], v[186:189], 0
	v_mfma_f32_16x16x32_bf16 v[36:39], v[116:119], v[194:197], 0
	v_mfma_f32_16x16x32_bf16 v[28:31], v[124:127], v[194:197], 0
	v_mfma_f32_16x16x32_bf16 v[20:23], v[116:119], v[202:205], 0
	v_mfma_f32_16x16x32_bf16 v[12:15], v[124:127], v[202:205], 0
	v_mfma_f32_16x16x32_bf16 v[64:67], v[120:123], v[182:185], v[64:67]
	v_mfma_f32_16x16x32_bf16 v[60:63], v[128:131], v[182:185], v[60:63]
	v_mfma_f32_16x16x32_bf16 v[48:51], v[120:123], v[190:193], v[48:51]
	v_mfma_f32_16x16x32_bf16 v[44:47], v[128:131], v[190:193], v[44:47]
	v_mfma_f32_16x16x32_bf16 v[36:39], v[120:123], v[198:201], v[36:39]
	v_mfma_f32_16x16x32_bf16 v[28:31], v[128:131], v[198:201], v[28:31]
	v_mfma_f32_16x16x32_bf16 v[20:23], v[120:123], v[206:209], v[20:23]
	v_mfma_f32_16x16x32_bf16 v[12:15], v[128:131], v[206:209], v[12:15]
	s_setprio 0
	s_setprio 1
	v_mfma_f32_16x16x32_bf16 v[56:59], v[148:151], v[172:175], 0
	v_mfma_f32_16x16x32_bf16 v[52:55], v[156:159], v[172:175], 0
	v_mfma_f32_16x16x32_bf16 v[40:43], v[148:151], v[186:189], 0
	v_mfma_f32_16x16x32_bf16 v[32:35], v[156:159], v[186:189], 0
	v_mfma_f32_16x16x32_bf16 v[24:27], v[148:151], v[194:197], 0
	v_mfma_f32_16x16x32_bf16 v[16:19], v[156:159], v[194:197], 0
	v_mfma_f32_16x16x32_bf16 v[8:11], v[148:151], v[202:205], 0
	v_mfma_f32_16x16x32_bf16 v[4:7], v[156:159], v[202:205], 0
	v_mfma_f32_16x16x32_bf16 v[56:59], v[152:155], v[182:185], v[56:59]
	v_mfma_f32_16x16x32_bf16 v[52:55], v[160:163], v[182:185], v[52:55]
	v_mfma_f32_16x16x32_bf16 v[40:43], v[152:155], v[190:193], v[40:43]
	v_mfma_f32_16x16x32_bf16 v[32:35], v[160:163], v[190:193], v[32:35]
	v_mfma_f32_16x16x32_bf16 v[24:27], v[152:155], v[198:201], v[24:27]
	v_mfma_f32_16x16x32_bf16 v[16:19], v[160:163], v[198:201], v[16:19]
	v_mfma_f32_16x16x32_bf16 v[8:11], v[152:155], v[206:209], v[8:11]
	v_mfma_f32_16x16x32_bf16 v[4:7], v[160:163], v[206:209], v[4:7]
	s_setprio 0
	s_barrier
	s_add_i32 s57, 0, 0x18000
	s_add_i32 s58, 0, 0x1c000
	v_add_u32_e32 v128, s57, v179
	v_add_u32_e32 v160, s58, v179
	ds_read_b128 v[116:119], v128
	ds_read_b128 v[120:123], v128 offset:1024
	ds_read_b128 v[124:127], v128 offset:2048
	ds_read_b128 v[128:131], v128 offset:3072
	ds_read_b128 v[148:151], v160
	ds_read_b128 v[152:155], v160 offset:1024
	ds_read_b128 v[156:159], v160 offset:2048
	ds_read_b128 v[160:163], v160 offset:3072
	s_add_u32 s20, s40, 0x40000
	s_addc_u32 s21, s41, 0
	s_mov_b32 m0, s49
	v_lshl_add_u64 v[216:217], s[20:21], 0, v[0:1]
	ds_read_b128 v[172:175], v181 offset:32768
	ds_read_b128 v[182:185], v181 offset:33792
	ds_read_b128 v[186:189], v181 offset:34816
	ds_read_b128 v[190:193], v181 offset:35840
	ds_read_b128 v[194:197], v181 offset:36864
	ds_read_b128 v[198:201], v181 offset:37888
	ds_read_b128 v[202:205], v181 offset:38912
	ds_read_b128 v[206:209], v181 offset:39936
	global_load_lds_dwordx4 v[216:217], off
	v_lshl_add_u64 v[216:217], s[20:21], 0, v[164:165]
	s_mov_b32 m0, s50
	s_nop 0
	global_load_lds_dwordx4 v[216:217], off
	s_waitcnt vmcnt(8)
	s_waitcnt lgkmcnt(0)
	s_barrier
	s_setprio 1
	s_waitcnt lgkmcnt(0)
	v_mfma_f32_16x16x32_bf16 v[144:147], v[116:119], v[172:175], v[144:147]
	v_mfma_f32_16x16x32_bf16 v[140:143], v[124:127], v[172:175], v[140:143]
	v_mfma_f32_16x16x32_bf16 v[112:115], v[116:119], v[186:189], v[112:115]
	v_mfma_f32_16x16x32_bf16 v[108:111], v[124:127], v[186:189], v[108:111]
	v_mfma_f32_16x16x32_bf16 v[100:103], v[116:119], v[194:197], v[100:103]
	v_mfma_f32_16x16x32_bf16 v[92:95], v[124:127], v[194:197], v[92:95]
	v_mfma_f32_16x16x32_bf16 v[84:87], v[116:119], v[202:205], v[84:87]
	v_mfma_f32_16x16x32_bf16 v[76:79], v[124:127], v[202:205], v[76:79]
	v_mfma_f32_16x16x32_bf16 v[144:147], v[120:123], v[182:185], v[144:147]
	v_mfma_f32_16x16x32_bf16 v[140:143], v[128:131], v[182:185], v[140:143]
	v_mfma_f32_16x16x32_bf16 v[112:115], v[120:123], v[190:193], v[112:115]
	v_mfma_f32_16x16x32_bf16 v[108:111], v[128:131], v[190:193], v[108:111]
	v_mfma_f32_16x16x32_bf16 v[100:103], v[120:123], v[198:201], v[100:103]
	v_mfma_f32_16x16x32_bf16 v[92:95], v[128:131], v[198:201], v[92:95]
	v_mfma_f32_16x16x32_bf16 v[84:87], v[120:123], v[206:209], v[84:87]
	v_mfma_f32_16x16x32_bf16 v[76:79], v[128:131], v[206:209], v[76:79]
	s_setprio 0
	s_setprio 1
	v_mfma_f32_16x16x32_bf16 v[136:139], v[148:151], v[172:175], v[136:139]
	v_mfma_f32_16x16x32_bf16 v[132:135], v[156:159], v[172:175], v[132:135]
	v_mfma_f32_16x16x32_bf16 v[104:107], v[148:151], v[186:189], v[104:107]
	v_mfma_f32_16x16x32_bf16 v[96:99], v[156:159], v[186:189], v[96:99]
	v_mfma_f32_16x16x32_bf16 v[88:91], v[148:151], v[194:197], v[88:91]
	v_mfma_f32_16x16x32_bf16 v[80:83], v[156:159], v[194:197], v[80:83]
	v_mfma_f32_16x16x32_bf16 v[72:75], v[148:151], v[202:205], v[72:75]
	v_mfma_f32_16x16x32_bf16 v[68:71], v[156:159], v[202:205], v[68:71]
	v_mfma_f32_16x16x32_bf16 v[136:139], v[152:155], v[182:185], v[136:139]
	v_mfma_f32_16x16x32_bf16 v[132:135], v[160:163], v[182:185], v[132:135]
	v_mfma_f32_16x16x32_bf16 v[104:107], v[152:155], v[190:193], v[104:107]
	v_mfma_f32_16x16x32_bf16 v[96:99], v[160:163], v[190:193], v[96:99]
	v_mfma_f32_16x16x32_bf16 v[88:91], v[152:155], v[198:201], v[88:91]
	v_mfma_f32_16x16x32_bf16 v[80:83], v[160:163], v[198:201], v[80:83]
	v_mfma_f32_16x16x32_bf16 v[72:75], v[152:155], v[206:209], v[72:75]
	v_mfma_f32_16x16x32_bf16 v[68:71], v[160:163], v[206:209], v[68:71]
	s_setprio 0
	s_barrier
	s_add_i32 s20, s57, s46
	v_lshl_add_u64 v[176:177], v[176:177], 0, s[28:29]
	s_mov_b32 m0, s20
	ds_read_b128 v[172:175], v181 offset:49152
	ds_read_b128 v[182:185], v181 offset:50176
	ds_read_b128 v[186:189], v181 offset:51200
	ds_read_b128 v[190:193], v181 offset:52224
	ds_read_b128 v[194:197], v181 offset:53248
	ds_read_b128 v[198:201], v181 offset:54272
	ds_read_b128 v[202:205], v181 offset:55296
	ds_read_b128 v[206:209], v181 offset:56320
	global_load_lds_dwordx4 v[176:177], off
	s_add_i32 m0, s20, 0x2000
	s_add_u32 s20, s26, 0x40080
	v_lshl_add_u64 v[176:177], v[210:211], 0, s[28:29]
	s_addc_u32 s21, s27, 0
	s_add_i32 s26, s58, s46
	global_load_lds_dwordx4 v[176:177], off
	v_lshl_add_u64 v[176:177], s[20:21], 0, v[2:3]
	s_mov_b32 m0, s26
	s_nop 0
	global_load_lds_dwordx4 v[176:177], off
	v_lshl_add_u64 v[176:177], s[20:21], 0, v[166:167]
	s_add_i32 m0, s26, 0x2000
	s_nop 0
	global_load_lds_dwordx4 v[176:177], off
	v_lshl_add_u64 v[176:177], v[212:213], 0, s[28:29]
	s_mov_b32 m0, s53
	s_nop 0
	global_load_lds_dwordx4 v[176:177], off
	v_lshl_add_u64 v[176:177], v[214:215], 0, s[28:29]
	s_mov_b32 m0, s54
	s_nop 0
	global_load_lds_dwordx4 v[176:177], off
	s_waitcnt vmcnt(8)
	s_waitcnt lgkmcnt(0)
	s_barrier
	s_setprio 1
	s_waitcnt lgkmcnt(0)
	v_mfma_f32_16x16x32_bf16 v[64:67], v[116:119], v[172:175], v[64:67]
	v_mfma_f32_16x16x32_bf16 v[60:63], v[124:127], v[172:175], v[60:63]
	v_mfma_f32_16x16x32_bf16 v[48:51], v[116:119], v[186:189], v[48:51]
	v_mfma_f32_16x16x32_bf16 v[44:47], v[124:127], v[186:189], v[44:47]
	v_mfma_f32_16x16x32_bf16 v[36:39], v[116:119], v[194:197], v[36:39]
	v_mfma_f32_16x16x32_bf16 v[28:31], v[124:127], v[194:197], v[28:31]
	v_mfma_f32_16x16x32_bf16 v[20:23], v[116:119], v[202:205], v[20:23]
	v_mfma_f32_16x16x32_bf16 v[12:15], v[124:127], v[202:205], v[12:15]
	v_mfma_f32_16x16x32_bf16 v[64:67], v[120:123], v[182:185], v[64:67]
	v_mfma_f32_16x16x32_bf16 v[60:63], v[128:131], v[182:185], v[60:63]
	v_mfma_f32_16x16x32_bf16 v[48:51], v[120:123], v[190:193], v[48:51]
	v_mfma_f32_16x16x32_bf16 v[44:47], v[128:131], v[190:193], v[44:47]
	v_mfma_f32_16x16x32_bf16 v[36:39], v[120:123], v[198:201], v[36:39]
	v_mfma_f32_16x16x32_bf16 v[28:31], v[128:131], v[198:201], v[28:31]
	v_mfma_f32_16x16x32_bf16 v[20:23], v[120:123], v[206:209], v[20:23]
	v_mfma_f32_16x16x32_bf16 v[12:15], v[128:131], v[206:209], v[12:15]
	s_setprio 0
	s_setprio 1
	v_mfma_f32_16x16x32_bf16 v[56:59], v[148:151], v[172:175], v[56:59]
	v_mfma_f32_16x16x32_bf16 v[52:55], v[156:159], v[172:175], v[52:55]
	v_mfma_f32_16x16x32_bf16 v[40:43], v[148:151], v[186:189], v[40:43]
	v_mfma_f32_16x16x32_bf16 v[32:35], v[156:159], v[186:189], v[32:35]
	v_mfma_f32_16x16x32_bf16 v[24:27], v[148:151], v[194:197], v[24:27]
	v_mfma_f32_16x16x32_bf16 v[16:19], v[156:159], v[194:197], v[16:19]
	v_mfma_f32_16x16x32_bf16 v[8:11], v[148:151], v[202:205], v[8:11]
	v_mfma_f32_16x16x32_bf16 v[4:7], v[156:159], v[202:205], v[4:7]
	v_mfma_f32_16x16x32_bf16 v[56:59], v[152:155], v[182:185], v[56:59]
	v_mfma_f32_16x16x32_bf16 v[52:55], v[160:163], v[182:185], v[52:55]
	v_mfma_f32_16x16x32_bf16 v[40:43], v[152:155], v[190:193], v[40:43]
	v_mfma_f32_16x16x32_bf16 v[32:35], v[160:163], v[190:193], v[32:35]
	v_mfma_f32_16x16x32_bf16 v[24:27], v[152:155], v[198:201], v[24:27]
	v_mfma_f32_16x16x32_bf16 v[16:19], v[160:163], v[198:201], v[16:19]
	v_mfma_f32_16x16x32_bf16 v[8:11], v[152:155], v[206:209], v[8:11]
	v_mfma_f32_16x16x32_bf16 v[4:7], v[160:163], v[206:209], v[4:7]
	s_setprio 0
	s_barrier
	s_add_i32 s56, s56, 2
	s_add_u32 s13, s13, 0x100
	s_addc_u32 s15, s15, 0
	s_cmp_gt_u32 s56, 13
	s_mov_b64 s[20:21], s[22:23]
	s_cbranch_scc1 .Lmy_gx5
	.p2alignl 6, 3212836864

.LBB0_2282:
	s_ashr_i32 s15, s14, 31
	s_lshl_b64 s[16:17], s[14:15], 19
	s_add_u32 s20, s58, s16
	s_addc_u32 s21, s59, s17
	s_and_b64 s[16:17], s[38:39], exec
	s_cselect_b32 s11, s21, s41
	s_cselect_b32 s15, s20, s40
	s_ashr_i32 s19, s18, 31
	s_lshl_b64 s[16:17], s[18:19], 19
	s_add_u32 s22, s60, s16
	s_addc_u32 s23, s61, s17
	s_and_b64 s[16:17], s[38:39], exec
	s_cselect_b32 s16, s23, s43
	s_cselect_b32 s17, s22, s42
	s_add_u32 s19, s42, 0x100
	s_addc_u32 s73, s43, 0
	s_mov_b32 s76, -2
	s_add_u32 s42, s40, 0x100
	s_addc_u32 s43, s41, 0
	s_add_i32 s77, 0, 0x10000
	s_cmp_eq_u32 s76, 12
	s_cselect_b32 s47, s11, s43
	s_cselect_b32 s46, s15, s42
	s_cselect_b32 s45, s16, s73
	s_cselect_b32 s44, s17, s19
	s_add_i32 s78, 0, 0x14000
	v_add_u32_e32 v156, s77, v141
	v_add_u32_e32 v172, s78, v141
	ds_read_b128 v[144:147], v156
	ds_read_b128 v[148:151], v156 offset:1024
	ds_read_b128 v[152:155], v156 offset:2048
	ds_read_b128 v[156:159], v156 offset:3072
	ds_read_b128 v[160:163], v172
	ds_read_b128 v[164:167], v172 offset:1024
	ds_read_b128 v[168:171], v172 offset:2048
	ds_read_b128 v[172:175], v172 offset:3072
	v_lshl_add_u64 v[208:209], s[40:41], 0, v[138:139]
	s_add_i32 m0, s27, 0xc000
	ds_read_b128 v[176:179], v143
	ds_read_b128 v[180:183], v143 offset:1024
	ds_read_b128 v[184:187], v143 offset:2048
	ds_read_b128 v[188:191], v143 offset:3072
	ds_read_b128 v[192:195], v143 offset:4096
	ds_read_b128 v[196:199], v143 offset:5120
	ds_read_b128 v[200:203], v143 offset:6144
	ds_read_b128 v[204:207], v143 offset:7168
	global_load_lds_dwordx4 v[208:209], off
	v_lshl_add_u64 v[208:209], s[40:41], 0, v[136:137]
	s_add_i32 m0, s27, 0xe000
	s_nop 0
	global_load_lds_dwordx4 v[208:209], off
	s_waitcnt vmcnt(8)
	s_waitcnt lgkmcnt(0)
	s_barrier
	s_setprio 1
	s_waitcnt lgkmcnt(0)
	v_mfma_f32_16x16x32_bf16 v[128:131], v[144:147], v[176:179], 0
	v_mfma_f32_16x16x32_bf16 v[120:123], v[152:155], v[176:179], 0
	v_mfma_f32_16x16x32_bf16 v[112:115], v[144:147], v[184:187], 0
	v_mfma_f32_16x16x32_bf16 v[104:107], v[152:155], v[184:187], 0
	v_mfma_f32_16x16x32_bf16 v[96:99], v[144:147], v[192:195], 0
	v_mfma_f32_16x16x32_bf16 v[88:91], v[152:155], v[192:195], 0
	v_mfma_f32_16x16x32_bf16 v[80:83], v[144:147], v[200:203], 0
	v_mfma_f32_16x16x32_bf16 v[72:75], v[152:155], v[200:203], 0
	v_mfma_f32_16x16x32_bf16 v[128:131], v[148:151], v[180:183], v[128:131]
	v_mfma_f32_16x16x32_bf16 v[120:123], v[156:159], v[180:183], v[120:123]
	v_mfma_f32_16x16x32_bf16 v[112:115], v[148:151], v[188:191], v[112:115]
	v_mfma_f32_16x16x32_bf16 v[104:107], v[156:159], v[188:191], v[104:107]
	v_mfma_f32_16x16x32_bf16 v[96:99], v[148:151], v[196:199], v[96:99]
	v_mfma_f32_16x16x32_bf16 v[88:91], v[156:159], v[196:199], v[88:91]
	v_mfma_f32_16x16x32_bf16 v[80:83], v[148:151], v[204:207], v[80:83]
	v_mfma_f32_16x16x32_bf16 v[72:75], v[156:159], v[204:207], v[72:75]
	s_setprio 0
	s_setprio 1
	v_mfma_f32_16x16x32_bf16 v[124:127], v[160:163], v[176:179], 0
	v_mfma_f32_16x16x32_bf16 v[116:119], v[168:171], v[176:179], 0
	v_mfma_f32_16x16x32_bf16 v[108:111], v[160:163], v[184:187], 0
	v_mfma_f32_16x16x32_bf16 v[100:103], v[168:171], v[184:187], 0
	v_mfma_f32_16x16x32_bf16 v[92:95], v[160:163], v[192:195], 0
	v_mfma_f32_16x16x32_bf16 v[84:87], v[168:171], v[192:195], 0
	v_mfma_f32_16x16x32_bf16 v[76:79], v[160:163], v[200:203], 0
	v_mfma_f32_16x16x32_bf16 v[68:71], v[168:171], v[200:203], 0
	v_mfma_f32_16x16x32_bf16 v[124:127], v[164:167], v[180:183], v[124:127]
	v_mfma_f32_16x16x32_bf16 v[116:119], v[172:175], v[180:183], v[116:119]
	v_mfma_f32_16x16x32_bf16 v[108:111], v[164:167], v[188:191], v[108:111]
	v_mfma_f32_16x16x32_bf16 v[100:103], v[172:175], v[188:191], v[100:103]
	v_mfma_f32_16x16x32_bf16 v[92:95], v[164:167], v[196:199], v[92:95]
	v_mfma_f32_16x16x32_bf16 v[84:87], v[172:175], v[196:199], v[84:87]
	v_mfma_f32_16x16x32_bf16 v[76:79], v[164:167], v[204:207], v[76:79]
	v_mfma_f32_16x16x32_bf16 v[68:71], v[172:175], v[204:207], v[68:71]
	s_setprio 0
	s_barrier
	s_add_i32 s40, s77, s62
	v_lshl_add_u64 v[208:209], s[44:45], 0, v[2:3]
	s_mov_b32 m0, s40
	ds_read_b128 v[176:179], v143 offset:16384
	ds_read_b128 v[180:183], v143 offset:17408
	ds_read_b128 v[184:187], v143 offset:18432
	ds_read_b128 v[188:191], v143 offset:19456
	ds_read_b128 v[192:195], v143 offset:20480
	ds_read_b128 v[196:199], v143 offset:21504
	ds_read_b128 v[200:203], v143 offset:22528
	ds_read_b128 v[204:207], v143 offset:23552
	global_load_lds_dwordx4 v[208:209], off
	s_add_i32 m0, s40, 0x2000
	s_add_u32 s40, s44, 0x40000
	v_lshl_add_u64 v[210:211], s[44:45], 0, v[134:135]
	s_addc_u32 s41, s45, 0
	s_add_i32 s77, s78, s62
	global_load_lds_dwordx4 v[210:211], off
	v_lshl_add_u64 v[212:213], s[40:41], 0, v[2:3]
	s_mov_b32 m0, s77
	v_lshl_add_u64 v[214:215], s[46:47], 0, v[132:133]
	global_load_lds_dwordx4 v[212:213], off
	v_lshl_add_u64 v[212:213], s[40:41], 0, v[134:135]
	s_add_i32 m0, s77, 0x2000
	s_nop 0
	global_load_lds_dwordx4 v[212:213], off
	v_lshl_add_u64 v[212:213], s[46:47], 0, v[0:1]
	s_mov_b32 m0, s27
	s_nop 0
	global_load_lds_dwordx4 v[212:213], off
	s_mov_b32 m0, s63
	s_nop 0
	global_load_lds_dwordx4 v[214:215], off
	s_waitcnt vmcnt(8)
	s_waitcnt lgkmcnt(0)
	s_barrier
	s_setprio 1
	s_waitcnt lgkmcnt(0)
	v_mfma_f32_16x16x32_bf16 v[64:67], v[144:147], v[176:179], 0
	v_mfma_f32_16x16x32_bf16 v[56:59], v[152:155], v[176:179], 0
	v_mfma_f32_16x16x32_bf16 v[48:51], v[144:147], v[184:187], 0
	v_mfma_f32_16x16x32_bf16 v[40:43], v[152:155], v[184:187], 0
	v_mfma_f32_16x16x32_bf16 v[32:35], v[144:147], v[192:195], 0
	v_mfma_f32_16x16x32_bf16 v[24:27], v[152:155], v[192:195], 0
	v_mfma_f32_16x16x32_bf16 v[16:19], v[144:147], v[200:203], 0
	v_mfma_f32_16x16x32_bf16 v[8:11], v[152:155], v[200:203], 0
	v_mfma_f32_16x16x32_bf16 v[64:67], v[148:151], v[180:183], v[64:67]
	v_mfma_f32_16x16x32_bf16 v[56:59], v[156:159], v[180:183], v[56:59]
	v_mfma_f32_16x16x32_bf16 v[48:51], v[148:151], v[188:191], v[48:51]
	v_mfma_f32_16x16x32_bf16 v[40:43], v[156:159], v[188:191], v[40:43]
	v_mfma_f32_16x16x32_bf16 v[32:35], v[148:151], v[196:199], v[32:35]
	v_mfma_f32_16x16x32_bf16 v[24:27], v[156:159], v[196:199], v[24:27]
	v_mfma_f32_16x16x32_bf16 v[16:19], v[148:151], v[204:207], v[16:19]
	v_mfma_f32_16x16x32_bf16 v[8:11], v[156:159], v[204:207], v[8:11]
	s_setprio 0
	s_setprio 1
	v_mfma_f32_16x16x32_bf16 v[60:63], v[160:163], v[176:179], 0
	v_mfma_f32_16x16x32_bf16 v[52:55], v[168:171], v[176:179], 0
	v_mfma_f32_16x16x32_bf16 v[44:47], v[160:163], v[184:187], 0
	v_mfma_f32_16x16x32_bf16 v[36:39], v[168:171], v[184:187], 0
	v_mfma_f32_16x16x32_bf16 v[28:31], v[160:163], v[192:195], 0
	v_mfma_f32_16x16x32_bf16 v[20:23], v[168:171], v[192:195], 0
	v_mfma_f32_16x16x32_bf16 v[12:15], v[160:163], v[200:203], 0
	v_mfma_f32_16x16x32_bf16 v[4:7], v[168:171], v[200:203], 0
	v_mfma_f32_16x16x32_bf16 v[60:63], v[164:167], v[180:183], v[60:63]
	v_mfma_f32_16x16x32_bf16 v[52:55], v[172:175], v[180:183], v[52:55]
	v_mfma_f32_16x16x32_bf16 v[44:47], v[164:167], v[188:191], v[44:47]
	v_mfma_f32_16x16x32_bf16 v[36:39], v[172:175], v[188:191], v[36:39]
	v_mfma_f32_16x16x32_bf16 v[28:31], v[164:167], v[196:199], v[28:31]
	v_mfma_f32_16x16x32_bf16 v[20:23], v[172:175], v[196:199], v[20:23]
	v_mfma_f32_16x16x32_bf16 v[12:15], v[164:167], v[204:207], v[12:15]
	v_mfma_f32_16x16x32_bf16 v[4:7], v[172:175], v[204:207], v[4:7]
	s_setprio 0
	s_barrier
	s_add_i32 s77, 0, 0x18000
	s_add_i32 s78, 0, 0x1c000
	v_add_u32_e32 v156, s77, v141
	v_add_u32_e32 v172, s78, v141
	ds_read_b128 v[144:147], v156
	ds_read_b128 v[148:151], v156 offset:1024
	ds_read_b128 v[152:155], v156 offset:2048
	ds_read_b128 v[156:159], v156 offset:3072
	ds_read_b128 v[160:163], v172
	ds_read_b128 v[164:167], v172 offset:1024
	ds_read_b128 v[168:171], v172 offset:2048
	ds_read_b128 v[172:175], v172 offset:3072
	s_add_u32 s40, s46, 0x40000
	s_addc_u32 s41, s47, 0
	s_mov_b32 m0, s68
	v_lshl_add_u64 v[216:217], s[40:41], 0, v[0:1]
	ds_read_b128 v[176:179], v143 offset:32768
	ds_read_b128 v[180:183], v143 offset:33792
	ds_read_b128 v[184:187], v143 offset:34816
	ds_read_b128 v[188:191], v143 offset:35840
	ds_read_b128 v[192:195], v143 offset:36864
	ds_read_b128 v[196:199], v143 offset:37888
	ds_read_b128 v[200:203], v143 offset:38912
	ds_read_b128 v[204:207], v143 offset:39936
	global_load_lds_dwordx4 v[216:217], off
	v_lshl_add_u64 v[216:217], s[40:41], 0, v[132:133]
	s_mov_b32 m0, s69
	s_nop 0
	global_load_lds_dwordx4 v[216:217], off
	s_waitcnt vmcnt(8)
	s_waitcnt lgkmcnt(0)
	s_barrier
	s_setprio 1
	s_waitcnt lgkmcnt(0)
	v_mfma_f32_16x16x32_bf16 v[128:131], v[144:147], v[176:179], v[128:131]
	v_mfma_f32_16x16x32_bf16 v[120:123], v[152:155], v[176:179], v[120:123]
	v_mfma_f32_16x16x32_bf16 v[112:115], v[144:147], v[184:187], v[112:115]
	v_mfma_f32_16x16x32_bf16 v[104:107], v[152:155], v[184:187], v[104:107]
	v_mfma_f32_16x16x32_bf16 v[96:99], v[144:147], v[192:195], v[96:99]
	v_mfma_f32_16x16x32_bf16 v[88:91], v[152:155], v[192:195], v[88:91]
	v_mfma_f32_16x16x32_bf16 v[80:83], v[144:147], v[200:203], v[80:83]
	v_mfma_f32_16x16x32_bf16 v[72:75], v[152:155], v[200:203], v[72:75]
	v_mfma_f32_16x16x32_bf16 v[128:131], v[148:151], v[180:183], v[128:131]
	v_mfma_f32_16x16x32_bf16 v[120:123], v[156:159], v[180:183], v[120:123]
	v_mfma_f32_16x16x32_bf16 v[112:115], v[148:151], v[188:191], v[112:115]
	v_mfma_f32_16x16x32_bf16 v[104:107], v[156:159], v[188:191], v[104:107]
	v_mfma_f32_16x16x32_bf16 v[96:99], v[148:151], v[196:199], v[96:99]
	v_mfma_f32_16x16x32_bf16 v[88:91], v[156:159], v[196:199], v[88:91]
	v_mfma_f32_16x16x32_bf16 v[80:83], v[148:151], v[204:207], v[80:83]
	v_mfma_f32_16x16x32_bf16 v[72:75], v[156:159], v[204:207], v[72:75]
	s_setprio 0
	s_setprio 1
	v_mfma_f32_16x16x32_bf16 v[124:127], v[160:163], v[176:179], v[124:127]
	v_mfma_f32_16x16x32_bf16 v[116:119], v[168:171], v[176:179], v[116:119]
	v_mfma_f32_16x16x32_bf16 v[108:111], v[160:163], v[184:187], v[108:111]
	v_mfma_f32_16x16x32_bf16 v[100:103], v[168:171], v[184:187], v[100:103]
	v_mfma_f32_16x16x32_bf16 v[92:95], v[160:163], v[192:195], v[92:95]
	v_mfma_f32_16x16x32_bf16 v[84:87], v[168:171], v[192:195], v[84:87]
	v_mfma_f32_16x16x32_bf16 v[76:79], v[160:163], v[200:203], v[76:79]
	v_mfma_f32_16x16x32_bf16 v[68:71], v[168:171], v[200:203], v[68:71]
	v_mfma_f32_16x16x32_bf16 v[124:127], v[164:167], v[180:183], v[124:127]
	v_mfma_f32_16x16x32_bf16 v[116:119], v[172:175], v[180:183], v[116:119]
	v_mfma_f32_16x16x32_bf16 v[108:111], v[164:167], v[188:191], v[108:111]
	v_mfma_f32_16x16x32_bf16 v[100:103], v[172:175], v[188:191], v[100:103]
	v_mfma_f32_16x16x32_bf16 v[92:95], v[164:167], v[196:199], v[92:95]
	v_mfma_f32_16x16x32_bf16 v[84:87], v[172:175], v[196:199], v[84:87]
	v_mfma_f32_16x16x32_bf16 v[76:79], v[164:167], v[204:207], v[76:79]
	v_mfma_f32_16x16x32_bf16 v[68:71], v[172:175], v[204:207], v[68:71]
	s_setprio 0
	s_barrier
	s_add_i32 s40, s77, s62
	v_lshl_add_u64 v[208:209], v[208:209], 0, s[28:29]
	s_mov_b32 m0, s40
	ds_read_b128 v[176:179], v143 offset:49152
	ds_read_b128 v[180:183], v143 offset:50176
	ds_read_b128 v[184:187], v143 offset:51200
	ds_read_b128 v[188:191], v143 offset:52224
	ds_read_b128 v[192:195], v143 offset:53248
	ds_read_b128 v[196:199], v143 offset:54272
	ds_read_b128 v[200:203], v143 offset:55296
	ds_read_b128 v[204:207], v143 offset:56320
	global_load_lds_dwordx4 v[208:209], off
	s_add_i32 m0, s40, 0x2000
	s_add_u32 s40, s44, 0x40080
	v_lshl_add_u64 v[208:209], v[210:211], 0, s[28:29]
	s_addc_u32 s41, s45, 0
	s_add_i32 s44, s78, s62
	global_load_lds_dwordx4 v[208:209], off
	v_lshl_add_u64 v[208:209], s[40:41], 0, v[2:3]
	s_mov_b32 m0, s44
	s_nop 0
	global_load_lds_dwordx4 v[208:209], off
	v_lshl_add_u64 v[208:209], s[40:41], 0, v[134:135]
	s_add_i32 m0, s44, 0x2000
	s_nop 0
	global_load_lds_dwordx4 v[208:209], off
	v_lshl_add_u64 v[208:209], v[212:213], 0, s[28:29]
	s_mov_b32 m0, s70
	s_nop 0
	global_load_lds_dwordx4 v[208:209], off
	v_lshl_add_u64 v[208:209], v[214:215], 0, s[28:29]
	s_mov_b32 m0, s71
	s_nop 0
	global_load_lds_dwordx4 v[208:209], off
	s_waitcnt vmcnt(8)
	s_waitcnt lgkmcnt(0)
	s_barrier
	s_setprio 1
	s_waitcnt lgkmcnt(0)
	v_mfma_f32_16x16x32_bf16 v[64:67], v[144:147], v[176:179], v[64:67]
	v_mfma_f32_16x16x32_bf16 v[56:59], v[152:155], v[176:179], v[56:59]
	v_mfma_f32_16x16x32_bf16 v[48:51], v[144:147], v[184:187], v[48:51]
	v_mfma_f32_16x16x32_bf16 v[40:43], v[152:155], v[184:187], v[40:43]
	v_mfma_f32_16x16x32_bf16 v[32:35], v[144:147], v[192:195], v[32:35]
	v_mfma_f32_16x16x32_bf16 v[24:27], v[152:155], v[192:195], v[24:27]
	v_mfma_f32_16x16x32_bf16 v[16:19], v[144:147], v[200:203], v[16:19]
	v_mfma_f32_16x16x32_bf16 v[8:11], v[152:155], v[200:203], v[8:11]
	v_mfma_f32_16x16x32_bf16 v[64:67], v[148:151], v[180:183], v[64:67]
	v_mfma_f32_16x16x32_bf16 v[56:59], v[156:159], v[180:183], v[56:59]
	v_mfma_f32_16x16x32_bf16 v[48:51], v[148:151], v[188:191], v[48:51]
	v_mfma_f32_16x16x32_bf16 v[40:43], v[156:159], v[188:191], v[40:43]
	v_mfma_f32_16x16x32_bf16 v[32:35], v[148:151], v[196:199], v[32:35]
	v_mfma_f32_16x16x32_bf16 v[24:27], v[156:159], v[196:199], v[24:27]
	v_mfma_f32_16x16x32_bf16 v[16:19], v[148:151], v[204:207], v[16:19]
	v_mfma_f32_16x16x32_bf16 v[8:11], v[156:159], v[204:207], v[8:11]
	s_setprio 0
	s_setprio 1
	v_mfma_f32_16x16x32_bf16 v[60:63], v[160:163], v[176:179], v[60:63]
	v_mfma_f32_16x16x32_bf16 v[52:55], v[168:171], v[176:179], v[52:55]
	v_mfma_f32_16x16x32_bf16 v[44:47], v[160:163], v[184:187], v[44:47]
	v_mfma_f32_16x16x32_bf16 v[36:39], v[168:171], v[184:187], v[36:39]
	v_mfma_f32_16x16x32_bf16 v[28:31], v[160:163], v[192:195], v[28:31]
	v_mfma_f32_16x16x32_bf16 v[20:23], v[168:171], v[192:195], v[20:23]
	v_mfma_f32_16x16x32_bf16 v[12:15], v[160:163], v[200:203], v[12:15]
	v_mfma_f32_16x16x32_bf16 v[4:7], v[168:171], v[200:203], v[4:7]
	v_mfma_f32_16x16x32_bf16 v[60:63], v[164:167], v[180:183], v[60:63]
	v_mfma_f32_16x16x32_bf16 v[52:55], v[172:175], v[180:183], v[52:55]
	v_mfma_f32_16x16x32_bf16 v[44:47], v[164:167], v[188:191], v[44:47]
	v_mfma_f32_16x16x32_bf16 v[36:39], v[172:175], v[188:191], v[36:39]
	v_mfma_f32_16x16x32_bf16 v[28:31], v[164:167], v[196:199], v[28:31]
	v_mfma_f32_16x16x32_bf16 v[20:23], v[172:175], v[196:199], v[20:23]
	v_mfma_f32_16x16x32_bf16 v[12:15], v[164:167], v[204:207], v[12:15]
	v_mfma_f32_16x16x32_bf16 v[4:7], v[172:175], v[204:207], v[4:7]
	s_setprio 0
	s_barrier
	s_add_i32 s76, s76, 2
	s_add_u32 s19, s19, 0x100
	s_addc_u32 s73, s73, 0
	s_cmp_gt_u32 s76, 13
	s_mov_b64 s[40:41], s[42:43]
	s_cbranch_scc1 .Lmy_gx6
	.p2alignl 6, 3212836864

.LBB0_2350:
	s_add_u32 s58, s18, 0x100
	s_addc_u32 s59, s19, 0
	s_mov_b32 s60, -2
	s_add_u32 s18, s14, 0x100
	s_addc_u32 s19, s15, 0
	s_add_i32 s61, 0, 0x10000
	s_cmp_eq_u32 s60, 52
	s_cselect_b32 s23, s11, s19
	s_cselect_b32 s22, s10, s18
	s_cselect_b32 s21, s13, s59
	s_cselect_b32 s20, s12, s58
	s_add_i32 s62, 0, 0x14000
	v_add_u32_e32 v156, s61, v141
	v_add_u32_e32 v172, s62, v141
	ds_read_b128 v[144:147], v156
	ds_read_b128 v[148:151], v156 offset:1024
	ds_read_b128 v[152:155], v156 offset:2048
	ds_read_b128 v[156:159], v156 offset:3072
	ds_read_b128 v[160:163], v172
	ds_read_b128 v[164:167], v172 offset:1024
	ds_read_b128 v[168:171], v172 offset:2048
	ds_read_b128 v[172:175], v172 offset:3072
	v_lshl_add_u64 v[208:209], s[14:15], 0, v[138:139]
	s_add_i32 m0, s47, 0xc000
	ds_read_b128 v[176:179], v143
	ds_read_b128 v[180:183], v143 offset:1024
	ds_read_b128 v[184:187], v143 offset:2048
	ds_read_b128 v[188:191], v143 offset:3072
	ds_read_b128 v[192:195], v143 offset:4096
	ds_read_b128 v[196:199], v143 offset:5120
	ds_read_b128 v[200:203], v143 offset:6144
	ds_read_b128 v[204:207], v143 offset:7168
	global_load_lds_dwordx4 v[208:209], off
	v_lshl_add_u64 v[208:209], s[14:15], 0, v[136:137]
	s_add_i32 m0, s47, 0xe000
	s_nop 0
	global_load_lds_dwordx4 v[208:209], off
	s_waitcnt vmcnt(8)
	s_waitcnt lgkmcnt(0)
	s_barrier
	s_setprio 1
	s_waitcnt lgkmcnt(0)
	v_mfma_f32_16x16x32_bf16 v[128:131], v[144:147], v[176:179], 0
	v_mfma_f32_16x16x32_bf16 v[124:127], v[152:155], v[176:179], 0
	v_mfma_f32_16x16x32_bf16 v[120:123], v[144:147], v[184:187], 0
	v_mfma_f32_16x16x32_bf16 v[116:119], v[152:155], v[184:187], 0
	v_mfma_f32_16x16x32_bf16 v[104:107], v[144:147], v[192:195], 0
	v_mfma_f32_16x16x32_bf16 v[100:103], v[152:155], v[192:195], 0
	v_mfma_f32_16x16x32_bf16 v[88:91], v[144:147], v[200:203], 0
	v_mfma_f32_16x16x32_bf16 v[84:87], v[152:155], v[200:203], 0
	v_mfma_f32_16x16x32_bf16 v[128:131], v[148:151], v[180:183], v[128:131]
	v_mfma_f32_16x16x32_bf16 v[124:127], v[156:159], v[180:183], v[124:127]
	v_mfma_f32_16x16x32_bf16 v[120:123], v[148:151], v[188:191], v[120:123]
	v_mfma_f32_16x16x32_bf16 v[116:119], v[156:159], v[188:191], v[116:119]
	v_mfma_f32_16x16x32_bf16 v[104:107], v[148:151], v[196:199], v[104:107]
	v_mfma_f32_16x16x32_bf16 v[100:103], v[156:159], v[196:199], v[100:103]
	v_mfma_f32_16x16x32_bf16 v[88:91], v[148:151], v[204:207], v[88:91]
	v_mfma_f32_16x16x32_bf16 v[84:87], v[156:159], v[204:207], v[84:87]
	s_setprio 0
	s_setprio 1
	v_mfma_f32_16x16x32_bf16 v[112:115], v[160:163], v[176:179], 0
	v_mfma_f32_16x16x32_bf16 v[108:111], v[168:171], v[176:179], 0
	v_mfma_f32_16x16x32_bf16 v[96:99], v[160:163], v[184:187], 0
	v_mfma_f32_16x16x32_bf16 v[92:95], v[168:171], v[184:187], 0
	v_mfma_f32_16x16x32_bf16 v[80:83], v[160:163], v[192:195], 0
	v_mfma_f32_16x16x32_bf16 v[76:79], v[168:171], v[192:195], 0
	v_mfma_f32_16x16x32_bf16 v[72:75], v[160:163], v[200:203], 0
	v_mfma_f32_16x16x32_bf16 v[68:71], v[168:171], v[200:203], 0
	v_mfma_f32_16x16x32_bf16 v[112:115], v[164:167], v[180:183], v[112:115]
	v_mfma_f32_16x16x32_bf16 v[108:111], v[172:175], v[180:183], v[108:111]
	v_mfma_f32_16x16x32_bf16 v[96:99], v[164:167], v[188:191], v[96:99]
	v_mfma_f32_16x16x32_bf16 v[92:95], v[172:175], v[188:191], v[92:95]
	v_mfma_f32_16x16x32_bf16 v[80:83], v[164:167], v[196:199], v[80:83]
	v_mfma_f32_16x16x32_bf16 v[76:79], v[172:175], v[196:199], v[76:79]
	v_mfma_f32_16x16x32_bf16 v[72:75], v[164:167], v[204:207], v[72:75]
	v_mfma_f32_16x16x32_bf16 v[68:71], v[172:175], v[204:207], v[68:71]
	s_setprio 0
	s_barrier
	s_add_i32 s14, s61, s45
	v_lshl_add_u64 v[208:209], s[20:21], 0, v[2:3]
	s_mov_b32 m0, s14
	ds_read_b128 v[176:179], v143 offset:16384
	ds_read_b128 v[180:183], v143 offset:17408
	ds_read_b128 v[184:187], v143 offset:18432
	ds_read_b128 v[188:191], v143 offset:19456
	ds_read_b128 v[192:195], v143 offset:20480
	ds_read_b128 v[196:199], v143 offset:21504
	ds_read_b128 v[200:203], v143 offset:22528
	ds_read_b128 v[204:207], v143 offset:23552
	global_load_lds_dwordx4 v[208:209], off
	s_add_i32 m0, s14, 0x2000
	s_add_u32 s14, s20, 0xe0000
	v_lshl_add_u64 v[210:211], s[20:21], 0, v[0:1]
	s_addc_u32 s15, s21, 0
	s_add_i32 s61, s62, s45
	global_load_lds_dwordx4 v[210:211], off
	v_lshl_add_u64 v[212:213], s[14:15], 0, v[2:3]
	s_mov_b32 m0, s61
	v_lshl_add_u64 v[214:215], s[22:23], 0, v[132:133]
	global_load_lds_dwordx4 v[212:213], off
	v_lshl_add_u64 v[212:213], s[14:15], 0, v[0:1]
	s_add_i32 m0, s61, 0x2000
	s_nop 0
	global_load_lds_dwordx4 v[212:213], off
	v_lshl_add_u64 v[212:213], s[22:23], 0, v[134:135]
	s_mov_b32 m0, s47
	s_nop 0
	global_load_lds_dwordx4 v[212:213], off
	s_mov_b32 m0, s48
	s_nop 0
	global_load_lds_dwordx4 v[214:215], off
	s_waitcnt vmcnt(8)
	s_waitcnt lgkmcnt(0)
	s_barrier
	s_setprio 1
	s_waitcnt lgkmcnt(0)
	v_mfma_f32_16x16x32_bf16 v[64:67], v[144:147], v[176:179], 0
	v_mfma_f32_16x16x32_bf16 v[60:63], v[152:155], v[176:179], 0
	v_mfma_f32_16x16x32_bf16 v[56:59], v[144:147], v[184:187], 0
	v_mfma_f32_16x16x32_bf16 v[52:55], v[152:155], v[184:187], 0
	v_mfma_f32_16x16x32_bf16 v[40:43], v[144:147], v[192:195], 0
	v_mfma_f32_16x16x32_bf16 v[36:39], v[152:155], v[192:195], 0
	v_mfma_f32_16x16x32_bf16 v[24:27], v[144:147], v[200:203], 0
	v_mfma_f32_16x16x32_bf16 v[20:23], v[152:155], v[200:203], 0
	v_mfma_f32_16x16x32_bf16 v[64:67], v[148:151], v[180:183], v[64:67]
	v_mfma_f32_16x16x32_bf16 v[60:63], v[156:159], v[180:183], v[60:63]
	v_mfma_f32_16x16x32_bf16 v[56:59], v[148:151], v[188:191], v[56:59]
	v_mfma_f32_16x16x32_bf16 v[52:55], v[156:159], v[188:191], v[52:55]
	v_mfma_f32_16x16x32_bf16 v[40:43], v[148:151], v[196:199], v[40:43]
	v_mfma_f32_16x16x32_bf16 v[36:39], v[156:159], v[196:199], v[36:39]
	v_mfma_f32_16x16x32_bf16 v[24:27], v[148:151], v[204:207], v[24:27]
	v_mfma_f32_16x16x32_bf16 v[20:23], v[156:159], v[204:207], v[20:23]
	s_setprio 0
	s_setprio 1
	v_mfma_f32_16x16x32_bf16 v[48:51], v[160:163], v[176:179], 0
	v_mfma_f32_16x16x32_bf16 v[44:47], v[168:171], v[176:179], 0
	v_mfma_f32_16x16x32_bf16 v[32:35], v[160:163], v[184:187], 0
	v_mfma_f32_16x16x32_bf16 v[28:31], v[168:171], v[184:187], 0
	v_mfma_f32_16x16x32_bf16 v[16:19], v[160:163], v[192:195], 0
	v_mfma_f32_16x16x32_bf16 v[12:15], v[168:171], v[192:195], 0
	v_mfma_f32_16x16x32_bf16 v[8:11], v[160:163], v[200:203], 0
	v_mfma_f32_16x16x32_bf16 v[4:7], v[168:171], v[200:203], 0
	v_mfma_f32_16x16x32_bf16 v[48:51], v[164:167], v[180:183], v[48:51]
	v_mfma_f32_16x16x32_bf16 v[44:47], v[172:175], v[180:183], v[44:47]
	v_mfma_f32_16x16x32_bf16 v[32:35], v[164:167], v[188:191], v[32:35]
	v_mfma_f32_16x16x32_bf16 v[28:31], v[172:175], v[188:191], v[28:31]
	v_mfma_f32_16x16x32_bf16 v[16:19], v[164:167], v[196:199], v[16:19]
	v_mfma_f32_16x16x32_bf16 v[12:15], v[172:175], v[196:199], v[12:15]
	v_mfma_f32_16x16x32_bf16 v[8:11], v[164:167], v[204:207], v[8:11]
	v_mfma_f32_16x16x32_bf16 v[4:7], v[172:175], v[204:207], v[4:7]
	s_setprio 0
	s_barrier
	s_add_i32 s61, 0, 0x18000
	s_add_i32 s62, 0, 0x1c000
	v_add_u32_e32 v156, s61, v141
	v_add_u32_e32 v172, s62, v141
	ds_read_b128 v[144:147], v156
	ds_read_b128 v[148:151], v156 offset:1024
	ds_read_b128 v[152:155], v156 offset:2048
	ds_read_b128 v[156:159], v156 offset:3072
	ds_read_b128 v[160:163], v172
	ds_read_b128 v[164:167], v172 offset:1024
	ds_read_b128 v[168:171], v172 offset:2048
	ds_read_b128 v[172:175], v172 offset:3072
	s_add_u32 s14, s22, 0xe0000
	s_addc_u32 s15, s23, 0
	s_mov_b32 m0, s49
	v_lshl_add_u64 v[216:217], s[14:15], 0, v[134:135]
	ds_read_b128 v[176:179], v143 offset:32768
	ds_read_b128 v[180:183], v143 offset:33792
	ds_read_b128 v[184:187], v143 offset:34816
	ds_read_b128 v[188:191], v143 offset:35840
	ds_read_b128 v[192:195], v143 offset:36864
	ds_read_b128 v[196:199], v143 offset:37888
	ds_read_b128 v[200:203], v143 offset:38912
	ds_read_b128 v[204:207], v143 offset:39936
	global_load_lds_dwordx4 v[216:217], off
	v_lshl_add_u64 v[216:217], s[14:15], 0, v[132:133]
	s_mov_b32 m0, s50
	s_nop 0
	global_load_lds_dwordx4 v[216:217], off
	s_waitcnt vmcnt(8)
	s_waitcnt lgkmcnt(0)
	s_barrier
	s_setprio 1
	s_waitcnt lgkmcnt(0)
	v_mfma_f32_16x16x32_bf16 v[128:131], v[144:147], v[176:179], v[128:131]
	v_mfma_f32_16x16x32_bf16 v[124:127], v[152:155], v[176:179], v[124:127]
	v_mfma_f32_16x16x32_bf16 v[120:123], v[144:147], v[184:187], v[120:123]
	v_mfma_f32_16x16x32_bf16 v[116:119], v[152:155], v[184:187], v[116:119]
	v_mfma_f32_16x16x32_bf16 v[104:107], v[144:147], v[192:195], v[104:107]
	v_mfma_f32_16x16x32_bf16 v[100:103], v[152:155], v[192:195], v[100:103]
	v_mfma_f32_16x16x32_bf16 v[88:91], v[144:147], v[200:203], v[88:91]
	v_mfma_f32_16x16x32_bf16 v[84:87], v[152:155], v[200:203], v[84:87]
	v_mfma_f32_16x16x32_bf16 v[128:131], v[148:151], v[180:183], v[128:131]
	v_mfma_f32_16x16x32_bf16 v[124:127], v[156:159], v[180:183], v[124:127]
	v_mfma_f32_16x16x32_bf16 v[120:123], v[148:151], v[188:191], v[120:123]
	v_mfma_f32_16x16x32_bf16 v[116:119], v[156:159], v[188:191], v[116:119]
	v_mfma_f32_16x16x32_bf16 v[104:107], v[148:151], v[196:199], v[104:107]
	v_mfma_f32_16x16x32_bf16 v[100:103], v[156:159], v[196:199], v[100:103]
	v_mfma_f32_16x16x32_bf16 v[88:91], v[148:151], v[204:207], v[88:91]
	v_mfma_f32_16x16x32_bf16 v[84:87], v[156:159], v[204:207], v[84:87]
	s_setprio 0
	s_setprio 1
	v_mfma_f32_16x16x32_bf16 v[112:115], v[160:163], v[176:179], v[112:115]
	v_mfma_f32_16x16x32_bf16 v[108:111], v[168:171], v[176:179], v[108:111]
	v_mfma_f32_16x16x32_bf16 v[96:99], v[160:163], v[184:187], v[96:99]
	v_mfma_f32_16x16x32_bf16 v[92:95], v[168:171], v[184:187], v[92:95]
	v_mfma_f32_16x16x32_bf16 v[80:83], v[160:163], v[192:195], v[80:83]
	v_mfma_f32_16x16x32_bf16 v[76:79], v[168:171], v[192:195], v[76:79]
	v_mfma_f32_16x16x32_bf16 v[72:75], v[160:163], v[200:203], v[72:75]
	v_mfma_f32_16x16x32_bf16 v[68:71], v[168:171], v[200:203], v[68:71]
	v_mfma_f32_16x16x32_bf16 v[112:115], v[164:167], v[180:183], v[112:115]
	v_mfma_f32_16x16x32_bf16 v[108:111], v[172:175], v[180:183], v[108:111]
	v_mfma_f32_16x16x32_bf16 v[96:99], v[164:167], v[188:191], v[96:99]
	v_mfma_f32_16x16x32_bf16 v[92:95], v[172:175], v[188:191], v[92:95]
	v_mfma_f32_16x16x32_bf16 v[80:83], v[164:167], v[196:199], v[80:83]
	v_mfma_f32_16x16x32_bf16 v[76:79], v[172:175], v[196:199], v[76:79]
	v_mfma_f32_16x16x32_bf16 v[72:75], v[164:167], v[204:207], v[72:75]
	v_mfma_f32_16x16x32_bf16 v[68:71], v[172:175], v[204:207], v[68:71]
	s_setprio 0
	s_barrier
	s_add_i32 s14, s61, s45
	v_lshl_add_u64 v[208:209], v[208:209], 0, s[28:29]
	s_mov_b32 m0, s14
	ds_read_b128 v[176:179], v143 offset:49152
	ds_read_b128 v[180:183], v143 offset:50176
	ds_read_b128 v[184:187], v143 offset:51200
	ds_read_b128 v[188:191], v143 offset:52224
	ds_read_b128 v[192:195], v143 offset:53248
	ds_read_b128 v[196:199], v143 offset:54272
	ds_read_b128 v[200:203], v143 offset:55296
	ds_read_b128 v[204:207], v143 offset:56320
	global_load_lds_dwordx4 v[208:209], off
	s_add_i32 m0, s14, 0x2000
	s_add_u32 s14, s20, 0xe0080
	v_lshl_add_u64 v[208:209], v[210:211], 0, s[28:29]
	s_addc_u32 s15, s21, 0
	s_add_i32 s20, s62, s45
	global_load_lds_dwordx4 v[208:209], off
	v_lshl_add_u64 v[208:209], s[14:15], 0, v[2:3]
	s_mov_b32 m0, s20
	s_nop 0
	global_load_lds_dwordx4 v[208:209], off
	v_lshl_add_u64 v[208:209], s[14:15], 0, v[0:1]
	s_add_i32 m0, s20, 0x2000
	s_nop 0
	global_load_lds_dwordx4 v[208:209], off
	v_lshl_add_u64 v[208:209], v[212:213], 0, s[28:29]
	s_mov_b32 m0, s51
	s_nop 0
	global_load_lds_dwordx4 v[208:209], off
	v_lshl_add_u64 v[208:209], v[214:215], 0, s[28:29]
	s_mov_b32 m0, s52
	s_nop 0
	global_load_lds_dwordx4 v[208:209], off
	s_waitcnt vmcnt(8)
	s_waitcnt lgkmcnt(0)
	s_barrier
	s_setprio 1
	s_waitcnt lgkmcnt(0)
	v_mfma_f32_16x16x32_bf16 v[64:67], v[144:147], v[176:179], v[64:67]
	v_mfma_f32_16x16x32_bf16 v[60:63], v[152:155], v[176:179], v[60:63]
	v_mfma_f32_16x16x32_bf16 v[56:59], v[144:147], v[184:187], v[56:59]
	v_mfma_f32_16x16x32_bf16 v[52:55], v[152:155], v[184:187], v[52:55]
	v_mfma_f32_16x16x32_bf16 v[40:43], v[144:147], v[192:195], v[40:43]
	v_mfma_f32_16x16x32_bf16 v[36:39], v[152:155], v[192:195], v[36:39]
	v_mfma_f32_16x16x32_bf16 v[24:27], v[144:147], v[200:203], v[24:27]
	v_mfma_f32_16x16x32_bf16 v[20:23], v[152:155], v[200:203], v[20:23]
	v_mfma_f32_16x16x32_bf16 v[64:67], v[148:151], v[180:183], v[64:67]
	v_mfma_f32_16x16x32_bf16 v[60:63], v[156:159], v[180:183], v[60:63]
	v_mfma_f32_16x16x32_bf16 v[56:59], v[148:151], v[188:191], v[56:59]
	v_mfma_f32_16x16x32_bf16 v[52:55], v[156:159], v[188:191], v[52:55]
	v_mfma_f32_16x16x32_bf16 v[40:43], v[148:151], v[196:199], v[40:43]
	v_mfma_f32_16x16x32_bf16 v[36:39], v[156:159], v[196:199], v[36:39]
	v_mfma_f32_16x16x32_bf16 v[24:27], v[148:151], v[204:207], v[24:27]
	v_mfma_f32_16x16x32_bf16 v[20:23], v[156:159], v[204:207], v[20:23]
	s_setprio 0
	s_setprio 1
	v_mfma_f32_16x16x32_bf16 v[48:51], v[160:163], v[176:179], v[48:51]
	v_mfma_f32_16x16x32_bf16 v[44:47], v[168:171], v[176:179], v[44:47]
	v_mfma_f32_16x16x32_bf16 v[32:35], v[160:163], v[184:187], v[32:35]
	v_mfma_f32_16x16x32_bf16 v[28:31], v[168:171], v[184:187], v[28:31]
	v_mfma_f32_16x16x32_bf16 v[16:19], v[160:163], v[192:195], v[16:19]
	v_mfma_f32_16x16x32_bf16 v[12:15], v[168:171], v[192:195], v[12:15]
	v_mfma_f32_16x16x32_bf16 v[8:11], v[160:163], v[200:203], v[8:11]
	v_mfma_f32_16x16x32_bf16 v[4:7], v[168:171], v[200:203], v[4:7]
	v_mfma_f32_16x16x32_bf16 v[48:51], v[164:167], v[180:183], v[48:51]
	v_mfma_f32_16x16x32_bf16 v[44:47], v[172:175], v[180:183], v[44:47]
	v_mfma_f32_16x16x32_bf16 v[32:35], v[164:167], v[188:191], v[32:35]
	v_mfma_f32_16x16x32_bf16 v[28:31], v[172:175], v[188:191], v[28:31]
	v_mfma_f32_16x16x32_bf16 v[16:19], v[164:167], v[196:199], v[16:19]
	v_mfma_f32_16x16x32_bf16 v[12:15], v[172:175], v[196:199], v[12:15]
	v_mfma_f32_16x16x32_bf16 v[8:11], v[164:167], v[204:207], v[8:11]
	v_mfma_f32_16x16x32_bf16 v[4:7], v[172:175], v[204:207], v[4:7]
	s_setprio 0
	s_barrier
	s_add_i32 s60, s60, 2
	s_add_u32 s58, s58, 0x100
	s_addc_u32 s59, s59, 0
	s_cmp_gt_u32 s60, 53
	s_mov_b64 s[14:15], s[18:19]
	s_cbranch_scc1 .Lmy_gx7
	.p2alignl 6, 3212836864

.LBB0_2373:
	s_mov_b64 s[70:71], 0x100
	v_lshl_add_u64 v[140:141], v[4:5], 0, s[70:71]
	s_mov_b32 s16, 0
	s_mov_b64 s[72:73], 0xe0000
	s_mov_b64 s[76:77], 0xe0080
	s_add_i32 s17, s16, 2
	s_add_u32 s18, s14, 0x100
	s_addc_u32 s19, s15, 0
	s_add_i32 s69, 0, 0x10000
	s_cmp_eq_u32 s62, s16
	s_cselect_b32 s21, s13, s19
	s_cselect_b32 s20, s12, s18
	v_add_u32_e32 v2, s69, v143
	s_cselect_b64 vcc, -1, 0
	s_add_i32 s16, 0, 0x14000
	ds_read_b128 v[148:151], v2
	ds_read_b128 v[152:155], v2 offset:1024
	ds_read_b128 v[156:159], v2 offset:2048
	ds_read_b128 v[160:163], v2 offset:3072
	v_add_u32_e32 v2, s16, v143
	ds_read_b128 v[164:167], v2
	ds_read_b128 v[168:171], v2 offset:1024
	ds_read_b128 v[172:175], v2 offset:2048
	ds_read_b128 v[176:179], v2 offset:3072
	v_cndmask_b32_e32 v213, v141, v139, vcc
	v_cndmask_b32_e32 v212, v140, v138, vcc
	v_lshl_add_u64 v[214:215], s[14:15], 0, v[136:137]
	s_add_i32 m0, s50, 0xc000
	ds_read_b128 v[180:183], v146
	ds_read_b128 v[184:187], v146 offset:1024
	ds_read_b128 v[188:191], v146 offset:2048
	ds_read_b128 v[192:195], v146 offset:3072
	ds_read_b128 v[196:199], v146 offset:4096
	ds_read_b128 v[200:203], v146 offset:5120
	ds_read_b128 v[204:207], v146 offset:6144
	ds_read_b128 v[208:211], v146 offset:7168
	global_load_lds_dwordx4 v[214:215], off
	v_lshl_add_u64 v[214:215], s[14:15], 0, v[134:135]
	s_add_i32 m0, s50, 0xe000
	s_nop 0
	global_load_lds_dwordx4 v[214:215], off
	s_waitcnt vmcnt(8)
	s_waitcnt lgkmcnt(0)
	s_barrier
	s_setprio 1
	s_waitcnt lgkmcnt(0)
	v_mfma_f32_16x16x32_bf16 v[128:131], v[148:151], v[180:183], 0
	v_mfma_f32_16x16x32_bf16 v[124:127], v[156:159], v[180:183], 0
	v_mfma_f32_16x16x32_bf16 v[120:123], v[148:151], v[188:191], 0
	v_mfma_f32_16x16x32_bf16 v[116:119], v[156:159], v[188:191], 0
	v_mfma_f32_16x16x32_bf16 v[108:111], v[148:151], v[196:199], 0
	v_mfma_f32_16x16x32_bf16 v[100:103], v[156:159], v[196:199], 0
	v_mfma_f32_16x16x32_bf16 v[92:95], v[148:151], v[204:207], 0
	v_mfma_f32_16x16x32_bf16 v[84:87], v[156:159], v[204:207], 0
	v_mfma_f32_16x16x32_bf16 v[128:131], v[152:155], v[184:187], v[128:131]
	v_mfma_f32_16x16x32_bf16 v[124:127], v[160:163], v[184:187], v[124:127]
	v_mfma_f32_16x16x32_bf16 v[120:123], v[152:155], v[192:195], v[120:123]
	v_mfma_f32_16x16x32_bf16 v[116:119], v[160:163], v[192:195], v[116:119]
	v_mfma_f32_16x16x32_bf16 v[108:111], v[152:155], v[200:203], v[108:111]
	v_mfma_f32_16x16x32_bf16 v[100:103], v[160:163], v[200:203], v[100:103]
	v_mfma_f32_16x16x32_bf16 v[92:95], v[152:155], v[208:211], v[92:95]
	v_mfma_f32_16x16x32_bf16 v[84:87], v[160:163], v[208:211], v[84:87]
	s_setprio 0
	s_setprio 1
	v_mfma_f32_16x16x32_bf16 v[112:115], v[164:167], v[180:183], 0
	v_mfma_f32_16x16x32_bf16 v[104:107], v[172:175], v[180:183], 0
	v_mfma_f32_16x16x32_bf16 v[96:99], v[164:167], v[188:191], 0
	v_mfma_f32_16x16x32_bf16 v[88:91], v[172:175], v[188:191], 0
	v_mfma_f32_16x16x32_bf16 v[80:83], v[164:167], v[196:199], 0
	v_mfma_f32_16x16x32_bf16 v[76:79], v[172:175], v[196:199], 0
	v_mfma_f32_16x16x32_bf16 v[72:75], v[164:167], v[204:207], 0
	v_mfma_f32_16x16x32_bf16 v[68:71], v[172:175], v[204:207], 0
	v_mfma_f32_16x16x32_bf16 v[112:115], v[168:171], v[184:187], v[112:115]
	v_mfma_f32_16x16x32_bf16 v[104:107], v[176:179], v[184:187], v[104:107]
	v_mfma_f32_16x16x32_bf16 v[96:99], v[168:171], v[192:195], v[96:99]
	v_mfma_f32_16x16x32_bf16 v[88:91], v[176:179], v[192:195], v[88:91]
	v_mfma_f32_16x16x32_bf16 v[80:83], v[168:171], v[200:203], v[80:83]
	v_mfma_f32_16x16x32_bf16 v[76:79], v[176:179], v[200:203], v[76:79]
	v_mfma_f32_16x16x32_bf16 v[72:75], v[168:171], v[208:211], v[72:75]
	v_mfma_f32_16x16x32_bf16 v[68:71], v[176:179], v[208:211], v[68:71]
	s_setprio 0
	s_barrier
	s_add_i32 s14, s69, s45
	v_lshl_add_u64 v[214:215], v[212:213], 0, v[132:133]
	s_mov_b32 m0, s14
	ds_read_b128 v[180:183], v146 offset:16384
	ds_read_b128 v[184:187], v146 offset:17408
	ds_read_b128 v[188:191], v146 offset:18432
	ds_read_b128 v[192:195], v146 offset:19456
	ds_read_b128 v[196:199], v146 offset:20480
	ds_read_b128 v[200:203], v146 offset:21504
	ds_read_b128 v[204:207], v146 offset:22528
	ds_read_b128 v[208:211], v146 offset:23552
	global_load_lds_dwordx4 v[214:215], off
	v_lshl_add_u64 v[216:217], v[212:213], 0, v[0:1]
	s_add_i32 m0, s14, 0x2000
	v_lshl_add_u64 v[218:219], v[212:213], 0, s[72:73]
	s_add_i32 s14, s16, s45
	global_load_lds_dwordx4 v[216:217], off
	v_lshl_add_u64 v[220:221], v[218:219], 0, v[132:133]
	s_mov_b32 m0, s14
	v_lshl_add_u64 v[218:219], v[218:219], 0, v[0:1]
	global_load_lds_dwordx4 v[220:221], off
	s_add_i32 m0, s14, 0x2000
	v_lshl_add_u64 v[220:221], s[20:21], 0, v[0:1]
	global_load_lds_dwordx4 v[218:219], off
	v_lshl_add_u64 v[218:219], s[20:21], 0, v[132:133]
	s_mov_b32 m0, s50
	s_nop 0
	global_load_lds_dwordx4 v[218:219], off
	s_mov_b32 m0, s51
	s_nop 0
	global_load_lds_dwordx4 v[220:221], off
	s_waitcnt vmcnt(8)
	s_waitcnt lgkmcnt(0)
	s_barrier
	s_setprio 1
	s_waitcnt lgkmcnt(0)
	v_mfma_f32_16x16x32_bf16 v[64:67], v[148:151], v[180:183], 0
	v_mfma_f32_16x16x32_bf16 v[60:63], v[156:159], v[180:183], 0
	v_mfma_f32_16x16x32_bf16 v[56:59], v[148:151], v[188:191], 0
	v_mfma_f32_16x16x32_bf16 v[52:55], v[156:159], v[188:191], 0
	v_mfma_f32_16x16x32_bf16 v[40:43], v[148:151], v[196:199], 0
	v_mfma_f32_16x16x32_bf16 v[36:39], v[156:159], v[196:199], 0
	v_mfma_f32_16x16x32_bf16 v[24:27], v[148:151], v[204:207], 0
	v_mfma_f32_16x16x32_bf16 v[20:23], v[156:159], v[204:207], 0
	v_mfma_f32_16x16x32_bf16 v[64:67], v[152:155], v[184:187], v[64:67]
	v_mfma_f32_16x16x32_bf16 v[60:63], v[160:163], v[184:187], v[60:63]
	v_mfma_f32_16x16x32_bf16 v[56:59], v[152:155], v[192:195], v[56:59]
	v_mfma_f32_16x16x32_bf16 v[52:55], v[160:163], v[192:195], v[52:55]
	v_mfma_f32_16x16x32_bf16 v[40:43], v[152:155], v[200:203], v[40:43]
	v_mfma_f32_16x16x32_bf16 v[36:39], v[160:163], v[200:203], v[36:39]
	v_mfma_f32_16x16x32_bf16 v[24:27], v[152:155], v[208:211], v[24:27]
	v_mfma_f32_16x16x32_bf16 v[20:23], v[160:163], v[208:211], v[20:23]
	s_setprio 0
	s_setprio 1
	v_mfma_f32_16x16x32_bf16 v[48:51], v[164:167], v[180:183], 0
	v_mfma_f32_16x16x32_bf16 v[44:47], v[172:175], v[180:183], 0
	v_mfma_f32_16x16x32_bf16 v[32:35], v[164:167], v[188:191], 0
	v_mfma_f32_16x16x32_bf16 v[28:31], v[172:175], v[188:191], 0
	v_mfma_f32_16x16x32_bf16 v[16:19], v[164:167], v[196:199], 0
	v_mfma_f32_16x16x32_bf16 v[12:15], v[172:175], v[196:199], 0
	v_mfma_f32_16x16x32_bf16 v[8:11], v[164:167], v[204:207], 0
	v_mfma_f32_16x16x32_bf16 v[4:7], v[172:175], v[204:207], 0
	v_mfma_f32_16x16x32_bf16 v[48:51], v[168:171], v[184:187], v[48:51]
	v_mfma_f32_16x16x32_bf16 v[44:47], v[176:179], v[184:187], v[44:47]
	v_mfma_f32_16x16x32_bf16 v[32:35], v[168:171], v[192:195], v[32:35]
	v_mfma_f32_16x16x32_bf16 v[28:31], v[176:179], v[192:195], v[28:31]
	v_mfma_f32_16x16x32_bf16 v[16:19], v[168:171], v[200:203], v[16:19]
	v_mfma_f32_16x16x32_bf16 v[12:15], v[176:179], v[200:203], v[12:15]
	v_mfma_f32_16x16x32_bf16 v[8:11], v[168:171], v[208:211], v[8:11]
	v_mfma_f32_16x16x32_bf16 v[4:7], v[176:179], v[208:211], v[4:7]
	s_setprio 0
	s_barrier
	s_add_i32 s16, 0, 0x18000
	v_add_u32_e32 v2, s16, v143
	s_add_i32 s69, 0, 0x1c000
	ds_read_b128 v[148:151], v2
	ds_read_b128 v[152:155], v2 offset:1024
	ds_read_b128 v[156:159], v2 offset:2048
	ds_read_b128 v[160:163], v2 offset:3072
	v_add_u32_e32 v2, s69, v143
	ds_read_b128 v[164:167], v2
	ds_read_b128 v[168:171], v2 offset:1024
	ds_read_b128 v[172:175], v2 offset:2048
	ds_read_b128 v[176:179], v2 offset:3072
	s_add_u32 s14, s20, 0xe0000
	s_addc_u32 s15, s21, 0
	s_mov_b32 m0, s52
	v_lshl_add_u64 v[222:223], s[14:15], 0, v[132:133]
	ds_read_b128 v[180:183], v146 offset:32768
	ds_read_b128 v[184:187], v146 offset:33792
	ds_read_b128 v[188:191], v146 offset:34816
	ds_read_b128 v[192:195], v146 offset:35840
	ds_read_b128 v[196:199], v146 offset:36864
	ds_read_b128 v[200:203], v146 offset:37888
	ds_read_b128 v[204:207], v146 offset:38912
	ds_read_b128 v[208:211], v146 offset:39936
	global_load_lds_dwordx4 v[222:223], off
	v_lshl_add_u64 v[222:223], s[14:15], 0, v[0:1]
	s_mov_b32 m0, s53
	s_nop 0
	global_load_lds_dwordx4 v[222:223], off
	s_waitcnt vmcnt(8)
	s_waitcnt lgkmcnt(0)
	s_barrier
	s_setprio 1
	s_waitcnt lgkmcnt(0)
	v_mfma_f32_16x16x32_bf16 v[128:131], v[148:151], v[180:183], v[128:131]
	v_mfma_f32_16x16x32_bf16 v[124:127], v[156:159], v[180:183], v[124:127]
	v_mfma_f32_16x16x32_bf16 v[120:123], v[148:151], v[188:191], v[120:123]
	v_mfma_f32_16x16x32_bf16 v[116:119], v[156:159], v[188:191], v[116:119]
	v_mfma_f32_16x16x32_bf16 v[108:111], v[148:151], v[196:199], v[108:111]
	v_mfma_f32_16x16x32_bf16 v[100:103], v[156:159], v[196:199], v[100:103]
	v_mfma_f32_16x16x32_bf16 v[92:95], v[148:151], v[204:207], v[92:95]
	v_mfma_f32_16x16x32_bf16 v[84:87], v[156:159], v[204:207], v[84:87]
	v_mfma_f32_16x16x32_bf16 v[128:131], v[152:155], v[184:187], v[128:131]
	v_mfma_f32_16x16x32_bf16 v[124:127], v[160:163], v[184:187], v[124:127]
	v_mfma_f32_16x16x32_bf16 v[120:123], v[152:155], v[192:195], v[120:123]
	v_mfma_f32_16x16x32_bf16 v[116:119], v[160:163], v[192:195], v[116:119]
	v_mfma_f32_16x16x32_bf16 v[108:111], v[152:155], v[200:203], v[108:111]
	v_mfma_f32_16x16x32_bf16 v[100:103], v[160:163], v[200:203], v[100:103]
	v_mfma_f32_16x16x32_bf16 v[92:95], v[152:155], v[208:211], v[92:95]
	v_mfma_f32_16x16x32_bf16 v[84:87], v[160:163], v[208:211], v[84:87]
	s_setprio 0
	s_setprio 1
	v_mfma_f32_16x16x32_bf16 v[112:115], v[164:167], v[180:183], v[112:115]
	v_mfma_f32_16x16x32_bf16 v[104:107], v[172:175], v[180:183], v[104:107]
	v_mfma_f32_16x16x32_bf16 v[96:99], v[164:167], v[188:191], v[96:99]
	v_mfma_f32_16x16x32_bf16 v[88:91], v[172:175], v[188:191], v[88:91]
	v_mfma_f32_16x16x32_bf16 v[80:83], v[164:167], v[196:199], v[80:83]
	v_mfma_f32_16x16x32_bf16 v[76:79], v[172:175], v[196:199], v[76:79]
	v_mfma_f32_16x16x32_bf16 v[72:75], v[164:167], v[204:207], v[72:75]
	v_mfma_f32_16x16x32_bf16 v[68:71], v[172:175], v[204:207], v[68:71]
	v_mfma_f32_16x16x32_bf16 v[112:115], v[168:171], v[184:187], v[112:115]
	v_mfma_f32_16x16x32_bf16 v[104:107], v[176:179], v[184:187], v[104:107]
	v_mfma_f32_16x16x32_bf16 v[96:99], v[168:171], v[192:195], v[96:99]
	v_mfma_f32_16x16x32_bf16 v[88:91], v[176:179], v[192:195], v[88:91]
	v_mfma_f32_16x16x32_bf16 v[80:83], v[168:171], v[200:203], v[80:83]
	v_mfma_f32_16x16x32_bf16 v[76:79], v[176:179], v[200:203], v[76:79]
	v_mfma_f32_16x16x32_bf16 v[72:75], v[168:171], v[208:211], v[72:75]
	v_mfma_f32_16x16x32_bf16 v[68:71], v[176:179], v[208:211], v[68:71]
	s_setprio 0
	s_barrier
	s_add_i32 s14, s16, s45
	v_lshl_add_u64 v[214:215], v[214:215], 0, s[28:29]
	s_mov_b32 m0, s14
	ds_read_b128 v[180:183], v146 offset:49152
	ds_read_b128 v[184:187], v146 offset:50176
	ds_read_b128 v[188:191], v146 offset:51200
	ds_read_b128 v[192:195], v146 offset:52224
	ds_read_b128 v[196:199], v146 offset:53248
	ds_read_b128 v[200:203], v146 offset:54272
	ds_read_b128 v[204:207], v146 offset:55296
	ds_read_b128 v[208:211], v146 offset:56320
	global_load_lds_dwordx4 v[214:215], off
	v_lshl_add_u64 v[214:215], v[216:217], 0, s[28:29]
	s_add_i32 m0, s14, 0x2000
	v_lshl_add_u64 v[212:213], v[212:213], 0, s[76:77]
	s_add_i32 s14, s69, s45
	global_load_lds_dwordx4 v[214:215], off
	v_lshl_add_u64 v[214:215], v[212:213], 0, v[132:133]
	s_mov_b32 m0, s14
	v_lshl_add_u64 v[212:213], v[212:213], 0, v[0:1]
	global_load_lds_dwordx4 v[214:215], off
	s_add_i32 m0, s14, 0x2000
	s_nop 0
	global_load_lds_dwordx4 v[212:213], off
	v_lshl_add_u64 v[212:213], v[218:219], 0, s[28:29]
	s_mov_b32 m0, s60
	s_nop 0
	global_load_lds_dwordx4 v[212:213], off
	v_lshl_add_u64 v[212:213], v[220:221], 0, s[28:29]
	s_mov_b32 m0, s61
	s_nop 0
	global_load_lds_dwordx4 v[212:213], off
	s_waitcnt vmcnt(8)
	s_waitcnt lgkmcnt(0)
	s_barrier
	s_setprio 1
	s_waitcnt lgkmcnt(0)
	v_mfma_f32_16x16x32_bf16 v[64:67], v[148:151], v[180:183], v[64:67]
	v_mfma_f32_16x16x32_bf16 v[60:63], v[156:159], v[180:183], v[60:63]
	v_mfma_f32_16x16x32_bf16 v[56:59], v[148:151], v[188:191], v[56:59]
	v_mfma_f32_16x16x32_bf16 v[52:55], v[156:159], v[188:191], v[52:55]
	v_mfma_f32_16x16x32_bf16 v[40:43], v[148:151], v[196:199], v[40:43]
	v_mfma_f32_16x16x32_bf16 v[36:39], v[156:159], v[196:199], v[36:39]
	v_mfma_f32_16x16x32_bf16 v[24:27], v[148:151], v[204:207], v[24:27]
	v_mfma_f32_16x16x32_bf16 v[20:23], v[156:159], v[204:207], v[20:23]
	v_mfma_f32_16x16x32_bf16 v[64:67], v[152:155], v[184:187], v[64:67]
	v_mfma_f32_16x16x32_bf16 v[60:63], v[160:163], v[184:187], v[60:63]
	v_mfma_f32_16x16x32_bf16 v[56:59], v[152:155], v[192:195], v[56:59]
	v_mfma_f32_16x16x32_bf16 v[52:55], v[160:163], v[192:195], v[52:55]
	v_mfma_f32_16x16x32_bf16 v[40:43], v[152:155], v[200:203], v[40:43]
	v_mfma_f32_16x16x32_bf16 v[36:39], v[160:163], v[200:203], v[36:39]
	v_mfma_f32_16x16x32_bf16 v[24:27], v[152:155], v[208:211], v[24:27]
	v_mfma_f32_16x16x32_bf16 v[20:23], v[160:163], v[208:211], v[20:23]
	s_setprio 0
	s_setprio 1
	v_mfma_f32_16x16x32_bf16 v[48:51], v[164:167], v[180:183], v[48:51]
	v_mfma_f32_16x16x32_bf16 v[44:47], v[172:175], v[180:183], v[44:47]
	v_mfma_f32_16x16x32_bf16 v[32:35], v[164:167], v[188:191], v[32:35]
	v_mfma_f32_16x16x32_bf16 v[28:31], v[172:175], v[188:191], v[28:31]
	v_mfma_f32_16x16x32_bf16 v[16:19], v[164:167], v[196:199], v[16:19]
	v_mfma_f32_16x16x32_bf16 v[12:15], v[172:175], v[196:199], v[12:15]
	v_mfma_f32_16x16x32_bf16 v[8:11], v[164:167], v[204:207], v[8:11]
	v_mfma_f32_16x16x32_bf16 v[4:7], v[172:175], v[204:207], v[4:7]
	v_mfma_f32_16x16x32_bf16 v[48:51], v[168:171], v[184:187], v[48:51]
	v_mfma_f32_16x16x32_bf16 v[44:47], v[176:179], v[184:187], v[44:47]
	v_mfma_f32_16x16x32_bf16 v[32:35], v[168:171], v[192:195], v[32:35]
	v_mfma_f32_16x16x32_bf16 v[28:31], v[176:179], v[192:195], v[28:31]
	v_mfma_f32_16x16x32_bf16 v[16:19], v[168:171], v[200:203], v[16:19]
	v_mfma_f32_16x16x32_bf16 v[12:15], v[176:179], v[200:203], v[12:15]
	v_mfma_f32_16x16x32_bf16 v[8:11], v[168:171], v[208:211], v[8:11]
	v_mfma_f32_16x16x32_bf16 v[4:7], v[176:179], v[208:211], v[4:7]
	s_setprio 0
	s_barrier
	v_lshl_add_u64 v[140:141], v[140:141], 0, s[70:71]
	s_cmp_ge_u32 s17, s57
	s_mov_b64 s[14:15], s[18:19]
	s_mov_b32 s16, s17
	s_cbranch_scc1 .Lmy_gx8
	.p2alignl 6, 3212836864
